# speedup vs baseline: 1.0011x; 1.0011x over previous
_Z4k_k2ILb0EEvPKDF16_S1_PKfS3_S3_S1_S1_PfS3_S3_S1_PDF16_PKiS4_S4_:
	s_load_dwordx2 s[24:25], s[0:1], 0x58
	s_load_dwordx8 s[4:11], s[0:1], 0x38
	s_load_dwordx4 s[20:23], s[0:1], 0x0
	s_load_dwordx8 s[12:19], s[0:1], 0x18
	s_load_dwordx2 s[54:55], s[0:1], 0x10
	s_lshl_b32 s3, s2, 5
	s_and_b32 s3, s3, 0xe0
	s_lshr_b32 s26, s2, 3
	s_or_b32 s3, s3, s26
	s_movk_i32 s26, 0x100
	s_lshl_b32 s28, s3, 5
	v_cmp_gt_u32_e32 vcc, s26, v0
	v_mov_b32_e32 v67, 0
	v_lshlrev_b32_e32 v66, 4, v0
	s_lshl_b32 s0, s3, 1
	s_and_b32 s26, s0, 0xffffffe
	s_mov_b32 s27, 0
	s_waitcnt lgkmcnt(0)
	v_lshl_add_u64 v[2:3], s[16:17], 0, v[66:67]
	s_lshl_b64 s[0:1], s[26:27], 13
	s_or_b32 s26, s26, 1
	v_lshl_add_u64 v[4:5], v[2:3], 0, s[0:1]
	s_lshl_b64 s[0:1], s[26:27], 13
	v_lshl_add_u64 v[2:3], v[2:3], 0, s[0:1]
	global_load_dwordx4 v[68:71], v[4:5], off
	global_load_dwordx4 v[72:75], v[2:3], off
	v_lshl_add_u64 v[2:3], s[12:13], 0, v[66:67]
	s_movk_i32 s29, 0x2000
	v_add_co_u32_e32 v4, vcc, s29, v2
	s_movk_i32 s52, 0x4000
	s_nop 0
	v_addc_co_u32_e32 v5, vcc, 0, v3, vcc
	v_add_co_u32_e32 v18, vcc, s52, v2
	s_movk_i32 s33, 0x6000
	s_nop 0
	v_addc_co_u32_e32 v19, vcc, 0, v3, vcc
	s_lshl_b32 s26, s3, 2
	global_load_dwordx4 v[14:17], v66, s[12:13]
	global_load_dwordx4 v[10:13], v[4:5], off
	global_load_dwordx4 v[6:9], v[18:19], off
	v_add_co_u32_e32 v18, vcc, s33, v2
	s_add_u32 s0, s24, 0x800000
	s_nop 0
	v_addc_co_u32_e32 v19, vcc, 0, v3, vcc
	s_addc_u32 s1, s25, 0
	s_lshl_b64 s[12:13], s[26:27], 13
	v_lshlrev_b32_e32 v20, 2, v0
	global_load_dwordx4 v[2:5], v[18:19], off
	global_load_dword v1, v20, s[14:15]
	v_or_b32_e32 v18, s12, v66
	v_mov_b32_e32 v19, s13
	s_or_b32 s12, s26, 1
	s_mov_b32 s13, s27
	s_lshl_b64 s[12:13], s[12:13], 13
	v_lshl_add_u64 v[76:77], s[22:23], 0, v[18:19]
	v_lshl_add_u64 v[78:79], s[20:21], 0, v[18:19]
	v_lshl_add_u64 v[80:81], s[0:1], 0, v[18:19]
	v_or_b32_e32 v18, s12, v66
	v_mov_b32_e32 v19, s13
	s_or_b32 s12, s26, 2
	s_mov_b32 s13, s27
	s_lshl_b64 s[12:13], s[12:13], 13
	s_or_b32 s26, s26, 3
	v_lshl_add_u64 v[82:83], s[22:23], 0, v[18:19]
	v_lshl_add_u64 v[84:85], s[20:21], 0, v[18:19]
	v_lshl_add_u64 v[86:87], s[0:1], 0, v[18:19]
	v_or_b32_e32 v18, s12, v66
	v_mov_b32_e32 v19, s13
	s_lshl_b64 s[12:13], s[26:27], 13
	v_lshl_add_u64 v[88:89], s[22:23], 0, v[18:19]
	v_lshl_add_u64 v[90:91], s[20:21], 0, v[18:19]
	v_lshl_add_u64 v[92:93], s[0:1], 0, v[18:19]
	v_or_b32_e32 v18, s12, v66
	v_mov_b32_e32 v19, s13
	v_lshl_add_u64 v[94:95], s[22:23], 0, v[18:19]
	v_lshl_add_u64 v[96:97], s[20:21], 0, v[18:19]
	v_lshl_add_u64 v[98:99], s[0:1], 0, v[18:19]
	global_load_dwordx4 v[62:65], v[76:77], off
	global_load_dwordx4 v[54:57], v[78:79], off
	global_load_dwordx4 v[58:61], v[80:81], off
	v_mov_b64_e32 v[212:213], v[82:83]
	v_mov_b64_e32 v[214:215], v[84:85]
	v_mov_b64_e32 v[216:217], v[86:87]
	v_mov_b64_e32 v[218:219], v[88:89]
	v_mov_b64_e32 v[220:221], v[90:91]
	v_mov_b64_e32 v[222:223], v[92:93]
	v_mov_b64_e32 v[224:225], v[94:95]
	v_mov_b64_e32 v[226:227], v[96:97]
	v_mov_b64_e32 v[228:229], v[98:99]
	s_lshl_b32 s30, s28, 7
	s_add_u32 s54, s54, s30
	s_addc_u32 s55, s55, 0
	s_load_dwordx16 s[36:51], s[54:55], 0x0
	s_load_dwordx16 s[72:87], s[54:55], 0x40
	s_load_dwordx16 s[56:71], s[54:55], 0x80
	s_load_dwordx8 s[88:95], s[54:55], 0xc0
	s_load_dwordx4 s[96:99], s[54:55], 0xe0
	s_load_dwordx4 s[20:23], s[54:55], 0xf0
	v_lshrrev_b32_e32 v196, 6, v0
	s_nop 1
	v_readfirstlane_b32 s16, v196
	s_nop 3
	s_lshl_b32 s16, s16, 9
	s_add_u32 s16, s54, s16
	s_addc_u32 s17, s55, 0
	s_load_dword s30, s[16:17], 0x0
	s_load_dword s30, s[16:17], 0x40
	s_load_dword s30, s[16:17], 0x80
	s_load_dword s30, s[16:17], 0xc0
	s_load_dword s30, s[16:17], 0x100
	s_load_dword s30, s[16:17], 0x140
	s_load_dword s30, s[16:17], 0x180
	s_load_dword s30, s[16:17], 0x1c0
	s_waitcnt vmcnt(9)
	v_cvt_f32_f16_e32 v134, v68
	v_cvt_f32_f16_sdwa v135, v68 dst_sel:DWORD dst_unused:UNUSED_PAD src0_sel:WORD_1
	v_cvt_f32_f16_e32 v136, v69
	v_cvt_f32_f16_sdwa v137, v69 dst_sel:DWORD dst_unused:UNUSED_PAD src0_sel:WORD_1
	v_cvt_f32_f16_e32 v138, v70
	v_cvt_f32_f16_sdwa v139, v70 dst_sel:DWORD dst_unused:UNUSED_PAD src0_sel:WORD_1
	v_cvt_f32_f16_e32 v140, v71
	v_cvt_f32_f16_sdwa v141, v71 dst_sel:DWORD dst_unused:UNUSED_PAD src0_sel:WORD_1
	s_waitcnt vmcnt(8)
	v_cvt_f32_f16_e32 v142, v72
	v_cvt_f32_f16_sdwa v143, v72 dst_sel:DWORD dst_unused:UNUSED_PAD src0_sel:WORD_1
	v_cvt_f32_f16_e32 v144, v73
	v_cvt_f32_f16_sdwa v145, v73 dst_sel:DWORD dst_unused:UNUSED_PAD src0_sel:WORD_1
	v_cvt_f32_f16_e32 v146, v74
	v_cvt_f32_f16_sdwa v147, v74 dst_sel:DWORD dst_unused:UNUSED_PAD src0_sel:WORD_1
	v_cvt_f32_f16_e32 v148, v75
	v_cvt_f32_f16_sdwa v149, v75 dst_sel:DWORD dst_unused:UNUSED_PAD src0_sel:WORD_1
	s_waitcnt lgkmcnt(0)
	v_lshlrev_b32_e32 v68, 1, v0
	s_waitcnt vmcnt(2)
	v_cvt_f32_f16_e32 v150, v62
	s_waitcnt vmcnt(1)
	v_pk_mul_f32 v[154:155], v[150:151], v[14:15] op_sel_hi:[0,1]
	v_exp_f32_e32 v154, v154
	v_exp_f32_e32 v155, v155
	v_pk_mul_f32 v[156:157], v[150:151], v[16:17] op_sel_hi:[0,1]
	v_exp_f32_e32 v156, v156
	v_exp_f32_e32 v157, v157
	v_fma_mix_f32 v152, v150, v54, 0 op_sel_hi:[0,1,0]
	v_pk_mul_f32 v[134:135], v[154:155], v[134:135]
	v_pk_fma_f32 v[134:135], v[152:153], s[36:37], v[134:135] op_sel_hi:[0, 1, 1]
	v_pk_fma_f32 v[70:71], s[72:73], v[134:135], 0 op_sel_hi:[1, 1, 0]
	v_pk_mul_f32 v[86:87], v[156:157], v[136:137]
	s_nop 0
	v_pk_fma_f32 v[136:137], v[152:153], s[38:39], v[86:87] op_sel_hi:[0, 1, 1]
	v_pk_mul_f32 v[72:73], v[150:151], v[10:11] op_sel_hi:[0,1]
	v_exp_f32_e32 v72, v72
	v_exp_f32_e32 v73, v73
	v_pk_mul_f32 v[86:87], v[150:151], v[12:13] op_sel_hi:[0,1]
	v_exp_f32_e32 v86, v86
	v_exp_f32_e32 v87, v87
	v_pk_mul_f32 v[72:73], v[72:73], v[138:139]
	v_pk_fma_f32 v[70:71], s[74:75], v[136:137], v[70:71]
	v_pk_fma_f32 v[138:139], v[152:153], s[40:41], v[72:73] op_sel_hi:[0, 1, 1]
	v_pk_mul_f32 v[72:73], v[86:87], v[140:141]
	v_pk_mul_f32 v[74:75], v[150:151], v[8:9] op_sel_hi:[0,1]
	v_pk_fma_f32 v[140:141], v[152:153], s[42:43], v[72:73] op_sel_hi:[0, 1, 1]
	v_pk_mul_f32 v[72:73], v[150:151], v[6:7] op_sel_hi:[0,1]
	v_exp_f32_e32 v72, v72
	v_exp_f32_e32 v73, v73
	v_exp_f32_e32 v74, v74
	v_exp_f32_e32 v75, v75
	v_pk_fma_f32 v[70:71], s[76:77], v[138:139], v[70:71]
	v_pk_mul_f32 v[72:73], v[72:73], v[142:143]
	v_pk_fma_f32 v[70:71], s[78:79], v[140:141], v[70:71]
	v_pk_fma_f32 v[142:143], v[152:153], s[44:45], v[72:73] op_sel_hi:[0, 1, 1]
	v_pk_mul_f32 v[72:73], v[74:75], v[144:145]
	v_pk_mul_f32 v[74:75], v[150:151], v[4:5] op_sel_hi:[0,1]
	v_pk_fma_f32 v[144:145], v[152:153], s[46:47], v[72:73] op_sel_hi:[0, 1, 1]
	v_pk_mul_f32 v[72:73], v[150:151], v[2:3] op_sel_hi:[0,1]
	v_exp_f32_e32 v72, v72
	v_exp_f32_e32 v73, v73
	v_exp_f32_e32 v74, v74
	v_exp_f32_e32 v75, v75
	v_pk_fma_f32 v[70:71], s[80:81], v[142:143], v[70:71]
	v_pk_mul_f32 v[72:73], v[72:73], v[146:147]
	v_pk_fma_f32 v[70:71], s[82:83], v[144:145], v[70:71]
	v_pk_fma_f32 v[146:147], v[152:153], s[48:49], v[72:73] op_sel_hi:[0, 1, 1]
	v_pk_mul_f32 v[72:73], v[74:75], v[148:149]
	v_pk_fma_f32 v[70:71], s[84:85], v[146:147], v[70:71]
	v_pk_fma_f32 v[148:149], v[152:153], s[50:51], v[72:73] op_sel_hi:[0, 1, 1]
	v_pk_fma_f32 v[70:71], s[86:87], v[148:149], v[70:71]
	s_nop 0
	v_add_f32_e32 v69, v70, v71
	v_fma_mix_f32 v69, v1, v54, v69 op_sel_hi:[0,1,0]
	s_waitcnt vmcnt(0)
	v_fma_mixlo_f16 v69, v69, v58, 0 op_sel_hi:[0,1,0]
	ds_write_b16 v68, v69 offset:4096
	global_load_dwordx4 v[50:53], v[212:213], off
	global_load_dwordx4 v[42:45], v[214:215], off
	global_load_dwordx4 v[46:49], v[216:217], off
	global_load_dwordx4 v[38:41], v[218:219], off
	global_load_dwordx4 v[30:33], v[220:221], off
	global_load_dwordx4 v[34:37], v[222:223], off
	global_load_dwordx4 v[26:29], v[224:225], off
	global_load_dwordx4 v[18:21], v[226:227], off
	global_load_dwordx4 v[22:25], v[228:229], off
	s_waitcnt lgkmcnt(0)
	s_load_dwordx16 s[36:51], s[54:55], 0x100
	s_load_dwordx16 s[72:87], s[54:55], 0x140
	v_cvt_f32_f16_sdwa v62, v62 dst_sel:DWORD dst_unused:UNUSED_PAD src0_sel:WORD_1
	v_pk_mul_f32 v[152:153], v[62:63], v[14:15] op_sel_hi:[0,1]
	v_exp_f32_e32 v152, v152
	v_exp_f32_e32 v153, v153
	v_pk_mul_f32 v[154:155], v[62:63], v[16:17] op_sel_hi:[0,1]
	v_exp_f32_e32 v154, v154
	v_exp_f32_e32 v155, v155
	v_fma_mix_f32 v150, v62, v54, 0 op_sel:[0,1,0] op_sel_hi:[0,1,0]
	v_pk_mul_f32 v[134:135], v[152:153], v[134:135]
	v_pk_fma_f32 v[134:135], v[150:151], s[56:57], v[134:135] op_sel_hi:[0, 1, 1]
	v_pk_fma_f32 v[102:103], s[88:89], v[134:135], 0 op_sel_hi:[1, 1, 0]
	v_pk_mul_f32 v[118:119], v[154:155], v[136:137]
	s_nop 0
	v_pk_fma_f32 v[136:137], v[150:151], s[58:59], v[118:119] op_sel_hi:[0, 1, 1]
	v_pk_mul_f32 v[104:105], v[62:63], v[10:11] op_sel_hi:[0,1]
	v_exp_f32_e32 v104, v104
	v_exp_f32_e32 v105, v105
	v_pk_mul_f32 v[118:119], v[62:63], v[12:13] op_sel_hi:[0,1]
	v_exp_f32_e32 v118, v118
	v_exp_f32_e32 v119, v119
	v_pk_mul_f32 v[104:105], v[104:105], v[138:139]
	v_pk_fma_f32 v[102:103], s[90:91], v[136:137], v[102:103]
	v_pk_fma_f32 v[138:139], v[150:151], s[60:61], v[104:105] op_sel_hi:[0, 1, 1]
	v_pk_mul_f32 v[104:105], v[118:119], v[140:141]
	v_pk_mul_f32 v[106:107], v[62:63], v[8:9] op_sel_hi:[0,1]
	v_pk_fma_f32 v[140:141], v[150:151], s[62:63], v[104:105] op_sel_hi:[0, 1, 1]
	v_pk_mul_f32 v[104:105], v[62:63], v[6:7] op_sel_hi:[0,1]
	v_exp_f32_e32 v104, v104
	v_exp_f32_e32 v105, v105
	v_exp_f32_e32 v106, v106
	v_exp_f32_e32 v107, v107
	v_pk_fma_f32 v[102:103], s[92:93], v[138:139], v[102:103]
	v_pk_mul_f32 v[104:105], v[104:105], v[142:143]
	v_pk_fma_f32 v[102:103], s[94:95], v[140:141], v[102:103]
	v_pk_fma_f32 v[142:143], v[150:151], s[64:65], v[104:105] op_sel_hi:[0, 1, 1]
	v_pk_mul_f32 v[104:105], v[106:107], v[144:145]
	v_pk_mul_f32 v[106:107], v[62:63], v[4:5] op_sel_hi:[0,1]
	v_pk_fma_f32 v[144:145], v[150:151], s[66:67], v[104:105] op_sel_hi:[0, 1, 1]
	v_pk_mul_f32 v[104:105], v[62:63], v[2:3] op_sel_hi:[0,1]
	v_exp_f32_e32 v104, v104
	v_exp_f32_e32 v105, v105
	v_exp_f32_e32 v106, v106
	v_exp_f32_e32 v107, v107
	v_pk_fma_f32 v[102:103], s[96:97], v[142:143], v[102:103]
	v_pk_mul_f32 v[104:105], v[104:105], v[146:147]
	v_pk_fma_f32 v[102:103], s[98:99], v[144:145], v[102:103]
	v_pk_fma_f32 v[146:147], v[150:151], s[68:69], v[104:105] op_sel_hi:[0, 1, 1]
	v_pk_mul_f32 v[104:105], v[106:107], v[148:149]
	v_pk_fma_f32 v[102:103], s[20:21], v[146:147], v[102:103]
	v_pk_fma_f32 v[148:149], v[150:151], s[70:71], v[104:105] op_sel_hi:[0, 1, 1]
	v_pk_fma_f32 v[102:103], s[22:23], v[148:149], v[102:103]
	s_nop 0
	v_add_f32_e32 v62, v102, v103
	v_fma_mix_f32 v54, v1, v54, v62 op_sel:[0,1,0] op_sel_hi:[0,1,0]
	v_fma_mixlo_f16 v54, v54, v58, 0 op_sel:[0,1,0] op_sel_hi:[0,1,0]
	ds_write_b16 v68, v54 offset:5136
	s_waitcnt lgkmcnt(0)
	s_load_dwordx16 s[56:71], s[54:55], 0x180
	s_load_dwordx8 s[88:95], s[54:55], 0x1c0
	s_load_dwordx4 s[96:99], s[54:55], 0x1e0
	s_load_dwordx4 s[20:23], s[54:55], 0x1f0
	v_cvt_f32_f16_e32 v54, v63
	v_pk_mul_f32 v[150:151], v[54:55], v[14:15] op_sel_hi:[0,1]
	v_exp_f32_e32 v150, v150
	v_exp_f32_e32 v151, v151
	v_pk_mul_f32 v[152:153], v[54:55], v[16:17] op_sel_hi:[0,1]
	v_exp_f32_e32 v152, v152
	v_exp_f32_e32 v153, v153
	v_fma_mix_f32 v58, v54, v55, 0 op_sel_hi:[0,1,0]
	v_pk_mul_f32 v[134:135], v[150:151], v[134:135]
	v_pk_fma_f32 v[134:135], v[58:59], s[36:37], v[134:135] op_sel_hi:[0, 1, 1]
	v_pk_fma_f32 v[70:71], s[72:73], v[134:135], 0 op_sel_hi:[1, 1, 0]
	v_pk_mul_f32 v[86:87], v[152:153], v[136:137]
	s_nop 0
	v_pk_fma_f32 v[136:137], v[58:59], s[38:39], v[86:87] op_sel_hi:[0, 1, 1]
	v_pk_mul_f32 v[72:73], v[54:55], v[10:11] op_sel_hi:[0,1]
	v_exp_f32_e32 v72, v72
	v_exp_f32_e32 v73, v73
	v_pk_mul_f32 v[86:87], v[54:55], v[12:13] op_sel_hi:[0,1]
	v_exp_f32_e32 v86, v86
	v_exp_f32_e32 v87, v87
	v_pk_mul_f32 v[72:73], v[72:73], v[138:139]
	v_pk_fma_f32 v[70:71], s[74:75], v[136:137], v[70:71]
	v_pk_fma_f32 v[138:139], v[58:59], s[40:41], v[72:73] op_sel_hi:[0, 1, 1]
	v_pk_mul_f32 v[72:73], v[86:87], v[140:141]
	v_pk_mul_f32 v[74:75], v[54:55], v[8:9] op_sel_hi:[0,1]
	v_pk_fma_f32 v[140:141], v[58:59], s[42:43], v[72:73] op_sel_hi:[0, 1, 1]
	v_pk_mul_f32 v[72:73], v[54:55], v[6:7] op_sel_hi:[0,1]
	v_exp_f32_e32 v72, v72
	v_exp_f32_e32 v73, v73
	v_exp_f32_e32 v74, v74
	v_exp_f32_e32 v75, v75
	v_pk_fma_f32 v[70:71], s[76:77], v[138:139], v[70:71]
	v_pk_mul_f32 v[72:73], v[72:73], v[142:143]
	v_pk_fma_f32 v[70:71], s[78:79], v[140:141], v[70:71]
	v_pk_fma_f32 v[142:143], v[58:59], s[44:45], v[72:73] op_sel_hi:[0, 1, 1]
	v_pk_mul_f32 v[72:73], v[74:75], v[144:145]
	v_pk_mul_f32 v[74:75], v[54:55], v[4:5] op_sel_hi:[0,1]
	v_pk_fma_f32 v[144:145], v[58:59], s[46:47], v[72:73] op_sel_hi:[0, 1, 1]
	v_pk_mul_f32 v[72:73], v[54:55], v[2:3] op_sel_hi:[0,1]
	v_exp_f32_e32 v72, v72
	v_exp_f32_e32 v73, v73
	v_exp_f32_e32 v74, v74
	v_exp_f32_e32 v75, v75
	v_pk_fma_f32 v[70:71], s[80:81], v[142:143], v[70:71]
	v_pk_mul_f32 v[72:73], v[72:73], v[146:147]
	v_pk_fma_f32 v[70:71], s[82:83], v[144:145], v[70:71]
	v_pk_fma_f32 v[146:147], v[58:59], s[48:49], v[72:73] op_sel_hi:[0, 1, 1]
	v_pk_mul_f32 v[72:73], v[74:75], v[148:149]
	v_pk_fma_f32 v[70:71], s[84:85], v[146:147], v[70:71]
	v_pk_fma_f32 v[148:149], v[58:59], s[50:51], v[72:73] op_sel_hi:[0, 1, 1]
	v_pk_fma_f32 v[70:71], s[86:87], v[148:149], v[70:71]
	s_nop 0
	v_add_f32_e32 v54, v70, v71
	v_fma_mix_f32 v54, v1, v55, v54 op_sel_hi:[0,1,0]
	v_fma_mixlo_f16 v54, v54, v59, 0 op_sel_hi:[0,1,0]
	ds_write_b16 v68, v54 offset:6176
	s_waitcnt lgkmcnt(0)
	s_load_dwordx16 s[36:51], s[54:55], 0x200
	s_load_dwordx16 s[72:87], s[54:55], 0x240
	v_cvt_f32_f16_sdwa v54, v63 dst_sel:DWORD dst_unused:UNUSED_PAD src0_sel:WORD_1
	v_pk_mul_f32 v[62:63], v[54:55], v[14:15] op_sel_hi:[0,1]
	v_exp_f32_e32 v62, v62
	v_exp_f32_e32 v63, v63
	v_pk_mul_f32 v[150:151], v[54:55], v[16:17] op_sel_hi:[0,1]
	v_exp_f32_e32 v150, v150
	v_exp_f32_e32 v151, v151
	v_fma_mix_f32 v58, v54, v55, 0 op_sel:[0,1,0] op_sel_hi:[0,1,0]
	v_pk_mul_f32 v[62:63], v[62:63], v[134:135]
	v_pk_fma_f32 v[62:63], v[58:59], s[56:57], v[62:63] op_sel_hi:[0, 1, 1]
	v_pk_fma_f32 v[102:103], s[88:89], v[62:63], 0 op_sel_hi:[1, 1, 0]
	v_pk_mul_f32 v[118:119], v[150:151], v[136:137]
	s_nop 0
	v_pk_fma_f32 v[134:135], v[58:59], s[58:59], v[118:119] op_sel_hi:[0, 1, 1]
	v_pk_mul_f32 v[104:105], v[54:55], v[10:11] op_sel_hi:[0,1]
	v_exp_f32_e32 v104, v104
	v_exp_f32_e32 v105, v105
	v_pk_mul_f32 v[118:119], v[54:55], v[12:13] op_sel_hi:[0,1]
	v_exp_f32_e32 v118, v118
	v_exp_f32_e32 v119, v119
	v_pk_mul_f32 v[104:105], v[104:105], v[138:139]
	v_pk_fma_f32 v[102:103], s[90:91], v[134:135], v[102:103]
	v_pk_fma_f32 v[136:137], v[58:59], s[60:61], v[104:105] op_sel_hi:[0, 1, 1]
	v_pk_mul_f32 v[104:105], v[118:119], v[140:141]
	v_pk_mul_f32 v[106:107], v[54:55], v[8:9] op_sel_hi:[0,1]
	v_pk_fma_f32 v[138:139], v[58:59], s[62:63], v[104:105] op_sel_hi:[0, 1, 1]
	v_pk_mul_f32 v[104:105], v[54:55], v[6:7] op_sel_hi:[0,1]
	v_exp_f32_e32 v104, v104
	v_exp_f32_e32 v105, v105
	v_exp_f32_e32 v106, v106
	v_exp_f32_e32 v107, v107
	v_pk_fma_f32 v[102:103], s[92:93], v[136:137], v[102:103]
	v_pk_mul_f32 v[104:105], v[104:105], v[142:143]
	v_pk_fma_f32 v[102:103], s[94:95], v[138:139], v[102:103]
	v_pk_fma_f32 v[140:141], v[58:59], s[64:65], v[104:105] op_sel_hi:[0, 1, 1]
	v_pk_mul_f32 v[104:105], v[106:107], v[144:145]
	v_pk_mul_f32 v[106:107], v[54:55], v[4:5] op_sel_hi:[0,1]
	v_pk_fma_f32 v[142:143], v[58:59], s[66:67], v[104:105] op_sel_hi:[0, 1, 1]
	v_pk_mul_f32 v[104:105], v[54:55], v[2:3] op_sel_hi:[0,1]
	v_exp_f32_e32 v104, v104
	v_exp_f32_e32 v105, v105
	v_exp_f32_e32 v106, v106
	v_exp_f32_e32 v107, v107
	v_pk_fma_f32 v[102:103], s[96:97], v[140:141], v[102:103]
	v_pk_mul_f32 v[104:105], v[104:105], v[146:147]
	v_pk_fma_f32 v[102:103], s[98:99], v[142:143], v[102:103]
	v_pk_fma_f32 v[144:145], v[58:59], s[68:69], v[104:105] op_sel_hi:[0, 1, 1]
	v_pk_mul_f32 v[104:105], v[106:107], v[148:149]
	v_pk_fma_f32 v[102:103], s[20:21], v[144:145], v[102:103]
	v_pk_fma_f32 v[146:147], v[58:59], s[70:71], v[104:105] op_sel_hi:[0, 1, 1]
	v_pk_fma_f32 v[102:103], s[22:23], v[146:147], v[102:103]
	s_nop 0
	v_add_f32_e32 v54, v102, v103
	v_fma_mix_f32 v54, v1, v55, v54 op_sel:[0,1,0] op_sel_hi:[0,1,0]
	v_fma_mixlo_f16 v54, v54, v59, 0 op_sel:[0,1,0] op_sel_hi:[0,1,0]
	ds_write_b16 v68, v54 offset:7216
	s_waitcnt lgkmcnt(0)
	s_load_dwordx16 s[56:71], s[54:55], 0x280
	s_load_dwordx8 s[88:95], s[54:55], 0x2c0
	s_load_dwordx4 s[96:99], s[54:55], 0x2e0
	s_load_dwordx4 s[20:23], s[54:55], 0x2f0
	v_cvt_f32_f16_e32 v54, v64
	v_pk_mul_f32 v[148:149], v[54:55], v[14:15] op_sel_hi:[0,1]
	v_exp_f32_e32 v148, v148
	v_exp_f32_e32 v149, v149
	v_pk_mul_f32 v[150:151], v[54:55], v[16:17] op_sel_hi:[0,1]
	v_exp_f32_e32 v150, v150
	v_exp_f32_e32 v151, v151
	v_fma_mix_f32 v58, v54, v56, 0 op_sel_hi:[0,1,0]
	v_pk_mul_f32 v[62:63], v[148:149], v[62:63]
	v_pk_fma_f32 v[62:63], v[58:59], s[36:37], v[62:63] op_sel_hi:[0, 1, 1]
	v_pk_fma_f32 v[70:71], s[72:73], v[62:63], 0 op_sel_hi:[1, 1, 0]
	v_pk_mul_f32 v[86:87], v[150:151], v[134:135]
	s_nop 0
	v_pk_fma_f32 v[134:135], v[58:59], s[38:39], v[86:87] op_sel_hi:[0, 1, 1]
	v_pk_mul_f32 v[72:73], v[54:55], v[10:11] op_sel_hi:[0,1]
	v_exp_f32_e32 v72, v72
	v_exp_f32_e32 v73, v73
	v_pk_mul_f32 v[86:87], v[54:55], v[12:13] op_sel_hi:[0,1]
	v_exp_f32_e32 v86, v86
	v_exp_f32_e32 v87, v87
	v_pk_mul_f32 v[72:73], v[72:73], v[136:137]
	v_pk_fma_f32 v[70:71], s[74:75], v[134:135], v[70:71]
	v_pk_fma_f32 v[136:137], v[58:59], s[40:41], v[72:73] op_sel_hi:[0, 1, 1]
	v_pk_mul_f32 v[72:73], v[86:87], v[138:139]
	v_pk_mul_f32 v[74:75], v[54:55], v[8:9] op_sel_hi:[0,1]
	v_pk_fma_f32 v[138:139], v[58:59], s[42:43], v[72:73] op_sel_hi:[0, 1, 1]
	v_pk_mul_f32 v[72:73], v[54:55], v[6:7] op_sel_hi:[0,1]
	v_exp_f32_e32 v72, v72
	v_exp_f32_e32 v73, v73
	v_exp_f32_e32 v74, v74
	v_exp_f32_e32 v75, v75
	v_pk_fma_f32 v[70:71], s[76:77], v[136:137], v[70:71]
	v_pk_mul_f32 v[72:73], v[72:73], v[140:141]
	v_pk_fma_f32 v[70:71], s[78:79], v[138:139], v[70:71]
	v_pk_fma_f32 v[140:141], v[58:59], s[44:45], v[72:73] op_sel_hi:[0, 1, 1]
	v_pk_mul_f32 v[72:73], v[74:75], v[142:143]
	v_pk_fma_f32 v[70:71], s[80:81], v[140:141], v[70:71]
	v_pk_fma_f32 v[142:143], v[58:59], s[46:47], v[72:73] op_sel_hi:[0, 1, 1]
	v_pk_mul_f32 v[72:73], v[54:55], v[2:3] op_sel_hi:[0,1]
	v_exp_f32_e32 v72, v72
	v_exp_f32_e32 v73, v73
	v_pk_mul_f32 v[54:55], v[54:55], v[4:5] op_sel_hi:[0,1]
	v_exp_f32_e32 v54, v54
	v_exp_f32_e32 v55, v55
	v_pk_mul_f32 v[72:73], v[72:73], v[144:145]
	v_pk_fma_f32 v[70:71], s[82:83], v[142:143], v[70:71]
	v_pk_fma_f32 v[144:145], v[58:59], s[48:49], v[72:73] op_sel_hi:[0, 1, 1]
	v_pk_mul_f32 v[54:55], v[54:55], v[146:147]
	v_pk_fma_f32 v[70:71], s[84:85], v[144:145], v[70:71]
	v_pk_fma_f32 v[54:55], v[58:59], s[50:51], v[54:55] op_sel_hi:[0, 1, 1]
	v_pk_fma_f32 v[58:59], s[86:87], v[54:55], v[70:71]
	s_nop 0
	v_add_f32_e32 v58, v58, v59
	v_fma_mix_f32 v58, v1, v56, v58 op_sel_hi:[0,1,0]
	v_fma_mixlo_f16 v58, v58, v60, 0 op_sel_hi:[0,1,0]
	ds_write_b16 v68, v58 offset:8256
	s_waitcnt lgkmcnt(0)
	s_load_dwordx16 s[36:51], s[54:55], 0x300
	s_load_dwordx16 s[72:87], s[54:55], 0x340
	v_cvt_f32_f16_sdwa v58, v64 dst_sel:DWORD dst_unused:UNUSED_PAD src0_sel:WORD_1
	v_pk_mul_f32 v[146:147], v[58:59], v[14:15] op_sel_hi:[0,1]
	v_exp_f32_e32 v146, v146
	v_exp_f32_e32 v147, v147
	v_pk_mul_f32 v[148:149], v[58:59], v[16:17] op_sel_hi:[0,1]
	v_exp_f32_e32 v148, v148
	v_exp_f32_e32 v149, v149
	v_fma_mix_f32 v64, v58, v56, 0 op_sel:[0,1,0] op_sel_hi:[0,1,0]
	v_pk_mul_f32 v[62:63], v[146:147], v[62:63]
	v_pk_fma_f32 v[62:63], v[64:65], s[56:57], v[62:63] op_sel_hi:[0, 1, 1]
	v_pk_fma_f32 v[102:103], s[88:89], v[62:63], 0 op_sel_hi:[1, 1, 0]
	v_pk_mul_f32 v[118:119], v[148:149], v[134:135]
	s_nop 0
	v_pk_fma_f32 v[134:135], v[64:65], s[58:59], v[118:119] op_sel_hi:[0, 1, 1]
	v_pk_mul_f32 v[104:105], v[58:59], v[10:11] op_sel_hi:[0,1]
	v_exp_f32_e32 v104, v104
	v_exp_f32_e32 v105, v105
	v_pk_mul_f32 v[118:119], v[58:59], v[12:13] op_sel_hi:[0,1]
	v_exp_f32_e32 v118, v118
	v_exp_f32_e32 v119, v119
	v_pk_mul_f32 v[104:105], v[104:105], v[136:137]
	v_pk_fma_f32 v[102:103], s[90:91], v[134:135], v[102:103]
	v_pk_fma_f32 v[136:137], v[64:65], s[60:61], v[104:105] op_sel_hi:[0, 1, 1]
	v_pk_mul_f32 v[104:105], v[118:119], v[138:139]
	v_pk_mul_f32 v[106:107], v[58:59], v[8:9] op_sel_hi:[0,1]
	v_pk_fma_f32 v[138:139], v[64:65], s[62:63], v[104:105] op_sel_hi:[0, 1, 1]
	v_pk_mul_f32 v[104:105], v[58:59], v[6:7] op_sel_hi:[0,1]
	v_exp_f32_e32 v104, v104
	v_exp_f32_e32 v105, v105
	v_exp_f32_e32 v106, v106
	v_exp_f32_e32 v107, v107
	v_pk_fma_f32 v[102:103], s[92:93], v[136:137], v[102:103]
	v_pk_mul_f32 v[104:105], v[104:105], v[140:141]
	v_pk_fma_f32 v[102:103], s[94:95], v[138:139], v[102:103]
	v_pk_fma_f32 v[140:141], v[64:65], s[64:65], v[104:105] op_sel_hi:[0, 1, 1]
	v_pk_mul_f32 v[104:105], v[106:107], v[142:143]
	v_pk_fma_f32 v[102:103], s[96:97], v[140:141], v[102:103]
	v_pk_fma_f32 v[142:143], v[64:65], s[66:67], v[104:105] op_sel_hi:[0, 1, 1]
	v_pk_mul_f32 v[104:105], v[58:59], v[2:3] op_sel_hi:[0,1]
	v_exp_f32_e32 v104, v104
	v_exp_f32_e32 v105, v105
	v_pk_mul_f32 v[58:59], v[58:59], v[4:5] op_sel_hi:[0,1]
	v_exp_f32_e32 v58, v58
	v_exp_f32_e32 v59, v59
	v_pk_mul_f32 v[104:105], v[104:105], v[144:145]
	v_pk_fma_f32 v[102:103], s[98:99], v[142:143], v[102:103]
	v_pk_fma_f32 v[144:145], v[64:65], s[68:69], v[104:105] op_sel_hi:[0, 1, 1]
	v_pk_mul_f32 v[54:55], v[58:59], v[54:55]
	v_pk_fma_f32 v[102:103], s[20:21], v[144:145], v[102:103]
	v_pk_fma_f32 v[54:55], v[64:65], s[70:71], v[54:55] op_sel_hi:[0, 1, 1]
	v_pk_fma_f32 v[58:59], s[22:23], v[54:55], v[102:103]
	s_nop 0
	v_add_f32_e32 v58, v58, v59
	v_fma_mix_f32 v56, v1, v56, v58 op_sel:[0,1,0] op_sel_hi:[0,1,0]
	v_fma_mixlo_f16 v56, v56, v60, 0 op_sel:[0,1,0] op_sel_hi:[0,1,0]
	ds_write_b16 v68, v56 offset:9296
	s_waitcnt lgkmcnt(0)
	s_load_dwordx16 s[56:71], s[54:55], 0x380
	s_load_dwordx8 s[88:95], s[54:55], 0x3c0
	s_load_dwordx4 s[96:99], s[54:55], 0x3e0
	s_load_dwordx4 s[20:23], s[54:55], 0x3f0
	v_cvt_f32_f16_e32 v56, v65
	v_pk_mul_f32 v[146:147], v[56:57], v[14:15] op_sel_hi:[0,1]
	v_exp_f32_e32 v146, v146
	v_exp_f32_e32 v147, v147
	v_pk_mul_f32 v[148:149], v[56:57], v[16:17] op_sel_hi:[0,1]
	v_exp_f32_e32 v148, v148
	v_exp_f32_e32 v149, v149
	v_fma_mix_f32 v58, v56, v57, 0 op_sel_hi:[0,1,0]
	v_pk_mul_f32 v[62:63], v[146:147], v[62:63]
	v_pk_fma_f32 v[62:63], v[58:59], s[36:37], v[62:63] op_sel_hi:[0, 1, 1]
	v_pk_fma_f32 v[70:71], s[72:73], v[62:63], 0 op_sel_hi:[1, 1, 0]
	v_pk_mul_f32 v[86:87], v[148:149], v[134:135]
	s_nop 0
	v_pk_fma_f32 v[134:135], v[58:59], s[38:39], v[86:87] op_sel_hi:[0, 1, 1]
	v_pk_mul_f32 v[72:73], v[56:57], v[10:11] op_sel_hi:[0,1]
	v_exp_f32_e32 v72, v72
	v_exp_f32_e32 v73, v73
	v_pk_mul_f32 v[86:87], v[56:57], v[12:13] op_sel_hi:[0,1]
	v_exp_f32_e32 v86, v86
	v_exp_f32_e32 v87, v87
	v_pk_mul_f32 v[72:73], v[72:73], v[136:137]
	v_pk_fma_f32 v[70:71], s[74:75], v[134:135], v[70:71]
	v_pk_fma_f32 v[136:137], v[58:59], s[40:41], v[72:73] op_sel_hi:[0, 1, 1]
	v_pk_mul_f32 v[72:73], v[86:87], v[138:139]
	v_pk_mul_f32 v[74:75], v[56:57], v[8:9] op_sel_hi:[0,1]
	v_pk_fma_f32 v[138:139], v[58:59], s[42:43], v[72:73] op_sel_hi:[0, 1, 1]
	v_pk_mul_f32 v[72:73], v[56:57], v[6:7] op_sel_hi:[0,1]
	v_exp_f32_e32 v72, v72
	v_exp_f32_e32 v73, v73
	v_exp_f32_e32 v74, v74
	v_exp_f32_e32 v75, v75
	v_pk_fma_f32 v[70:71], s[76:77], v[136:137], v[70:71]
	v_pk_mul_f32 v[72:73], v[72:73], v[140:141]
	v_pk_fma_f32 v[70:71], s[78:79], v[138:139], v[70:71]
	v_pk_fma_f32 v[140:141], v[58:59], s[44:45], v[72:73] op_sel_hi:[0, 1, 1]
	v_pk_mul_f32 v[72:73], v[74:75], v[142:143]
	v_pk_mul_f32 v[74:75], v[56:57], v[4:5] op_sel_hi:[0,1]
	v_pk_fma_f32 v[142:143], v[58:59], s[46:47], v[72:73] op_sel_hi:[0, 1, 1]
	v_pk_mul_f32 v[72:73], v[56:57], v[2:3] op_sel_hi:[0,1]
	v_exp_f32_e32 v72, v72
	v_exp_f32_e32 v73, v73
	v_exp_f32_e32 v74, v74
	v_exp_f32_e32 v75, v75
	v_pk_fma_f32 v[70:71], s[80:81], v[140:141], v[70:71]
	v_pk_mul_f32 v[72:73], v[72:73], v[144:145]
	v_pk_fma_f32 v[70:71], s[82:83], v[142:143], v[70:71]
	v_pk_fma_f32 v[144:145], v[58:59], s[48:49], v[72:73] op_sel_hi:[0, 1, 1]
	v_pk_mul_f32 v[54:55], v[74:75], v[54:55]
	v_pk_fma_f32 v[70:71], s[84:85], v[144:145], v[70:71]
	v_pk_fma_f32 v[54:55], v[58:59], s[50:51], v[54:55] op_sel_hi:[0, 1, 1]
	v_pk_fma_f32 v[58:59], s[86:87], v[54:55], v[70:71]
	s_nop 0
	v_add_f32_e32 v56, v58, v59
	v_fma_mix_f32 v56, v1, v57, v56 op_sel_hi:[0,1,0]
	v_fma_mixlo_f16 v56, v56, v61, 0 op_sel_hi:[0,1,0]
	ds_write_b16 v68, v56 offset:10336
	s_waitcnt lgkmcnt(0)
	s_load_dwordx16 s[36:51], s[54:55], 0x400
	s_load_dwordx16 s[72:87], s[54:55], 0x440
	v_cvt_f32_f16_sdwa v56, v65 dst_sel:DWORD dst_unused:UNUSED_PAD src0_sel:WORD_1
	v_pk_mul_f32 v[64:65], v[56:57], v[14:15] op_sel_hi:[0,1]
	v_pk_mul_f32 v[146:147], v[56:57], v[16:17] op_sel_hi:[0,1]
	v_exp_f32_e32 v64, v64
	v_exp_f32_e32 v65, v65
	v_exp_f32_e32 v146, v146
	v_exp_f32_e32 v147, v147
	v_fma_mix_f32 v58, v56, v57, 0 op_sel:[0,1,0] op_sel_hi:[0,1,0]
	v_pk_mul_f32 v[62:63], v[64:65], v[62:63]
	v_pk_mul_f32 v[64:65], v[146:147], v[134:135]
	v_pk_fma_f32 v[134:135], v[58:59], s[58:59], v[64:65] op_sel_hi:[0, 1, 1]
	v_pk_mul_f32 v[64:65], v[56:57], v[10:11] op_sel_hi:[0,1]
	v_pk_fma_f32 v[148:149], v[58:59], s[56:57], v[62:63] op_sel_hi:[0, 1, 1]
	v_exp_f32_e32 v64, v64
	v_exp_f32_e32 v65, v65
	v_pk_mul_f32 v[102:103], v[56:57], v[12:13] op_sel_hi:[0,1]
	v_exp_f32_e32 v102, v102
	v_exp_f32_e32 v103, v103
	v_pk_fma_f32 v[62:63], s[88:89], v[148:149], 0 op_sel_hi:[1, 1, 0]
	v_pk_mul_f32 v[64:65], v[64:65], v[136:137]
	v_pk_fma_f32 v[62:63], s[90:91], v[134:135], v[62:63]
	v_pk_fma_f32 v[136:137], v[58:59], s[60:61], v[64:65] op_sel_hi:[0, 1, 1]
	v_pk_mul_f32 v[64:65], v[102:103], v[138:139]
	v_pk_fma_f32 v[62:63], s[92:93], v[136:137], v[62:63]
	v_pk_fma_f32 v[122:123], v[58:59], s[62:63], v[64:65] op_sel_hi:[0, 1, 1]
	v_pk_mul_f32 v[64:65], v[56:57], v[6:7] op_sel_hi:[0,1]
	v_exp_f32_e32 v64, v64
	v_exp_f32_e32 v65, v65
	v_pk_mul_f32 v[102:103], v[56:57], v[8:9] op_sel_hi:[0,1]
	v_exp_f32_e32 v102, v102
	v_exp_f32_e32 v103, v103
	v_pk_mul_f32 v[64:65], v[64:65], v[140:141]
	v_pk_fma_f32 v[62:63], s[94:95], v[122:123], v[62:63]
	v_pk_fma_f32 v[124:125], v[58:59], s[64:65], v[64:65] op_sel_hi:[0, 1, 1]
	v_pk_mul_f32 v[64:65], v[102:103], v[142:143]
	v_pk_fma_f32 v[62:63], s[96:97], v[124:125], v[62:63]
	v_pk_fma_f32 v[126:127], v[58:59], s[66:67], v[64:65] op_sel_hi:[0, 1, 1]
	v_pk_mul_f32 v[64:65], v[56:57], v[2:3] op_sel_hi:[0,1]
	v_exp_f32_e32 v64, v64
	v_exp_f32_e32 v65, v65
	v_pk_mul_f32 v[102:103], v[56:57], v[4:5] op_sel_hi:[0,1]
	v_exp_f32_e32 v102, v102
	v_exp_f32_e32 v103, v103
	v_pk_mul_f32 v[64:65], v[64:65], v[144:145]
	v_pk_fma_f32 v[62:63], s[98:99], v[126:127], v[62:63]
	v_pk_fma_f32 v[128:129], v[58:59], s[68:69], v[64:65] op_sel_hi:[0, 1, 1]
	v_pk_mul_f32 v[54:55], v[102:103], v[54:55]
	v_pk_fma_f32 v[62:63], s[20:21], v[128:129], v[62:63]
	v_pk_fma_f32 v[130:131], v[58:59], s[70:71], v[54:55] op_sel_hi:[0, 1, 1]
	v_pk_fma_f32 v[54:55], s[22:23], v[130:131], v[62:63]
	s_nop 0
	v_add_f32_e32 v54, v54, v55
	v_fma_mix_f32 v54, v1, v57, v54 op_sel:[0,1,0] op_sel_hi:[0,1,0]
	v_fma_mixlo_f16 v54, v54, v61, 0 op_sel:[0,1,0] op_sel_hi:[0,1,0]
	ds_write_b16 v68, v54 offset:11376
	s_waitcnt lgkmcnt(0)
	s_load_dwordx16 s[56:71], s[54:55], 0x480
	s_load_dwordx8 s[88:95], s[54:55], 0x4c0
	s_load_dwordx4 s[96:99], s[54:55], 0x4e0
	s_load_dwordx4 s[20:23], s[54:55], 0x4f0
	s_waitcnt vmcnt(8)
	v_cvt_f32_f16_e32 v132, v50
	s_waitcnt vmcnt(7)
	v_pk_mul_f32 v[140:141], v[132:133], v[14:15] op_sel_hi:[0,1]
	v_exp_f32_e32 v140, v140
	v_exp_f32_e32 v141, v141
	v_pk_mul_f32 v[142:143], v[132:133], v[16:17] op_sel_hi:[0,1]
	v_exp_f32_e32 v142, v142
	v_exp_f32_e32 v143, v143
	v_fma_mix_f32 v138, v132, v42, 0 op_sel_hi:[0,1,0]
	v_pk_mul_f32 v[140:141], v[140:141], v[148:149]
	v_pk_fma_f32 v[140:141], v[138:139], s[36:37], v[140:141] op_sel_hi:[0, 1, 1]
	v_pk_fma_f32 v[70:71], s[72:73], v[140:141], 0 op_sel_hi:[1, 1, 0]
	v_pk_mul_f32 v[86:87], v[142:143], v[134:135]
	s_nop 0
	v_pk_fma_f32 v[134:135], v[138:139], s[38:39], v[86:87] op_sel_hi:[0, 1, 1]
	v_pk_mul_f32 v[72:73], v[132:133], v[10:11] op_sel_hi:[0,1]
	v_exp_f32_e32 v72, v72
	v_exp_f32_e32 v73, v73
	v_pk_mul_f32 v[86:87], v[132:133], v[12:13] op_sel_hi:[0,1]
	v_exp_f32_e32 v86, v86
	v_exp_f32_e32 v87, v87
	v_pk_mul_f32 v[72:73], v[72:73], v[136:137]
	v_pk_fma_f32 v[70:71], s[74:75], v[134:135], v[70:71]
	v_pk_fma_f32 v[136:137], v[138:139], s[40:41], v[72:73] op_sel_hi:[0, 1, 1]
	v_pk_mul_f32 v[72:73], v[86:87], v[122:123]
	v_pk_mul_f32 v[74:75], v[132:133], v[8:9] op_sel_hi:[0,1]
	v_pk_fma_f32 v[122:123], v[138:139], s[42:43], v[72:73] op_sel_hi:[0, 1, 1]
	v_pk_mul_f32 v[72:73], v[132:133], v[6:7] op_sel_hi:[0,1]
	v_exp_f32_e32 v72, v72
	v_exp_f32_e32 v73, v73
	v_exp_f32_e32 v74, v74
	v_exp_f32_e32 v75, v75
	v_pk_fma_f32 v[70:71], s[76:77], v[136:137], v[70:71]
	v_pk_mul_f32 v[72:73], v[72:73], v[124:125]
	v_pk_fma_f32 v[70:71], s[78:79], v[122:123], v[70:71]
	v_pk_fma_f32 v[124:125], v[138:139], s[44:45], v[72:73] op_sel_hi:[0, 1, 1]
	v_pk_mul_f32 v[72:73], v[74:75], v[126:127]
	v_pk_mul_f32 v[74:75], v[132:133], v[4:5] op_sel_hi:[0,1]
	v_pk_fma_f32 v[126:127], v[138:139], s[46:47], v[72:73] op_sel_hi:[0, 1, 1]
	v_pk_mul_f32 v[72:73], v[132:133], v[2:3] op_sel_hi:[0,1]
	v_exp_f32_e32 v72, v72
	v_exp_f32_e32 v73, v73
	v_exp_f32_e32 v74, v74
	v_exp_f32_e32 v75, v75
	v_pk_fma_f32 v[70:71], s[80:81], v[124:125], v[70:71]
	v_pk_mul_f32 v[72:73], v[72:73], v[128:129]
	v_pk_fma_f32 v[70:71], s[82:83], v[126:127], v[70:71]
	v_pk_fma_f32 v[128:129], v[138:139], s[48:49], v[72:73] op_sel_hi:[0, 1, 1]
	v_pk_mul_f32 v[72:73], v[74:75], v[130:131]
	v_pk_fma_f32 v[70:71], s[84:85], v[128:129], v[70:71]
	v_pk_fma_f32 v[130:131], v[138:139], s[50:51], v[72:73] op_sel_hi:[0, 1, 1]
	v_pk_fma_f32 v[70:71], s[86:87], v[130:131], v[70:71]
	s_nop 0
	v_add_f32_e32 v69, v70, v71
	v_fma_mix_f32 v69, v1, v42, v69 op_sel_hi:[0,1,0]
	s_waitcnt vmcnt(6)
	v_fma_mixlo_f16 v69, v69, v46, 0 op_sel_hi:[0,1,0]
	ds_write_b16 v68, v69 offset:12416
	s_waitcnt lgkmcnt(0)
	s_load_dwordx16 s[36:51], s[54:55], 0x500
	s_load_dwordx16 s[72:87], s[54:55], 0x540
	v_cvt_f32_f16_sdwa v50, v50 dst_sel:DWORD dst_unused:UNUSED_PAD src0_sel:WORD_1
	v_pk_mul_f32 v[138:139], v[50:51], v[14:15] op_sel_hi:[0,1]
	v_exp_f32_e32 v138, v138
	v_exp_f32_e32 v139, v139
	v_pk_mul_f32 v[142:143], v[50:51], v[16:17] op_sel_hi:[0,1]
	v_exp_f32_e32 v142, v142
	v_exp_f32_e32 v143, v143
	v_fma_mix_f32 v132, v50, v42, 0 op_sel:[0,1,0] op_sel_hi:[0,1,0]
	v_pk_mul_f32 v[138:139], v[138:139], v[140:141]
	v_pk_fma_f32 v[138:139], v[132:133], s[56:57], v[138:139] op_sel_hi:[0, 1, 1]
	v_pk_fma_f32 v[54:55], s[88:89], v[138:139], 0 op_sel_hi:[1, 1, 0]
	v_pk_mul_f32 v[106:107], v[142:143], v[134:135]
	s_nop 0
	v_pk_fma_f32 v[134:135], v[132:133], s[58:59], v[106:107] op_sel_hi:[0, 1, 1]
	v_pk_mul_f32 v[56:57], v[50:51], v[10:11] op_sel_hi:[0,1]
	v_exp_f32_e32 v56, v56
	v_exp_f32_e32 v57, v57
	v_pk_mul_f32 v[106:107], v[50:51], v[12:13] op_sel_hi:[0,1]
	v_exp_f32_e32 v106, v106
	v_exp_f32_e32 v107, v107
	v_pk_mul_f32 v[56:57], v[56:57], v[136:137]
	v_pk_fma_f32 v[54:55], s[90:91], v[134:135], v[54:55]
	v_pk_fma_f32 v[136:137], v[132:133], s[60:61], v[56:57] op_sel_hi:[0, 1, 1]
	v_pk_mul_f32 v[56:57], v[106:107], v[122:123]
	v_pk_mul_f32 v[58:59], v[50:51], v[8:9] op_sel_hi:[0,1]
	v_pk_fma_f32 v[122:123], v[132:133], s[62:63], v[56:57] op_sel_hi:[0, 1, 1]
	v_pk_mul_f32 v[56:57], v[50:51], v[6:7] op_sel_hi:[0,1]
	v_exp_f32_e32 v56, v56
	v_exp_f32_e32 v57, v57
	v_exp_f32_e32 v58, v58
	v_exp_f32_e32 v59, v59
	v_pk_fma_f32 v[54:55], s[92:93], v[136:137], v[54:55]
	v_pk_mul_f32 v[56:57], v[56:57], v[124:125]
	v_pk_fma_f32 v[54:55], s[94:95], v[122:123], v[54:55]
	v_pk_fma_f32 v[124:125], v[132:133], s[64:65], v[56:57] op_sel_hi:[0, 1, 1]
	v_pk_mul_f32 v[56:57], v[58:59], v[126:127]
	v_pk_mul_f32 v[58:59], v[50:51], v[4:5] op_sel_hi:[0,1]
	v_pk_fma_f32 v[126:127], v[132:133], s[66:67], v[56:57] op_sel_hi:[0, 1, 1]
	v_pk_mul_f32 v[56:57], v[50:51], v[2:3] op_sel_hi:[0,1]
	v_exp_f32_e32 v56, v56
	v_exp_f32_e32 v57, v57
	v_exp_f32_e32 v58, v58
	v_exp_f32_e32 v59, v59
	v_pk_fma_f32 v[54:55], s[96:97], v[124:125], v[54:55]
	v_pk_mul_f32 v[56:57], v[56:57], v[128:129]
	v_pk_fma_f32 v[54:55], s[98:99], v[126:127], v[54:55]
	v_pk_fma_f32 v[128:129], v[132:133], s[68:69], v[56:57] op_sel_hi:[0, 1, 1]
	v_pk_mul_f32 v[56:57], v[58:59], v[130:131]
	v_pk_fma_f32 v[54:55], s[20:21], v[128:129], v[54:55]
	v_pk_fma_f32 v[130:131], v[132:133], s[70:71], v[56:57] op_sel_hi:[0, 1, 1]
	v_pk_fma_f32 v[54:55], s[22:23], v[130:131], v[54:55]
	s_nop 0
	v_add_f32_e32 v50, v54, v55
	v_fma_mix_f32 v42, v1, v42, v50 op_sel:[0,1,0] op_sel_hi:[0,1,0]
	v_fma_mixlo_f16 v42, v42, v46, 0 op_sel:[0,1,0] op_sel_hi:[0,1,0]
	ds_write_b16 v68, v42 offset:13456
	s_waitcnt lgkmcnt(0)
	s_load_dwordx16 s[56:71], s[54:55], 0x580
	s_load_dwordx8 s[88:95], s[54:55], 0x5c0
	s_load_dwordx4 s[96:99], s[54:55], 0x5e0
	s_load_dwordx4 s[20:23], s[54:55], 0x5f0
	v_cvt_f32_f16_e32 v42, v51
	v_pk_mul_f32 v[132:133], v[42:43], v[14:15] op_sel_hi:[0,1]
	v_exp_f32_e32 v132, v132
	v_exp_f32_e32 v133, v133
	v_pk_mul_f32 v[140:141], v[42:43], v[16:17] op_sel_hi:[0,1]
	v_exp_f32_e32 v140, v140
	v_exp_f32_e32 v141, v141
	v_fma_mix_f32 v46, v42, v43, 0 op_sel_hi:[0,1,0]
	v_pk_mul_f32 v[132:133], v[132:133], v[138:139]
	v_pk_fma_f32 v[132:133], v[46:47], s[36:37], v[132:133] op_sel_hi:[0, 1, 1]
	v_pk_fma_f32 v[70:71], s[72:73], v[132:133], 0 op_sel_hi:[1, 1, 0]
	v_pk_mul_f32 v[86:87], v[140:141], v[134:135]
	s_nop 0
	v_pk_fma_f32 v[134:135], v[46:47], s[38:39], v[86:87] op_sel_hi:[0, 1, 1]
	v_pk_mul_f32 v[72:73], v[42:43], v[10:11] op_sel_hi:[0,1]
	v_exp_f32_e32 v72, v72
	v_exp_f32_e32 v73, v73
	v_pk_mul_f32 v[86:87], v[42:43], v[12:13] op_sel_hi:[0,1]
	v_exp_f32_e32 v86, v86
	v_exp_f32_e32 v87, v87
	v_pk_mul_f32 v[72:73], v[72:73], v[136:137]
	v_pk_fma_f32 v[70:71], s[74:75], v[134:135], v[70:71]
	v_pk_fma_f32 v[136:137], v[46:47], s[40:41], v[72:73] op_sel_hi:[0, 1, 1]
	v_pk_mul_f32 v[72:73], v[86:87], v[122:123]
	v_pk_mul_f32 v[74:75], v[42:43], v[8:9] op_sel_hi:[0,1]
	v_pk_fma_f32 v[122:123], v[46:47], s[42:43], v[72:73] op_sel_hi:[0, 1, 1]
	v_pk_mul_f32 v[72:73], v[42:43], v[6:7] op_sel_hi:[0,1]
	v_exp_f32_e32 v72, v72
	v_exp_f32_e32 v73, v73
	v_exp_f32_e32 v74, v74
	v_exp_f32_e32 v75, v75
	v_pk_fma_f32 v[70:71], s[76:77], v[136:137], v[70:71]
	v_pk_mul_f32 v[72:73], v[72:73], v[124:125]
	v_pk_fma_f32 v[70:71], s[78:79], v[122:123], v[70:71]
	v_pk_fma_f32 v[124:125], v[46:47], s[44:45], v[72:73] op_sel_hi:[0, 1, 1]
	v_pk_mul_f32 v[72:73], v[74:75], v[126:127]
	v_pk_mul_f32 v[74:75], v[42:43], v[4:5] op_sel_hi:[0,1]
	v_pk_fma_f32 v[126:127], v[46:47], s[46:47], v[72:73] op_sel_hi:[0, 1, 1]
	v_pk_mul_f32 v[72:73], v[42:43], v[2:3] op_sel_hi:[0,1]
	v_exp_f32_e32 v72, v72
	v_exp_f32_e32 v73, v73
	v_exp_f32_e32 v74, v74
	v_exp_f32_e32 v75, v75
	v_pk_fma_f32 v[70:71], s[80:81], v[124:125], v[70:71]
	v_pk_mul_f32 v[72:73], v[72:73], v[128:129]
	v_pk_fma_f32 v[70:71], s[82:83], v[126:127], v[70:71]
	v_pk_fma_f32 v[128:129], v[46:47], s[48:49], v[72:73] op_sel_hi:[0, 1, 1]
	v_pk_mul_f32 v[72:73], v[74:75], v[130:131]
	v_pk_fma_f32 v[70:71], s[84:85], v[128:129], v[70:71]
	v_pk_fma_f32 v[130:131], v[46:47], s[50:51], v[72:73] op_sel_hi:[0, 1, 1]
	v_pk_fma_f32 v[70:71], s[86:87], v[130:131], v[70:71]
	s_nop 0
	v_add_f32_e32 v42, v70, v71
	v_fma_mix_f32 v42, v1, v43, v42 op_sel_hi:[0,1,0]
	v_fma_mixlo_f16 v42, v42, v47, 0 op_sel_hi:[0,1,0]
	ds_write_b16 v68, v42 offset:14496
	s_waitcnt lgkmcnt(0)
	s_load_dwordx16 s[36:51], s[54:55], 0x600
	s_load_dwordx16 s[72:87], s[54:55], 0x640
	v_cvt_f32_f16_sdwa v42, v51 dst_sel:DWORD dst_unused:UNUSED_PAD src0_sel:WORD_1
	v_pk_mul_f32 v[50:51], v[42:43], v[14:15] op_sel_hi:[0,1]
	v_exp_f32_e32 v50, v50
	v_exp_f32_e32 v51, v51
	v_pk_mul_f32 v[138:139], v[42:43], v[16:17] op_sel_hi:[0,1]
	v_exp_f32_e32 v138, v138
	v_exp_f32_e32 v139, v139
	v_fma_mix_f32 v46, v42, v43, 0 op_sel:[0,1,0] op_sel_hi:[0,1,0]
	v_pk_mul_f32 v[50:51], v[50:51], v[132:133]
	v_pk_fma_f32 v[50:51], v[46:47], s[56:57], v[50:51] op_sel_hi:[0, 1, 1]
	v_pk_fma_f32 v[54:55], s[88:89], v[50:51], 0 op_sel_hi:[1, 1, 0]
	v_pk_mul_f32 v[106:107], v[138:139], v[134:135]
	s_nop 0
	v_pk_fma_f32 v[132:133], v[46:47], s[58:59], v[106:107] op_sel_hi:[0, 1, 1]
	v_pk_mul_f32 v[56:57], v[42:43], v[10:11] op_sel_hi:[0,1]
	v_exp_f32_e32 v56, v56
	v_exp_f32_e32 v57, v57
	v_pk_mul_f32 v[106:107], v[42:43], v[12:13] op_sel_hi:[0,1]
	v_exp_f32_e32 v106, v106
	v_exp_f32_e32 v107, v107
	v_pk_mul_f32 v[56:57], v[56:57], v[136:137]
	v_pk_fma_f32 v[54:55], s[90:91], v[132:133], v[54:55]
	v_pk_fma_f32 v[134:135], v[46:47], s[60:61], v[56:57] op_sel_hi:[0, 1, 1]
	v_pk_mul_f32 v[56:57], v[106:107], v[122:123]
	v_pk_mul_f32 v[58:59], v[42:43], v[8:9] op_sel_hi:[0,1]
	v_pk_fma_f32 v[122:123], v[46:47], s[62:63], v[56:57] op_sel_hi:[0, 1, 1]
	v_pk_mul_f32 v[56:57], v[42:43], v[6:7] op_sel_hi:[0,1]
	v_exp_f32_e32 v56, v56
	v_exp_f32_e32 v57, v57
	v_exp_f32_e32 v58, v58
	v_exp_f32_e32 v59, v59
	v_pk_fma_f32 v[54:55], s[92:93], v[134:135], v[54:55]
	v_pk_mul_f32 v[56:57], v[56:57], v[124:125]
	v_pk_fma_f32 v[54:55], s[94:95], v[122:123], v[54:55]
	v_pk_fma_f32 v[124:125], v[46:47], s[64:65], v[56:57] op_sel_hi:[0, 1, 1]
	v_pk_mul_f32 v[56:57], v[58:59], v[126:127]
	v_pk_mul_f32 v[58:59], v[42:43], v[4:5] op_sel_hi:[0,1]
	v_pk_fma_f32 v[126:127], v[46:47], s[66:67], v[56:57] op_sel_hi:[0, 1, 1]
	v_pk_mul_f32 v[56:57], v[42:43], v[2:3] op_sel_hi:[0,1]
	v_exp_f32_e32 v56, v56
	v_exp_f32_e32 v57, v57
	v_exp_f32_e32 v58, v58
	v_exp_f32_e32 v59, v59
	v_pk_fma_f32 v[54:55], s[96:97], v[124:125], v[54:55]
	v_pk_mul_f32 v[56:57], v[56:57], v[128:129]
	v_pk_fma_f32 v[54:55], s[98:99], v[126:127], v[54:55]
	v_pk_fma_f32 v[128:129], v[46:47], s[68:69], v[56:57] op_sel_hi:[0, 1, 1]
	v_pk_mul_f32 v[56:57], v[58:59], v[130:131]
	v_pk_fma_f32 v[54:55], s[20:21], v[128:129], v[54:55]
	v_pk_fma_f32 v[130:131], v[46:47], s[70:71], v[56:57] op_sel_hi:[0, 1, 1]
	v_pk_fma_f32 v[54:55], s[22:23], v[130:131], v[54:55]
	s_nop 0
	v_add_f32_e32 v42, v54, v55
	v_fma_mix_f32 v42, v1, v43, v42 op_sel:[0,1,0] op_sel_hi:[0,1,0]
	v_fma_mixlo_f16 v42, v42, v47, 0 op_sel:[0,1,0] op_sel_hi:[0,1,0]
	ds_write_b16 v68, v42 offset:15536
	s_waitcnt lgkmcnt(0)
	s_load_dwordx16 s[56:71], s[54:55], 0x680
	s_load_dwordx8 s[88:95], s[54:55], 0x6c0
	s_load_dwordx4 s[96:99], s[54:55], 0x6e0
	s_load_dwordx4 s[20:23], s[54:55], 0x6f0
	v_cvt_f32_f16_e32 v42, v52
	v_pk_mul_f32 v[136:137], v[42:43], v[14:15] op_sel_hi:[0,1]
	v_exp_f32_e32 v136, v136
	v_exp_f32_e32 v137, v137
	v_pk_mul_f32 v[138:139], v[42:43], v[16:17] op_sel_hi:[0,1]
	v_exp_f32_e32 v138, v138
	v_exp_f32_e32 v139, v139
	v_fma_mix_f32 v46, v42, v44, 0 op_sel_hi:[0,1,0]
	v_pk_mul_f32 v[50:51], v[136:137], v[50:51]
	v_pk_fma_f32 v[50:51], v[46:47], s[36:37], v[50:51] op_sel_hi:[0, 1, 1]
	v_pk_fma_f32 v[70:71], s[72:73], v[50:51], 0 op_sel_hi:[1, 1, 0]
	v_pk_mul_f32 v[86:87], v[138:139], v[132:133]
	s_nop 0
	v_pk_fma_f32 v[132:133], v[46:47], s[38:39], v[86:87] op_sel_hi:[0, 1, 1]
	v_pk_mul_f32 v[72:73], v[42:43], v[10:11] op_sel_hi:[0,1]
	v_exp_f32_e32 v72, v72
	v_exp_f32_e32 v73, v73
	v_pk_mul_f32 v[86:87], v[42:43], v[12:13] op_sel_hi:[0,1]
	v_exp_f32_e32 v86, v86
	v_exp_f32_e32 v87, v87
	v_pk_mul_f32 v[72:73], v[72:73], v[134:135]
	v_pk_fma_f32 v[70:71], s[74:75], v[132:133], v[70:71]
	v_pk_fma_f32 v[134:135], v[46:47], s[40:41], v[72:73] op_sel_hi:[0, 1, 1]
	v_pk_mul_f32 v[72:73], v[86:87], v[122:123]
	v_pk_mul_f32 v[74:75], v[42:43], v[8:9] op_sel_hi:[0,1]
	v_pk_fma_f32 v[122:123], v[46:47], s[42:43], v[72:73] op_sel_hi:[0, 1, 1]
	v_pk_mul_f32 v[72:73], v[42:43], v[6:7] op_sel_hi:[0,1]
	v_exp_f32_e32 v72, v72
	v_exp_f32_e32 v73, v73
	v_exp_f32_e32 v74, v74
	v_exp_f32_e32 v75, v75
	v_pk_fma_f32 v[70:71], s[76:77], v[134:135], v[70:71]
	v_pk_mul_f32 v[72:73], v[72:73], v[124:125]
	v_pk_fma_f32 v[70:71], s[78:79], v[122:123], v[70:71]
	v_pk_fma_f32 v[124:125], v[46:47], s[44:45], v[72:73] op_sel_hi:[0, 1, 1]
	v_pk_mul_f32 v[72:73], v[74:75], v[126:127]
	v_pk_fma_f32 v[70:71], s[80:81], v[124:125], v[70:71]
	v_pk_fma_f32 v[126:127], v[46:47], s[46:47], v[72:73] op_sel_hi:[0, 1, 1]
	v_pk_mul_f32 v[72:73], v[42:43], v[2:3] op_sel_hi:[0,1]
	v_exp_f32_e32 v72, v72
	v_exp_f32_e32 v73, v73
	v_pk_mul_f32 v[42:43], v[42:43], v[4:5] op_sel_hi:[0,1]
	v_exp_f32_e32 v42, v42
	v_exp_f32_e32 v43, v43
	v_pk_mul_f32 v[72:73], v[72:73], v[128:129]
	v_pk_fma_f32 v[70:71], s[82:83], v[126:127], v[70:71]
	v_pk_fma_f32 v[128:129], v[46:47], s[48:49], v[72:73] op_sel_hi:[0, 1, 1]
	v_pk_mul_f32 v[42:43], v[42:43], v[130:131]
	v_pk_fma_f32 v[70:71], s[84:85], v[128:129], v[70:71]
	v_pk_fma_f32 v[42:43], v[46:47], s[50:51], v[42:43] op_sel_hi:[0, 1, 1]
	v_pk_fma_f32 v[46:47], s[86:87], v[42:43], v[70:71]
	s_nop 0
	v_add_f32_e32 v46, v46, v47
	v_fma_mix_f32 v46, v1, v44, v46 op_sel_hi:[0,1,0]
	v_fma_mixlo_f16 v46, v46, v48, 0 op_sel_hi:[0,1,0]
	ds_write_b16 v68, v46 offset:16576
	s_waitcnt lgkmcnt(0)
	s_load_dwordx16 s[36:51], s[54:55], 0x700
	s_load_dwordx16 s[72:87], s[54:55], 0x740
	v_cvt_f32_f16_sdwa v46, v52 dst_sel:DWORD dst_unused:UNUSED_PAD src0_sel:WORD_1
	v_pk_mul_f32 v[130:131], v[46:47], v[14:15] op_sel_hi:[0,1]
	v_exp_f32_e32 v130, v130
	v_exp_f32_e32 v131, v131
	v_pk_mul_f32 v[136:137], v[46:47], v[16:17] op_sel_hi:[0,1]
	v_exp_f32_e32 v136, v136
	v_exp_f32_e32 v137, v137
	v_fma_mix_f32 v52, v46, v44, 0 op_sel:[0,1,0] op_sel_hi:[0,1,0]
	v_pk_mul_f32 v[50:51], v[130:131], v[50:51]
	v_pk_fma_f32 v[50:51], v[52:53], s[56:57], v[50:51] op_sel_hi:[0, 1, 1]
	v_pk_fma_f32 v[54:55], s[88:89], v[50:51], 0 op_sel_hi:[1, 1, 0]
	v_pk_mul_f32 v[106:107], v[136:137], v[132:133]
	s_nop 0
	v_pk_fma_f32 v[130:131], v[52:53], s[58:59], v[106:107] op_sel_hi:[0, 1, 1]
	v_pk_mul_f32 v[56:57], v[46:47], v[10:11] op_sel_hi:[0,1]
	v_exp_f32_e32 v56, v56
	v_exp_f32_e32 v57, v57
	v_pk_mul_f32 v[106:107], v[46:47], v[12:13] op_sel_hi:[0,1]
	v_exp_f32_e32 v106, v106
	v_exp_f32_e32 v107, v107
	v_pk_mul_f32 v[56:57], v[56:57], v[134:135]
	v_pk_fma_f32 v[54:55], s[90:91], v[130:131], v[54:55]
	v_pk_fma_f32 v[132:133], v[52:53], s[60:61], v[56:57] op_sel_hi:[0, 1, 1]
	v_pk_mul_f32 v[56:57], v[106:107], v[122:123]
	v_pk_mul_f32 v[58:59], v[46:47], v[8:9] op_sel_hi:[0,1]
	v_pk_fma_f32 v[122:123], v[52:53], s[62:63], v[56:57] op_sel_hi:[0, 1, 1]
	v_pk_mul_f32 v[56:57], v[46:47], v[6:7] op_sel_hi:[0,1]
	v_exp_f32_e32 v56, v56
	v_exp_f32_e32 v57, v57
	v_exp_f32_e32 v58, v58
	v_exp_f32_e32 v59, v59
	v_pk_fma_f32 v[54:55], s[92:93], v[132:133], v[54:55]
	v_pk_mul_f32 v[56:57], v[56:57], v[124:125]
	v_pk_fma_f32 v[54:55], s[94:95], v[122:123], v[54:55]
	v_pk_fma_f32 v[124:125], v[52:53], s[64:65], v[56:57] op_sel_hi:[0, 1, 1]
	v_pk_mul_f32 v[56:57], v[58:59], v[126:127]
	v_pk_fma_f32 v[54:55], s[96:97], v[124:125], v[54:55]
	v_pk_fma_f32 v[126:127], v[52:53], s[66:67], v[56:57] op_sel_hi:[0, 1, 1]
	v_pk_mul_f32 v[56:57], v[46:47], v[2:3] op_sel_hi:[0,1]
	v_exp_f32_e32 v56, v56
	v_exp_f32_e32 v57, v57
	v_pk_mul_f32 v[46:47], v[46:47], v[4:5] op_sel_hi:[0,1]
	v_exp_f32_e32 v46, v46
	v_exp_f32_e32 v47, v47
	v_pk_mul_f32 v[56:57], v[56:57], v[128:129]
	v_pk_fma_f32 v[54:55], s[98:99], v[126:127], v[54:55]
	v_pk_fma_f32 v[128:129], v[52:53], s[68:69], v[56:57] op_sel_hi:[0, 1, 1]
	v_pk_mul_f32 v[42:43], v[46:47], v[42:43]
	v_pk_fma_f32 v[54:55], s[20:21], v[128:129], v[54:55]
	v_pk_fma_f32 v[42:43], v[52:53], s[70:71], v[42:43] op_sel_hi:[0, 1, 1]
	v_pk_fma_f32 v[46:47], s[22:23], v[42:43], v[54:55]
	s_nop 0
	v_add_f32_e32 v46, v46, v47
	v_fma_mix_f32 v44, v1, v44, v46 op_sel:[0,1,0] op_sel_hi:[0,1,0]
	v_fma_mixlo_f16 v44, v44, v48, 0 op_sel:[0,1,0] op_sel_hi:[0,1,0]
	ds_write_b16 v68, v44 offset:17616
	s_waitcnt lgkmcnt(0)
	s_load_dwordx16 s[56:71], s[54:55], 0x780
	s_load_dwordx8 s[88:95], s[54:55], 0x7c0
	s_load_dwordx4 s[96:99], s[54:55], 0x7e0
	s_load_dwordx4 s[20:23], s[54:55], 0x7f0
	v_cvt_f32_f16_e32 v44, v53
	v_pk_mul_f32 v[134:135], v[44:45], v[14:15] op_sel_hi:[0,1]
	v_exp_f32_e32 v134, v134
	v_exp_f32_e32 v135, v135
	v_pk_mul_f32 v[136:137], v[44:45], v[16:17] op_sel_hi:[0,1]
	v_exp_f32_e32 v136, v136
	v_exp_f32_e32 v137, v137
	v_fma_mix_f32 v46, v44, v45, 0 op_sel_hi:[0,1,0]
	v_pk_mul_f32 v[50:51], v[134:135], v[50:51]
	v_pk_fma_f32 v[50:51], v[46:47], s[36:37], v[50:51] op_sel_hi:[0, 1, 1]
	v_pk_fma_f32 v[70:71], s[72:73], v[50:51], 0 op_sel_hi:[1, 1, 0]
	v_pk_mul_f32 v[86:87], v[136:137], v[130:131]
	s_nop 0
	v_pk_fma_f32 v[130:131], v[46:47], s[38:39], v[86:87] op_sel_hi:[0, 1, 1]
	v_pk_mul_f32 v[72:73], v[44:45], v[10:11] op_sel_hi:[0,1]
	v_exp_f32_e32 v72, v72
	v_exp_f32_e32 v73, v73
	v_pk_mul_f32 v[86:87], v[44:45], v[12:13] op_sel_hi:[0,1]
	v_exp_f32_e32 v86, v86
	v_exp_f32_e32 v87, v87
	v_pk_mul_f32 v[72:73], v[72:73], v[132:133]
	v_pk_fma_f32 v[70:71], s[74:75], v[130:131], v[70:71]
	v_pk_fma_f32 v[132:133], v[46:47], s[40:41], v[72:73] op_sel_hi:[0, 1, 1]
	v_pk_mul_f32 v[72:73], v[86:87], v[122:123]
	v_pk_mul_f32 v[74:75], v[44:45], v[8:9] op_sel_hi:[0,1]
	v_pk_fma_f32 v[122:123], v[46:47], s[42:43], v[72:73] op_sel_hi:[0, 1, 1]
	v_pk_mul_f32 v[72:73], v[44:45], v[6:7] op_sel_hi:[0,1]
	v_exp_f32_e32 v72, v72
	v_exp_f32_e32 v73, v73
	v_exp_f32_e32 v74, v74
	v_exp_f32_e32 v75, v75
	v_pk_fma_f32 v[70:71], s[76:77], v[132:133], v[70:71]
	v_pk_mul_f32 v[72:73], v[72:73], v[124:125]
	v_pk_fma_f32 v[70:71], s[78:79], v[122:123], v[70:71]
	v_pk_fma_f32 v[124:125], v[46:47], s[44:45], v[72:73] op_sel_hi:[0, 1, 1]
	v_pk_mul_f32 v[72:73], v[74:75], v[126:127]
	v_pk_mul_f32 v[74:75], v[44:45], v[4:5] op_sel_hi:[0,1]
	v_pk_fma_f32 v[126:127], v[46:47], s[46:47], v[72:73] op_sel_hi:[0, 1, 1]
	v_pk_mul_f32 v[72:73], v[44:45], v[2:3] op_sel_hi:[0,1]
	v_exp_f32_e32 v72, v72
	v_exp_f32_e32 v73, v73
	v_exp_f32_e32 v74, v74
	v_exp_f32_e32 v75, v75
	v_pk_fma_f32 v[70:71], s[80:81], v[124:125], v[70:71]
	v_pk_mul_f32 v[72:73], v[72:73], v[128:129]
	v_pk_fma_f32 v[70:71], s[82:83], v[126:127], v[70:71]
	v_pk_fma_f32 v[128:129], v[46:47], s[48:49], v[72:73] op_sel_hi:[0, 1, 1]
	v_pk_mul_f32 v[42:43], v[74:75], v[42:43]
	v_pk_fma_f32 v[70:71], s[84:85], v[128:129], v[70:71]
	v_pk_fma_f32 v[42:43], v[46:47], s[50:51], v[42:43] op_sel_hi:[0, 1, 1]
	v_pk_fma_f32 v[46:47], s[86:87], v[42:43], v[70:71]
	s_nop 0
	v_add_f32_e32 v44, v46, v47
	v_fma_mix_f32 v44, v1, v45, v44 op_sel_hi:[0,1,0]
	v_fma_mixlo_f16 v44, v44, v49, 0 op_sel_hi:[0,1,0]
	ds_write_b16 v68, v44 offset:18656
	s_waitcnt lgkmcnt(0)
	s_load_dwordx16 s[36:51], s[54:55], 0x800
	s_load_dwordx16 s[72:87], s[54:55], 0x840
	v_cvt_f32_f16_sdwa v44, v53 dst_sel:DWORD dst_unused:UNUSED_PAD src0_sel:WORD_1
	v_pk_mul_f32 v[52:53], v[44:45], v[14:15] op_sel_hi:[0,1]
	v_pk_mul_f32 v[134:135], v[44:45], v[16:17] op_sel_hi:[0,1]
	v_exp_f32_e32 v52, v52
	v_exp_f32_e32 v53, v53
	v_exp_f32_e32 v134, v134
	v_exp_f32_e32 v135, v135
	v_fma_mix_f32 v46, v44, v45, 0 op_sel:[0,1,0] op_sel_hi:[0,1,0]
	v_pk_mul_f32 v[50:51], v[52:53], v[50:51]
	v_pk_mul_f32 v[52:53], v[134:135], v[130:131]
	v_pk_fma_f32 v[130:131], v[46:47], s[58:59], v[52:53] op_sel_hi:[0, 1, 1]
	v_pk_mul_f32 v[52:53], v[44:45], v[10:11] op_sel_hi:[0,1]
	v_pk_fma_f32 v[136:137], v[46:47], s[56:57], v[50:51] op_sel_hi:[0, 1, 1]
	v_exp_f32_e32 v52, v52
	v_exp_f32_e32 v53, v53
	v_pk_mul_f32 v[54:55], v[44:45], v[12:13] op_sel_hi:[0,1]
	v_exp_f32_e32 v54, v54
	v_exp_f32_e32 v55, v55
	v_pk_fma_f32 v[50:51], s[88:89], v[136:137], 0 op_sel_hi:[1, 1, 0]
	v_pk_mul_f32 v[52:53], v[52:53], v[132:133]
	v_pk_fma_f32 v[50:51], s[90:91], v[130:131], v[50:51]
	v_pk_fma_f32 v[132:133], v[46:47], s[60:61], v[52:53] op_sel_hi:[0, 1, 1]
	v_pk_mul_f32 v[52:53], v[54:55], v[122:123]
	v_pk_fma_f32 v[50:51], s[92:93], v[132:133], v[50:51]
	v_pk_fma_f32 v[110:111], v[46:47], s[62:63], v[52:53] op_sel_hi:[0, 1, 1]
	v_pk_mul_f32 v[52:53], v[44:45], v[6:7] op_sel_hi:[0,1]
	v_exp_f32_e32 v52, v52
	v_exp_f32_e32 v53, v53
	v_pk_mul_f32 v[54:55], v[44:45], v[8:9] op_sel_hi:[0,1]
	v_exp_f32_e32 v54, v54
	v_exp_f32_e32 v55, v55
	v_pk_mul_f32 v[52:53], v[52:53], v[124:125]
	v_pk_fma_f32 v[50:51], s[94:95], v[110:111], v[50:51]
	v_pk_fma_f32 v[112:113], v[46:47], s[64:65], v[52:53] op_sel_hi:[0, 1, 1]
	v_pk_mul_f32 v[52:53], v[54:55], v[126:127]
	v_pk_fma_f32 v[50:51], s[96:97], v[112:113], v[50:51]
	v_pk_fma_f32 v[114:115], v[46:47], s[66:67], v[52:53] op_sel_hi:[0, 1, 1]
	v_pk_mul_f32 v[52:53], v[44:45], v[2:3] op_sel_hi:[0,1]
	v_exp_f32_e32 v52, v52
	v_exp_f32_e32 v53, v53
	v_pk_mul_f32 v[54:55], v[44:45], v[4:5] op_sel_hi:[0,1]
	v_exp_f32_e32 v54, v54
	v_exp_f32_e32 v55, v55
	v_pk_mul_f32 v[52:53], v[52:53], v[128:129]
	v_pk_fma_f32 v[50:51], s[98:99], v[114:115], v[50:51]
	v_pk_fma_f32 v[116:117], v[46:47], s[68:69], v[52:53] op_sel_hi:[0, 1, 1]
	v_pk_mul_f32 v[42:43], v[54:55], v[42:43]
	v_pk_fma_f32 v[50:51], s[20:21], v[116:117], v[50:51]
	v_pk_fma_f32 v[118:119], v[46:47], s[70:71], v[42:43] op_sel_hi:[0, 1, 1]
	v_pk_fma_f32 v[42:43], s[22:23], v[118:119], v[50:51]
	s_nop 0
	v_add_f32_e32 v42, v42, v43
	v_fma_mix_f32 v42, v1, v45, v42 op_sel:[0,1,0] op_sel_hi:[0,1,0]
	v_fma_mixlo_f16 v42, v42, v49, 0 op_sel:[0,1,0] op_sel_hi:[0,1,0]
	ds_write_b16 v68, v42 offset:19696
	s_waitcnt lgkmcnt(0)
	s_load_dwordx16 s[56:71], s[54:55], 0x880
	s_load_dwordx8 s[88:95], s[54:55], 0x8c0
	s_load_dwordx4 s[96:99], s[54:55], 0x8e0
	s_load_dwordx4 s[20:23], s[54:55], 0x8f0
	s_waitcnt vmcnt(5)
	v_cvt_f32_f16_e32 v120, v38
	s_waitcnt vmcnt(4)
	v_pk_mul_f32 v[124:125], v[120:121], v[14:15] op_sel_hi:[0,1]
	v_exp_f32_e32 v124, v124
	v_exp_f32_e32 v125, v125
	v_pk_mul_f32 v[126:127], v[120:121], v[16:17] op_sel_hi:[0,1]
	v_exp_f32_e32 v126, v126
	v_exp_f32_e32 v127, v127
	v_fma_mix_f32 v122, v120, v30, 0 op_sel_hi:[0,1,0]
	v_pk_mul_f32 v[124:125], v[124:125], v[136:137]
	v_pk_fma_f32 v[124:125], v[122:123], s[36:37], v[124:125] op_sel_hi:[0, 1, 1]
	v_pk_fma_f32 v[70:71], s[72:73], v[124:125], 0 op_sel_hi:[1, 1, 0]
	v_pk_mul_f32 v[86:87], v[126:127], v[130:131]
	s_nop 0
	v_pk_fma_f32 v[126:127], v[122:123], s[38:39], v[86:87] op_sel_hi:[0, 1, 1]
	v_pk_mul_f32 v[72:73], v[120:121], v[10:11] op_sel_hi:[0,1]
	v_exp_f32_e32 v72, v72
	v_exp_f32_e32 v73, v73
	v_pk_mul_f32 v[86:87], v[120:121], v[12:13] op_sel_hi:[0,1]
	v_exp_f32_e32 v86, v86
	v_exp_f32_e32 v87, v87
	v_pk_mul_f32 v[72:73], v[72:73], v[132:133]
	v_pk_fma_f32 v[70:71], s[74:75], v[126:127], v[70:71]
	v_pk_fma_f32 v[128:129], v[122:123], s[40:41], v[72:73] op_sel_hi:[0, 1, 1]
	v_pk_mul_f32 v[72:73], v[86:87], v[110:111]
	v_pk_mul_f32 v[74:75], v[120:121], v[8:9] op_sel_hi:[0,1]
	v_pk_fma_f32 v[110:111], v[122:123], s[42:43], v[72:73] op_sel_hi:[0, 1, 1]
	v_pk_mul_f32 v[72:73], v[120:121], v[6:7] op_sel_hi:[0,1]
	v_exp_f32_e32 v72, v72
	v_exp_f32_e32 v73, v73
	v_exp_f32_e32 v74, v74
	v_exp_f32_e32 v75, v75
	v_pk_fma_f32 v[70:71], s[76:77], v[128:129], v[70:71]
	v_pk_mul_f32 v[72:73], v[72:73], v[112:113]
	v_pk_fma_f32 v[70:71], s[78:79], v[110:111], v[70:71]
	v_pk_fma_f32 v[112:113], v[122:123], s[44:45], v[72:73] op_sel_hi:[0, 1, 1]
	v_pk_mul_f32 v[72:73], v[74:75], v[114:115]
	v_pk_mul_f32 v[74:75], v[120:121], v[4:5] op_sel_hi:[0,1]
	v_pk_fma_f32 v[114:115], v[122:123], s[46:47], v[72:73] op_sel_hi:[0, 1, 1]
	v_pk_mul_f32 v[72:73], v[120:121], v[2:3] op_sel_hi:[0,1]
	v_exp_f32_e32 v72, v72
	v_exp_f32_e32 v73, v73
	v_exp_f32_e32 v74, v74
	v_exp_f32_e32 v75, v75
	v_pk_fma_f32 v[70:71], s[80:81], v[112:113], v[70:71]
	v_pk_mul_f32 v[72:73], v[72:73], v[116:117]
	v_pk_fma_f32 v[70:71], s[82:83], v[114:115], v[70:71]
	v_pk_fma_f32 v[116:117], v[122:123], s[48:49], v[72:73] op_sel_hi:[0, 1, 1]
	v_pk_mul_f32 v[72:73], v[74:75], v[118:119]
	v_pk_fma_f32 v[70:71], s[84:85], v[116:117], v[70:71]
	v_pk_fma_f32 v[118:119], v[122:123], s[50:51], v[72:73] op_sel_hi:[0, 1, 1]
	v_pk_fma_f32 v[70:71], s[86:87], v[118:119], v[70:71]
	s_nop 0
	v_add_f32_e32 v69, v70, v71
	v_fma_mix_f32 v69, v1, v30, v69 op_sel_hi:[0,1,0]
	s_waitcnt vmcnt(3)
	v_fma_mixlo_f16 v69, v69, v34, 0 op_sel_hi:[0,1,0]
	ds_write_b16 v68, v69 offset:20736
	s_waitcnt lgkmcnt(0)
	s_load_dwordx16 s[36:51], s[54:55], 0x900
	s_load_dwordx16 s[72:87], s[54:55], 0x940
	v_cvt_f32_f16_sdwa v38, v38 dst_sel:DWORD dst_unused:UNUSED_PAD src0_sel:WORD_1
	v_pk_mul_f32 v[122:123], v[38:39], v[14:15] op_sel_hi:[0,1]
	v_exp_f32_e32 v122, v122
	v_exp_f32_e32 v123, v123
	v_pk_mul_f32 v[130:131], v[38:39], v[16:17] op_sel_hi:[0,1]
	v_exp_f32_e32 v130, v130
	v_exp_f32_e32 v131, v131
	v_fma_mix_f32 v120, v38, v30, 0 op_sel:[0,1,0] op_sel_hi:[0,1,0]
	v_pk_mul_f32 v[122:123], v[122:123], v[124:125]
	v_pk_fma_f32 v[122:123], v[120:121], s[56:57], v[122:123] op_sel_hi:[0, 1, 1]
	v_pk_fma_f32 v[42:43], s[88:89], v[122:123], 0 op_sel_hi:[1, 1, 0]
	v_pk_mul_f32 v[58:59], v[130:131], v[126:127]
	s_nop 0
	v_pk_fma_f32 v[124:125], v[120:121], s[58:59], v[58:59] op_sel_hi:[0, 1, 1]
	v_pk_mul_f32 v[44:45], v[38:39], v[10:11] op_sel_hi:[0,1]
	v_exp_f32_e32 v44, v44
	v_exp_f32_e32 v45, v45
	v_pk_mul_f32 v[58:59], v[38:39], v[12:13] op_sel_hi:[0,1]
	v_exp_f32_e32 v58, v58
	v_exp_f32_e32 v59, v59
	v_pk_mul_f32 v[44:45], v[44:45], v[128:129]
	v_pk_fma_f32 v[42:43], s[90:91], v[124:125], v[42:43]
	v_pk_fma_f32 v[126:127], v[120:121], s[60:61], v[44:45] op_sel_hi:[0, 1, 1]
	v_pk_mul_f32 v[44:45], v[58:59], v[110:111]
	v_pk_mul_f32 v[46:47], v[38:39], v[8:9] op_sel_hi:[0,1]
	v_pk_fma_f32 v[110:111], v[120:121], s[62:63], v[44:45] op_sel_hi:[0, 1, 1]
	v_pk_mul_f32 v[44:45], v[38:39], v[6:7] op_sel_hi:[0,1]
	v_exp_f32_e32 v44, v44
	v_exp_f32_e32 v45, v45
	v_exp_f32_e32 v46, v46
	v_exp_f32_e32 v47, v47
	v_pk_fma_f32 v[42:43], s[92:93], v[126:127], v[42:43]
	v_pk_mul_f32 v[44:45], v[44:45], v[112:113]
	v_pk_fma_f32 v[42:43], s[94:95], v[110:111], v[42:43]
	v_pk_fma_f32 v[112:113], v[120:121], s[64:65], v[44:45] op_sel_hi:[0, 1, 1]
	v_pk_mul_f32 v[44:45], v[46:47], v[114:115]
	v_pk_mul_f32 v[46:47], v[38:39], v[4:5] op_sel_hi:[0,1]
	v_pk_fma_f32 v[114:115], v[120:121], s[66:67], v[44:45] op_sel_hi:[0, 1, 1]
	v_pk_mul_f32 v[44:45], v[38:39], v[2:3] op_sel_hi:[0,1]
	v_exp_f32_e32 v44, v44
	v_exp_f32_e32 v45, v45
	v_exp_f32_e32 v46, v46
	v_exp_f32_e32 v47, v47
	v_pk_fma_f32 v[42:43], s[96:97], v[112:113], v[42:43]
	v_pk_mul_f32 v[44:45], v[44:45], v[116:117]
	v_pk_fma_f32 v[42:43], s[98:99], v[114:115], v[42:43]
	v_pk_fma_f32 v[116:117], v[120:121], s[68:69], v[44:45] op_sel_hi:[0, 1, 1]
	v_pk_mul_f32 v[44:45], v[46:47], v[118:119]
	v_pk_fma_f32 v[42:43], s[20:21], v[116:117], v[42:43]
	v_pk_fma_f32 v[118:119], v[120:121], s[70:71], v[44:45] op_sel_hi:[0, 1, 1]
	v_pk_fma_f32 v[42:43], s[22:23], v[118:119], v[42:43]
	s_nop 0
	v_add_f32_e32 v38, v42, v43
	v_fma_mix_f32 v30, v1, v30, v38 op_sel:[0,1,0] op_sel_hi:[0,1,0]
	v_fma_mixlo_f16 v30, v30, v34, 0 op_sel:[0,1,0] op_sel_hi:[0,1,0]
	ds_write_b16 v68, v30 offset:21776
	s_waitcnt lgkmcnt(0)
	s_load_dwordx16 s[56:71], s[54:55], 0x980
	s_load_dwordx8 s[88:95], s[54:55], 0x9c0
	s_load_dwordx4 s[96:99], s[54:55], 0x9e0
	s_load_dwordx4 s[20:23], s[54:55], 0x9f0
	v_cvt_f32_f16_e32 v30, v39
	v_pk_mul_f32 v[120:121], v[30:31], v[14:15] op_sel_hi:[0,1]
	v_exp_f32_e32 v120, v120
	v_exp_f32_e32 v121, v121
	v_pk_mul_f32 v[128:129], v[30:31], v[16:17] op_sel_hi:[0,1]
	v_exp_f32_e32 v128, v128
	v_exp_f32_e32 v129, v129
	v_fma_mix_f32 v34, v30, v31, 0 op_sel_hi:[0,1,0]
	v_pk_mul_f32 v[120:121], v[120:121], v[122:123]
	v_pk_fma_f32 v[120:121], v[34:35], s[36:37], v[120:121] op_sel_hi:[0, 1, 1]
	v_pk_fma_f32 v[70:71], s[72:73], v[120:121], 0 op_sel_hi:[1, 1, 0]
	v_pk_mul_f32 v[86:87], v[128:129], v[124:125]
	s_nop 0
	v_pk_fma_f32 v[122:123], v[34:35], s[38:39], v[86:87] op_sel_hi:[0, 1, 1]
	v_pk_mul_f32 v[72:73], v[30:31], v[10:11] op_sel_hi:[0,1]
	v_exp_f32_e32 v72, v72
	v_exp_f32_e32 v73, v73
	v_pk_mul_f32 v[86:87], v[30:31], v[12:13] op_sel_hi:[0,1]
	v_exp_f32_e32 v86, v86
	v_exp_f32_e32 v87, v87
	v_pk_mul_f32 v[72:73], v[72:73], v[126:127]
	v_pk_fma_f32 v[70:71], s[74:75], v[122:123], v[70:71]
	v_pk_fma_f32 v[124:125], v[34:35], s[40:41], v[72:73] op_sel_hi:[0, 1, 1]
	v_pk_mul_f32 v[72:73], v[86:87], v[110:111]
	v_pk_mul_f32 v[74:75], v[30:31], v[8:9] op_sel_hi:[0,1]
	v_pk_fma_f32 v[110:111], v[34:35], s[42:43], v[72:73] op_sel_hi:[0, 1, 1]
	v_pk_mul_f32 v[72:73], v[30:31], v[6:7] op_sel_hi:[0,1]
	v_exp_f32_e32 v72, v72
	v_exp_f32_e32 v73, v73
	v_exp_f32_e32 v74, v74
	v_exp_f32_e32 v75, v75
	v_pk_fma_f32 v[70:71], s[76:77], v[124:125], v[70:71]
	v_pk_mul_f32 v[72:73], v[72:73], v[112:113]
	v_pk_fma_f32 v[70:71], s[78:79], v[110:111], v[70:71]
	v_pk_fma_f32 v[112:113], v[34:35], s[44:45], v[72:73] op_sel_hi:[0, 1, 1]
	v_pk_mul_f32 v[72:73], v[74:75], v[114:115]
	v_pk_mul_f32 v[74:75], v[30:31], v[4:5] op_sel_hi:[0,1]
	v_pk_fma_f32 v[114:115], v[34:35], s[46:47], v[72:73] op_sel_hi:[0, 1, 1]
	v_pk_mul_f32 v[72:73], v[30:31], v[2:3] op_sel_hi:[0,1]
	v_exp_f32_e32 v72, v72
	v_exp_f32_e32 v73, v73
	v_exp_f32_e32 v74, v74
	v_exp_f32_e32 v75, v75
	v_pk_fma_f32 v[70:71], s[80:81], v[112:113], v[70:71]
	v_pk_mul_f32 v[72:73], v[72:73], v[116:117]
	v_pk_fma_f32 v[70:71], s[82:83], v[114:115], v[70:71]
	v_pk_fma_f32 v[116:117], v[34:35], s[48:49], v[72:73] op_sel_hi:[0, 1, 1]
	v_pk_mul_f32 v[72:73], v[74:75], v[118:119]
	v_pk_fma_f32 v[70:71], s[84:85], v[116:117], v[70:71]
	v_pk_fma_f32 v[118:119], v[34:35], s[50:51], v[72:73] op_sel_hi:[0, 1, 1]
	v_pk_fma_f32 v[70:71], s[86:87], v[118:119], v[70:71]
	s_nop 0
	v_add_f32_e32 v30, v70, v71
	v_fma_mix_f32 v30, v1, v31, v30 op_sel_hi:[0,1,0]
	v_fma_mixlo_f16 v30, v30, v35, 0 op_sel_hi:[0,1,0]
	ds_write_b16 v68, v30 offset:22816
	s_waitcnt lgkmcnt(0)
	s_load_dwordx16 s[36:51], s[54:55], 0xa00
	s_load_dwordx16 s[72:87], s[54:55], 0xa40
	v_cvt_f32_f16_sdwa v30, v39 dst_sel:DWORD dst_unused:UNUSED_PAD src0_sel:WORD_1
	v_pk_mul_f32 v[38:39], v[30:31], v[14:15] op_sel_hi:[0,1]
	v_exp_f32_e32 v38, v38
	v_exp_f32_e32 v39, v39
	v_pk_mul_f32 v[126:127], v[30:31], v[16:17] op_sel_hi:[0,1]
	v_exp_f32_e32 v126, v126
	v_exp_f32_e32 v127, v127
	v_fma_mix_f32 v34, v30, v31, 0 op_sel:[0,1,0] op_sel_hi:[0,1,0]
	v_pk_mul_f32 v[38:39], v[38:39], v[120:121]
	v_pk_fma_f32 v[38:39], v[34:35], s[56:57], v[38:39] op_sel_hi:[0, 1, 1]
	v_pk_fma_f32 v[42:43], s[88:89], v[38:39], 0 op_sel_hi:[1, 1, 0]
	v_pk_mul_f32 v[58:59], v[126:127], v[122:123]
	s_nop 0
	v_pk_fma_f32 v[120:121], v[34:35], s[58:59], v[58:59] op_sel_hi:[0, 1, 1]
	v_pk_mul_f32 v[44:45], v[30:31], v[10:11] op_sel_hi:[0,1]
	v_exp_f32_e32 v44, v44
	v_exp_f32_e32 v45, v45
	v_pk_mul_f32 v[58:59], v[30:31], v[12:13] op_sel_hi:[0,1]
	v_exp_f32_e32 v58, v58
	v_exp_f32_e32 v59, v59
	v_pk_mul_f32 v[44:45], v[44:45], v[124:125]
	v_pk_fma_f32 v[42:43], s[90:91], v[120:121], v[42:43]
	v_pk_fma_f32 v[122:123], v[34:35], s[60:61], v[44:45] op_sel_hi:[0, 1, 1]
	v_pk_mul_f32 v[44:45], v[58:59], v[110:111]
	v_pk_mul_f32 v[46:47], v[30:31], v[8:9] op_sel_hi:[0,1]
	v_pk_fma_f32 v[110:111], v[34:35], s[62:63], v[44:45] op_sel_hi:[0, 1, 1]
	v_pk_mul_f32 v[44:45], v[30:31], v[6:7] op_sel_hi:[0,1]
	v_exp_f32_e32 v44, v44
	v_exp_f32_e32 v45, v45
	v_exp_f32_e32 v46, v46
	v_exp_f32_e32 v47, v47
	v_pk_fma_f32 v[42:43], s[92:93], v[122:123], v[42:43]
	v_pk_mul_f32 v[44:45], v[44:45], v[112:113]
	v_pk_fma_f32 v[42:43], s[94:95], v[110:111], v[42:43]
	v_pk_fma_f32 v[112:113], v[34:35], s[64:65], v[44:45] op_sel_hi:[0, 1, 1]
	v_pk_mul_f32 v[44:45], v[46:47], v[114:115]
	v_pk_mul_f32 v[46:47], v[30:31], v[4:5] op_sel_hi:[0,1]
	v_pk_fma_f32 v[114:115], v[34:35], s[66:67], v[44:45] op_sel_hi:[0, 1, 1]
	v_pk_mul_f32 v[44:45], v[30:31], v[2:3] op_sel_hi:[0,1]
	v_exp_f32_e32 v44, v44
	v_exp_f32_e32 v45, v45
	v_exp_f32_e32 v46, v46
	v_exp_f32_e32 v47, v47
	v_pk_fma_f32 v[42:43], s[96:97], v[112:113], v[42:43]
	v_pk_mul_f32 v[44:45], v[44:45], v[116:117]
	v_pk_fma_f32 v[42:43], s[98:99], v[114:115], v[42:43]
	v_pk_fma_f32 v[116:117], v[34:35], s[68:69], v[44:45] op_sel_hi:[0, 1, 1]
	v_pk_mul_f32 v[44:45], v[46:47], v[118:119]
	v_pk_fma_f32 v[42:43], s[20:21], v[116:117], v[42:43]
	v_pk_fma_f32 v[118:119], v[34:35], s[70:71], v[44:45] op_sel_hi:[0, 1, 1]
	v_pk_fma_f32 v[42:43], s[22:23], v[118:119], v[42:43]
	s_nop 0
	v_add_f32_e32 v30, v42, v43
	v_fma_mix_f32 v30, v1, v31, v30 op_sel:[0,1,0] op_sel_hi:[0,1,0]
	v_fma_mixlo_f16 v30, v30, v35, 0 op_sel:[0,1,0] op_sel_hi:[0,1,0]
	ds_write_b16 v68, v30 offset:23856
	s_waitcnt lgkmcnt(0)
	s_load_dwordx16 s[56:71], s[54:55], 0xa80
	s_load_dwordx8 s[88:95], s[54:55], 0xac0
	s_load_dwordx4 s[96:99], s[54:55], 0xae0
	s_load_dwordx4 s[20:23], s[54:55], 0xaf0
	v_cvt_f32_f16_e32 v30, v40
	v_pk_mul_f32 v[124:125], v[30:31], v[14:15] op_sel_hi:[0,1]
	v_exp_f32_e32 v124, v124
	v_exp_f32_e32 v125, v125
	v_pk_mul_f32 v[126:127], v[30:31], v[16:17] op_sel_hi:[0,1]
	v_exp_f32_e32 v126, v126
	v_exp_f32_e32 v127, v127
	v_fma_mix_f32 v34, v30, v32, 0 op_sel_hi:[0,1,0]
	v_pk_mul_f32 v[38:39], v[124:125], v[38:39]
	v_pk_fma_f32 v[38:39], v[34:35], s[36:37], v[38:39] op_sel_hi:[0, 1, 1]
	v_pk_fma_f32 v[70:71], s[72:73], v[38:39], 0 op_sel_hi:[1, 1, 0]
	v_pk_mul_f32 v[86:87], v[126:127], v[120:121]
	s_nop 0
	v_pk_fma_f32 v[120:121], v[34:35], s[38:39], v[86:87] op_sel_hi:[0, 1, 1]
	v_pk_mul_f32 v[72:73], v[30:31], v[10:11] op_sel_hi:[0,1]
	v_exp_f32_e32 v72, v72
	v_exp_f32_e32 v73, v73
	v_pk_mul_f32 v[86:87], v[30:31], v[12:13] op_sel_hi:[0,1]
	v_exp_f32_e32 v86, v86
	v_exp_f32_e32 v87, v87
	v_pk_mul_f32 v[72:73], v[72:73], v[122:123]
	v_pk_fma_f32 v[70:71], s[74:75], v[120:121], v[70:71]
	v_pk_fma_f32 v[122:123], v[34:35], s[40:41], v[72:73] op_sel_hi:[0, 1, 1]
	v_pk_mul_f32 v[72:73], v[86:87], v[110:111]
	v_pk_mul_f32 v[74:75], v[30:31], v[8:9] op_sel_hi:[0,1]
	v_pk_fma_f32 v[110:111], v[34:35], s[42:43], v[72:73] op_sel_hi:[0, 1, 1]
	v_pk_mul_f32 v[72:73], v[30:31], v[6:7] op_sel_hi:[0,1]
	v_exp_f32_e32 v72, v72
	v_exp_f32_e32 v73, v73
	v_exp_f32_e32 v74, v74
	v_exp_f32_e32 v75, v75
	v_pk_fma_f32 v[70:71], s[76:77], v[122:123], v[70:71]
	v_pk_mul_f32 v[72:73], v[72:73], v[112:113]
	v_pk_fma_f32 v[70:71], s[78:79], v[110:111], v[70:71]
	v_pk_fma_f32 v[112:113], v[34:35], s[44:45], v[72:73] op_sel_hi:[0, 1, 1]
	v_pk_mul_f32 v[72:73], v[74:75], v[114:115]
	v_pk_fma_f32 v[70:71], s[80:81], v[112:113], v[70:71]
	v_pk_fma_f32 v[114:115], v[34:35], s[46:47], v[72:73] op_sel_hi:[0, 1, 1]
	v_pk_mul_f32 v[72:73], v[30:31], v[2:3] op_sel_hi:[0,1]
	v_exp_f32_e32 v72, v72
	v_exp_f32_e32 v73, v73
	v_pk_mul_f32 v[30:31], v[30:31], v[4:5] op_sel_hi:[0,1]
	v_exp_f32_e32 v30, v30
	v_exp_f32_e32 v31, v31
	v_pk_mul_f32 v[72:73], v[72:73], v[116:117]
	v_pk_fma_f32 v[70:71], s[82:83], v[114:115], v[70:71]
	v_pk_fma_f32 v[116:117], v[34:35], s[48:49], v[72:73] op_sel_hi:[0, 1, 1]
	v_pk_mul_f32 v[30:31], v[30:31], v[118:119]
	v_pk_fma_f32 v[70:71], s[84:85], v[116:117], v[70:71]
	v_pk_fma_f32 v[30:31], v[34:35], s[50:51], v[30:31] op_sel_hi:[0, 1, 1]
	v_pk_fma_f32 v[34:35], s[86:87], v[30:31], v[70:71]
	s_nop 0
	v_add_f32_e32 v34, v34, v35
	v_fma_mix_f32 v34, v1, v32, v34 op_sel_hi:[0,1,0]
	v_fma_mixlo_f16 v34, v34, v36, 0 op_sel_hi:[0,1,0]
	ds_write_b16 v68, v34 offset:24896
	s_waitcnt lgkmcnt(0)
	s_load_dwordx16 s[36:51], s[54:55], 0xb00
	s_load_dwordx16 s[72:87], s[54:55], 0xb40
	v_cvt_f32_f16_sdwa v34, v40 dst_sel:DWORD dst_unused:UNUSED_PAD src0_sel:WORD_1
	v_pk_mul_f32 v[118:119], v[34:35], v[14:15] op_sel_hi:[0,1]
	v_exp_f32_e32 v118, v118
	v_exp_f32_e32 v119, v119
	v_pk_mul_f32 v[124:125], v[34:35], v[16:17] op_sel_hi:[0,1]
	v_exp_f32_e32 v124, v124
	v_exp_f32_e32 v125, v125
	v_fma_mix_f32 v40, v34, v32, 0 op_sel:[0,1,0] op_sel_hi:[0,1,0]
	v_pk_mul_f32 v[38:39], v[118:119], v[38:39]
	v_pk_fma_f32 v[38:39], v[40:41], s[56:57], v[38:39] op_sel_hi:[0, 1, 1]
	v_pk_fma_f32 v[42:43], s[88:89], v[38:39], 0 op_sel_hi:[1, 1, 0]
	v_pk_mul_f32 v[58:59], v[124:125], v[120:121]
	s_nop 0
	v_pk_fma_f32 v[118:119], v[40:41], s[58:59], v[58:59] op_sel_hi:[0, 1, 1]
	v_pk_mul_f32 v[44:45], v[34:35], v[10:11] op_sel_hi:[0,1]
	v_exp_f32_e32 v44, v44
	v_exp_f32_e32 v45, v45
	v_pk_mul_f32 v[58:59], v[34:35], v[12:13] op_sel_hi:[0,1]
	v_exp_f32_e32 v58, v58
	v_exp_f32_e32 v59, v59
	v_pk_mul_f32 v[44:45], v[44:45], v[122:123]
	v_pk_fma_f32 v[42:43], s[90:91], v[118:119], v[42:43]
	v_pk_fma_f32 v[120:121], v[40:41], s[60:61], v[44:45] op_sel_hi:[0, 1, 1]
	v_pk_mul_f32 v[44:45], v[58:59], v[110:111]
	v_pk_mul_f32 v[46:47], v[34:35], v[8:9] op_sel_hi:[0,1]
	v_pk_fma_f32 v[110:111], v[40:41], s[62:63], v[44:45] op_sel_hi:[0, 1, 1]
	v_pk_mul_f32 v[44:45], v[34:35], v[6:7] op_sel_hi:[0,1]
	v_exp_f32_e32 v44, v44
	v_exp_f32_e32 v45, v45
	v_exp_f32_e32 v46, v46
	v_exp_f32_e32 v47, v47
	v_pk_fma_f32 v[42:43], s[92:93], v[120:121], v[42:43]
	v_pk_mul_f32 v[44:45], v[44:45], v[112:113]
	v_pk_fma_f32 v[42:43], s[94:95], v[110:111], v[42:43]
	v_pk_fma_f32 v[112:113], v[40:41], s[64:65], v[44:45] op_sel_hi:[0, 1, 1]
	v_pk_mul_f32 v[44:45], v[46:47], v[114:115]
	v_pk_fma_f32 v[42:43], s[96:97], v[112:113], v[42:43]
	v_pk_fma_f32 v[114:115], v[40:41], s[66:67], v[44:45] op_sel_hi:[0, 1, 1]
	v_pk_mul_f32 v[44:45], v[34:35], v[2:3] op_sel_hi:[0,1]
	v_exp_f32_e32 v44, v44
	v_exp_f32_e32 v45, v45
	v_pk_mul_f32 v[34:35], v[34:35], v[4:5] op_sel_hi:[0,1]
	v_exp_f32_e32 v34, v34
	v_exp_f32_e32 v35, v35
	v_pk_mul_f32 v[44:45], v[44:45], v[116:117]
	v_pk_fma_f32 v[42:43], s[98:99], v[114:115], v[42:43]
	v_pk_fma_f32 v[116:117], v[40:41], s[68:69], v[44:45] op_sel_hi:[0, 1, 1]
	v_pk_mul_f32 v[30:31], v[34:35], v[30:31]
	v_pk_fma_f32 v[42:43], s[20:21], v[116:117], v[42:43]
	v_pk_fma_f32 v[30:31], v[40:41], s[70:71], v[30:31] op_sel_hi:[0, 1, 1]
	v_pk_fma_f32 v[34:35], s[22:23], v[30:31], v[42:43]
	s_nop 0
	v_add_f32_e32 v34, v34, v35
	v_fma_mix_f32 v32, v1, v32, v34 op_sel:[0,1,0] op_sel_hi:[0,1,0]
	v_fma_mixlo_f16 v32, v32, v36, 0 op_sel:[0,1,0] op_sel_hi:[0,1,0]
	ds_write_b16 v68, v32 offset:25936
	s_waitcnt lgkmcnt(0)
	s_load_dwordx16 s[56:71], s[54:55], 0xb80
	s_load_dwordx8 s[88:95], s[54:55], 0xbc0
	s_load_dwordx4 s[96:99], s[54:55], 0xbe0
	s_load_dwordx4 s[20:23], s[54:55], 0xbf0
	v_cvt_f32_f16_e32 v32, v41
	v_pk_mul_f32 v[122:123], v[32:33], v[14:15] op_sel_hi:[0,1]
	v_exp_f32_e32 v122, v122
	v_exp_f32_e32 v123, v123
	v_pk_mul_f32 v[124:125], v[32:33], v[16:17] op_sel_hi:[0,1]
	v_exp_f32_e32 v124, v124
	v_exp_f32_e32 v125, v125
	v_fma_mix_f32 v34, v32, v33, 0 op_sel_hi:[0,1,0]
	v_pk_mul_f32 v[38:39], v[122:123], v[38:39]
	v_pk_fma_f32 v[38:39], v[34:35], s[36:37], v[38:39] op_sel_hi:[0, 1, 1]
	v_pk_fma_f32 v[70:71], s[72:73], v[38:39], 0 op_sel_hi:[1, 1, 0]
	v_pk_mul_f32 v[86:87], v[124:125], v[118:119]
	s_nop 0
	v_pk_fma_f32 v[118:119], v[34:35], s[38:39], v[86:87] op_sel_hi:[0, 1, 1]
	v_pk_mul_f32 v[72:73], v[32:33], v[10:11] op_sel_hi:[0,1]
	v_exp_f32_e32 v72, v72
	v_exp_f32_e32 v73, v73
	v_pk_mul_f32 v[86:87], v[32:33], v[12:13] op_sel_hi:[0,1]
	v_exp_f32_e32 v86, v86
	v_exp_f32_e32 v87, v87
	v_pk_mul_f32 v[72:73], v[72:73], v[120:121]
	v_pk_fma_f32 v[70:71], s[74:75], v[118:119], v[70:71]
	v_pk_fma_f32 v[120:121], v[34:35], s[40:41], v[72:73] op_sel_hi:[0, 1, 1]
	v_pk_mul_f32 v[72:73], v[86:87], v[110:111]
	v_pk_mul_f32 v[74:75], v[32:33], v[8:9] op_sel_hi:[0,1]
	v_pk_fma_f32 v[110:111], v[34:35], s[42:43], v[72:73] op_sel_hi:[0, 1, 1]
	v_pk_mul_f32 v[72:73], v[32:33], v[6:7] op_sel_hi:[0,1]
	v_exp_f32_e32 v72, v72
	v_exp_f32_e32 v73, v73
	v_exp_f32_e32 v74, v74
	v_exp_f32_e32 v75, v75
	v_pk_fma_f32 v[70:71], s[76:77], v[120:121], v[70:71]
	v_pk_mul_f32 v[72:73], v[72:73], v[112:113]
	v_pk_fma_f32 v[70:71], s[78:79], v[110:111], v[70:71]
	v_pk_fma_f32 v[112:113], v[34:35], s[44:45], v[72:73] op_sel_hi:[0, 1, 1]
	v_pk_mul_f32 v[72:73], v[74:75], v[114:115]
	v_pk_mul_f32 v[74:75], v[32:33], v[4:5] op_sel_hi:[0,1]
	v_pk_fma_f32 v[114:115], v[34:35], s[46:47], v[72:73] op_sel_hi:[0, 1, 1]
	v_pk_mul_f32 v[72:73], v[32:33], v[2:3] op_sel_hi:[0,1]
	v_exp_f32_e32 v72, v72
	v_exp_f32_e32 v73, v73
	v_exp_f32_e32 v74, v74
	v_exp_f32_e32 v75, v75
	v_pk_fma_f32 v[70:71], s[80:81], v[112:113], v[70:71]
	v_pk_mul_f32 v[72:73], v[72:73], v[116:117]
	v_pk_fma_f32 v[70:71], s[82:83], v[114:115], v[70:71]
	v_pk_fma_f32 v[116:117], v[34:35], s[48:49], v[72:73] op_sel_hi:[0, 1, 1]
	v_pk_mul_f32 v[30:31], v[74:75], v[30:31]
	v_pk_fma_f32 v[70:71], s[84:85], v[116:117], v[70:71]
	v_pk_fma_f32 v[30:31], v[34:35], s[50:51], v[30:31] op_sel_hi:[0, 1, 1]
	v_pk_fma_f32 v[34:35], s[86:87], v[30:31], v[70:71]
	s_nop 0
	v_add_f32_e32 v32, v34, v35
	v_fma_mix_f32 v32, v1, v33, v32 op_sel_hi:[0,1,0]
	v_fma_mixlo_f16 v32, v32, v37, 0 op_sel_hi:[0,1,0]
	ds_write_b16 v68, v32 offset:26976
	s_waitcnt lgkmcnt(0)
	s_load_dwordx16 s[36:51], s[54:55], 0xc00
	s_load_dwordx16 s[72:87], s[54:55], 0xc40
	v_cvt_f32_f16_sdwa v32, v41 dst_sel:DWORD dst_unused:UNUSED_PAD src0_sel:WORD_1
	v_pk_mul_f32 v[40:41], v[32:33], v[14:15] op_sel_hi:[0,1]
	v_pk_mul_f32 v[122:123], v[32:33], v[16:17] op_sel_hi:[0,1]
	v_exp_f32_e32 v40, v40
	v_exp_f32_e32 v41, v41
	v_exp_f32_e32 v122, v122
	v_exp_f32_e32 v123, v123
	v_fma_mix_f32 v34, v32, v33, 0 op_sel:[0,1,0] op_sel_hi:[0,1,0]
	v_pk_mul_f32 v[38:39], v[40:41], v[38:39]
	v_pk_mul_f32 v[40:41], v[122:123], v[118:119]
	v_pk_fma_f32 v[118:119], v[34:35], s[58:59], v[40:41] op_sel_hi:[0, 1, 1]
	v_pk_mul_f32 v[40:41], v[32:33], v[10:11] op_sel_hi:[0,1]
	v_pk_fma_f32 v[124:125], v[34:35], s[56:57], v[38:39] op_sel_hi:[0, 1, 1]
	v_exp_f32_e32 v40, v40
	v_exp_f32_e32 v41, v41
	v_pk_mul_f32 v[42:43], v[32:33], v[12:13] op_sel_hi:[0,1]
	v_exp_f32_e32 v42, v42
	v_exp_f32_e32 v43, v43
	v_pk_fma_f32 v[38:39], s[88:89], v[124:125], 0 op_sel_hi:[1, 1, 0]
	v_pk_mul_f32 v[40:41], v[40:41], v[120:121]
	v_pk_fma_f32 v[38:39], s[90:91], v[118:119], v[38:39]
	v_pk_fma_f32 v[120:121], v[34:35], s[60:61], v[40:41] op_sel_hi:[0, 1, 1]
	v_pk_mul_f32 v[40:41], v[42:43], v[110:111]
	v_pk_fma_f32 v[38:39], s[92:93], v[120:121], v[38:39]
	v_pk_fma_f32 v[62:63], v[34:35], s[62:63], v[40:41] op_sel_hi:[0, 1, 1]
	v_pk_mul_f32 v[40:41], v[32:33], v[6:7] op_sel_hi:[0,1]
	v_exp_f32_e32 v40, v40
	v_exp_f32_e32 v41, v41
	v_pk_mul_f32 v[42:43], v[32:33], v[8:9] op_sel_hi:[0,1]
	v_exp_f32_e32 v42, v42
	v_exp_f32_e32 v43, v43
	v_pk_mul_f32 v[40:41], v[40:41], v[112:113]
	v_pk_fma_f32 v[38:39], s[94:95], v[62:63], v[38:39]
	v_pk_fma_f32 v[64:65], v[34:35], s[64:65], v[40:41] op_sel_hi:[0, 1, 1]
	v_pk_mul_f32 v[40:41], v[42:43], v[114:115]
	v_pk_fma_f32 v[38:39], s[96:97], v[64:65], v[38:39]
	v_pk_fma_f32 v[102:103], v[34:35], s[66:67], v[40:41] op_sel_hi:[0, 1, 1]
	v_pk_mul_f32 v[40:41], v[32:33], v[2:3] op_sel_hi:[0,1]
	v_exp_f32_e32 v40, v40
	v_exp_f32_e32 v41, v41
	v_pk_mul_f32 v[42:43], v[32:33], v[4:5] op_sel_hi:[0,1]
	v_exp_f32_e32 v42, v42
	v_exp_f32_e32 v43, v43
	v_pk_mul_f32 v[40:41], v[40:41], v[116:117]
	v_pk_fma_f32 v[38:39], s[98:99], v[102:103], v[38:39]
	v_pk_fma_f32 v[104:105], v[34:35], s[68:69], v[40:41] op_sel_hi:[0, 1, 1]
	v_pk_mul_f32 v[30:31], v[42:43], v[30:31]
	v_pk_fma_f32 v[38:39], s[20:21], v[104:105], v[38:39]
	v_pk_fma_f32 v[106:107], v[34:35], s[70:71], v[30:31] op_sel_hi:[0, 1, 1]
	v_pk_fma_f32 v[30:31], s[22:23], v[106:107], v[38:39]
	s_nop 0
	v_add_f32_e32 v30, v30, v31
	v_fma_mix_f32 v30, v1, v33, v30 op_sel:[0,1,0] op_sel_hi:[0,1,0]
	v_fma_mixlo_f16 v30, v30, v37, 0 op_sel:[0,1,0] op_sel_hi:[0,1,0]
	ds_write_b16 v68, v30 offset:28016
	s_waitcnt lgkmcnt(0)
	s_load_dwordx16 s[56:71], s[54:55], 0xc80
	s_load_dwordx8 s[88:95], s[54:55], 0xcc0
	s_load_dwordx4 s[96:99], s[54:55], 0xce0
	s_load_dwordx4 s[20:23], s[54:55], 0xcf0
	s_waitcnt vmcnt(2)
	v_cvt_f32_f16_e32 v108, v26
	s_waitcnt vmcnt(1)
	v_pk_mul_f32 v[112:113], v[108:109], v[14:15] op_sel_hi:[0,1]
	v_exp_f32_e32 v112, v112
	v_exp_f32_e32 v113, v113
	v_pk_mul_f32 v[114:115], v[108:109], v[16:17] op_sel_hi:[0,1]
	v_exp_f32_e32 v114, v114
	v_exp_f32_e32 v115, v115
	v_fma_mix_f32 v110, v108, v18, 0 op_sel_hi:[0,1,0]
	v_pk_mul_f32 v[112:113], v[112:113], v[124:125]
	v_pk_fma_f32 v[112:113], v[110:111], s[36:37], v[112:113] op_sel_hi:[0, 1, 1]
	v_pk_fma_f32 v[70:71], s[72:73], v[112:113], 0 op_sel_hi:[1, 1, 0]
	v_pk_mul_f32 v[86:87], v[114:115], v[118:119]
	s_nop 0
	v_pk_fma_f32 v[114:115], v[110:111], s[38:39], v[86:87] op_sel_hi:[0, 1, 1]
	v_pk_mul_f32 v[72:73], v[108:109], v[10:11] op_sel_hi:[0,1]
	v_exp_f32_e32 v72, v72
	v_exp_f32_e32 v73, v73
	v_pk_mul_f32 v[86:87], v[108:109], v[12:13] op_sel_hi:[0,1]
	v_exp_f32_e32 v86, v86
	v_exp_f32_e32 v87, v87
	v_pk_mul_f32 v[72:73], v[72:73], v[120:121]
	v_pk_fma_f32 v[70:71], s[74:75], v[114:115], v[70:71]
	v_pk_fma_f32 v[116:117], v[110:111], s[40:41], v[72:73] op_sel_hi:[0, 1, 1]
	v_pk_mul_f32 v[62:63], v[86:87], v[62:63]
	v_pk_fma_f32 v[70:71], s[76:77], v[116:117], v[70:71]
	v_pk_fma_f32 v[118:119], v[110:111], s[42:43], v[62:63] op_sel_hi:[0, 1, 1]
	v_pk_fma_f32 v[62:63], s[78:79], v[118:119], v[70:71]
	v_pk_mul_f32 v[70:71], v[108:109], v[6:7] op_sel_hi:[0,1]
	v_exp_f32_e32 v70, v70
	v_exp_f32_e32 v71, v71
	v_pk_mul_f32 v[72:73], v[108:109], v[8:9] op_sel_hi:[0,1]
	v_exp_f32_e32 v72, v72
	v_exp_f32_e32 v73, v73
	v_pk_mul_f32 v[64:65], v[70:71], v[64:65]
	v_pk_mul_f32 v[70:71], v[108:109], v[4:5] op_sel_hi:[0,1]
	v_pk_fma_f32 v[120:121], v[110:111], s[44:45], v[64:65] op_sel_hi:[0, 1, 1]
	v_pk_mul_f32 v[64:65], v[72:73], v[102:103]
	v_exp_f32_e32 v70, v70
	v_pk_fma_f32 v[102:103], v[110:111], s[46:47], v[64:65] op_sel_hi:[0, 1, 1]
	v_pk_mul_f32 v[64:65], v[108:109], v[2:3] op_sel_hi:[0,1]
	v_exp_f32_e32 v64, v64
	v_exp_f32_e32 v65, v65
	v_exp_f32_e32 v71, v71
	v_pk_fma_f32 v[62:63], s[80:81], v[120:121], v[62:63]
	v_pk_mul_f32 v[64:65], v[64:65], v[104:105]
	v_pk_fma_f32 v[62:63], s[82:83], v[102:103], v[62:63]
	v_pk_fma_f32 v[104:105], v[110:111], s[48:49], v[64:65] op_sel_hi:[0, 1, 1]
	v_pk_mul_f32 v[64:65], v[70:71], v[106:107]
	v_pk_fma_f32 v[62:63], s[84:85], v[104:105], v[62:63]
	v_pk_fma_f32 v[98:99], v[110:111], s[50:51], v[64:65] op_sel_hi:[0, 1, 1]
	v_pk_fma_f32 v[62:63], s[86:87], v[98:99], v[62:63]
	s_nop 0
	v_add_f32_e32 v62, v62, v63
	v_fma_mix_f32 v62, v1, v18, v62 op_sel_hi:[0,1,0]
	s_waitcnt vmcnt(0)
	v_fma_mixlo_f16 v62, v62, v22, 0 op_sel_hi:[0,1,0]
	ds_write_b16 v68, v62 offset:29056
	v_lshrrev_b32_e32 v196, 6, v0
	v_and_b32_e32 v197, 48, v0
	v_lshl_or_b32 v196, v196, 7, v197
	v_and_b32_e32 v197, 15, v0
	v_or_b32_e32 v197, s28, v197
	v_lshl_or_b32 v196, v197, 10, v196
	v_add_u32_e32 v197, 0x4000, v196
	global_load_dwordx4 v[180:183], v196, s[4:5]
	global_load_dwordx4 v[184:187], v196, s[4:5] offset:64
	global_load_dwordx4 v[188:191], v197, s[4:5]
	global_load_dwordx4 v[192:195], v197, s[4:5] offset:64
	v_and_b32_e32 v196, 63, v0
	v_lshlrev_b32_e32 v196, 4, v196
	global_load_dwordx4 v[204:207], v196, s[6:7]
	global_load_dwordx4 v[208:211], v196, s[8:9]
	s_waitcnt lgkmcnt(0)
	s_load_dwordx16 s[36:51], s[54:55], 0xd00
	s_load_dwordx16 s[72:87], s[54:55], 0xd40
	v_cvt_f32_f16_sdwa v26, v26 dst_sel:DWORD dst_unused:UNUSED_PAD src0_sel:WORD_1
	v_pk_mul_f32 v[106:107], v[26:27], v[14:15] op_sel_hi:[0,1]
	v_exp_f32_e32 v106, v106
	v_exp_f32_e32 v107, v107
	v_pk_mul_f32 v[108:109], v[26:27], v[16:17] op_sel_hi:[0,1]
	v_exp_f32_e32 v108, v108
	v_exp_f32_e32 v109, v109
	v_fma_mix_f32 v100, v26, v18, 0 op_sel:[0,1,0] op_sel_hi:[0,1,0]
	v_pk_mul_f32 v[106:107], v[106:107], v[112:113]
	v_pk_fma_f32 v[106:107], v[100:101], s[56:57], v[106:107] op_sel_hi:[0, 1, 1]
	v_pk_fma_f32 v[30:31], s[88:89], v[106:107], 0 op_sel_hi:[1, 1, 0]
	v_pk_mul_f32 v[46:47], v[108:109], v[114:115]
	s_nop 0
	v_pk_fma_f32 v[108:109], v[100:101], s[58:59], v[46:47] op_sel_hi:[0, 1, 1]
	v_pk_mul_f32 v[32:33], v[26:27], v[10:11] op_sel_hi:[0,1]
	v_exp_f32_e32 v32, v32
	v_exp_f32_e32 v33, v33
	v_pk_mul_f32 v[46:47], v[26:27], v[12:13] op_sel_hi:[0,1]
	v_exp_f32_e32 v46, v46
	v_exp_f32_e32 v47, v47
	v_pk_mul_f32 v[32:33], v[32:33], v[116:117]
	v_pk_fma_f32 v[30:31], s[90:91], v[108:109], v[30:31]
	v_pk_fma_f32 v[110:111], v[100:101], s[60:61], v[32:33] op_sel_hi:[0, 1, 1]
	v_pk_mul_f32 v[32:33], v[46:47], v[118:119]
	v_pk_mul_f32 v[34:35], v[26:27], v[8:9] op_sel_hi:[0,1]
	v_pk_fma_f32 v[112:113], v[100:101], s[62:63], v[32:33] op_sel_hi:[0, 1, 1]
	v_pk_mul_f32 v[32:33], v[26:27], v[6:7] op_sel_hi:[0,1]
	v_exp_f32_e32 v32, v32
	v_exp_f32_e32 v33, v33
	v_exp_f32_e32 v34, v34
	v_exp_f32_e32 v35, v35
	v_pk_fma_f32 v[30:31], s[92:93], v[110:111], v[30:31]
	v_pk_mul_f32 v[32:33], v[32:33], v[120:121]
	v_pk_fma_f32 v[30:31], s[94:95], v[112:113], v[30:31]
	v_pk_fma_f32 v[114:115], v[100:101], s[64:65], v[32:33] op_sel_hi:[0, 1, 1]
	v_pk_mul_f32 v[32:33], v[34:35], v[102:103]
	v_pk_mul_f32 v[34:35], v[26:27], v[4:5] op_sel_hi:[0,1]
	v_pk_fma_f32 v[102:103], v[100:101], s[66:67], v[32:33] op_sel_hi:[0, 1, 1]
	v_pk_mul_f32 v[32:33], v[26:27], v[2:3] op_sel_hi:[0,1]
	v_exp_f32_e32 v32, v32
	v_exp_f32_e32 v33, v33
	v_exp_f32_e32 v34, v34
	v_exp_f32_e32 v35, v35
	v_pk_fma_f32 v[30:31], s[96:97], v[114:115], v[30:31]
	v_pk_mul_f32 v[32:33], v[32:33], v[104:105]
	v_pk_fma_f32 v[30:31], s[98:99], v[102:103], v[30:31]
	v_pk_fma_f32 v[104:105], v[100:101], s[68:69], v[32:33] op_sel_hi:[0, 1, 1]
	v_pk_mul_f32 v[32:33], v[34:35], v[98:99]
	v_pk_fma_f32 v[30:31], s[20:21], v[104:105], v[30:31]
	v_pk_fma_f32 v[98:99], v[100:101], s[70:71], v[32:33] op_sel_hi:[0, 1, 1]
	v_pk_fma_f32 v[30:31], s[22:23], v[98:99], v[30:31]
	s_nop 0
	v_add_f32_e32 v26, v30, v31
	v_fma_mix_f32 v18, v1, v18, v26 op_sel:[0,1,0] op_sel_hi:[0,1,0]
	v_fma_mixlo_f16 v18, v18, v22, 0 op_sel:[0,1,0] op_sel_hi:[0,1,0]
	ds_write_b16 v68, v18 offset:30096
	s_waitcnt lgkmcnt(0)
	s_load_dwordx16 s[56:71], s[54:55], 0xd80
	s_load_dwordx8 s[88:95], s[54:55], 0xdc0
	s_load_dwordx4 s[96:99], s[54:55], 0xde0
	s_load_dwordx4 s[20:23], s[54:55], 0xdf0
	v_cvt_f32_f16_e32 v18, v27
	v_pk_mul_f32 v[100:101], v[18:19], v[14:15] op_sel_hi:[0,1]
	v_exp_f32_e32 v100, v100
	v_exp_f32_e32 v101, v101
	v_pk_mul_f32 v[116:117], v[18:19], v[16:17] op_sel_hi:[0,1]
	v_exp_f32_e32 v116, v116
	v_exp_f32_e32 v117, v117
	v_fma_mix_f32 v22, v18, v19, 0 op_sel_hi:[0,1,0]
	v_pk_mul_f32 v[100:101], v[100:101], v[106:107]
	v_pk_fma_f32 v[100:101], v[22:23], s[36:37], v[100:101] op_sel_hi:[0, 1, 1]
	v_pk_fma_f32 v[62:63], s[72:73], v[100:101], 0 op_sel_hi:[1, 1, 0]
	v_pk_mul_f32 v[82:83], v[116:117], v[108:109]
	s_nop 0
	v_pk_fma_f32 v[106:107], v[22:23], s[38:39], v[82:83] op_sel_hi:[0, 1, 1]
	v_pk_mul_f32 v[64:65], v[18:19], v[10:11] op_sel_hi:[0,1]
	v_exp_f32_e32 v64, v64
	v_exp_f32_e32 v65, v65
	v_pk_mul_f32 v[82:83], v[18:19], v[12:13] op_sel_hi:[0,1]
	v_exp_f32_e32 v82, v82
	v_exp_f32_e32 v83, v83
	v_pk_mul_f32 v[64:65], v[64:65], v[110:111]
	v_pk_fma_f32 v[62:63], s[74:75], v[106:107], v[62:63]
	v_pk_fma_f32 v[108:109], v[22:23], s[40:41], v[64:65] op_sel_hi:[0, 1, 1]
	v_pk_mul_f32 v[64:65], v[82:83], v[112:113]
	v_pk_mul_f32 v[70:71], v[18:19], v[8:9] op_sel_hi:[0,1]
	v_pk_fma_f32 v[110:111], v[22:23], s[42:43], v[64:65] op_sel_hi:[0, 1, 1]
	v_pk_mul_f32 v[64:65], v[18:19], v[6:7] op_sel_hi:[0,1]
	v_exp_f32_e32 v64, v64
	v_exp_f32_e32 v65, v65
	v_exp_f32_e32 v70, v70
	v_exp_f32_e32 v71, v71
	v_pk_fma_f32 v[62:63], s[76:77], v[108:109], v[62:63]
	v_pk_mul_f32 v[64:65], v[64:65], v[114:115]
	v_pk_fma_f32 v[62:63], s[78:79], v[110:111], v[62:63]
	v_pk_fma_f32 v[112:113], v[22:23], s[44:45], v[64:65] op_sel_hi:[0, 1, 1]
	v_pk_mul_f32 v[64:65], v[70:71], v[102:103]
	v_pk_mul_f32 v[70:71], v[18:19], v[4:5] op_sel_hi:[0,1]
	v_pk_fma_f32 v[102:103], v[22:23], s[46:47], v[64:65] op_sel_hi:[0, 1, 1]
	v_pk_mul_f32 v[64:65], v[18:19], v[2:3] op_sel_hi:[0,1]
	v_exp_f32_e32 v64, v64
	v_exp_f32_e32 v65, v65
	v_exp_f32_e32 v70, v70
	v_exp_f32_e32 v71, v71
	v_pk_fma_f32 v[62:63], s[80:81], v[112:113], v[62:63]
	v_pk_mul_f32 v[64:65], v[64:65], v[104:105]
	v_pk_fma_f32 v[62:63], s[82:83], v[102:103], v[62:63]
	v_pk_fma_f32 v[104:105], v[22:23], s[48:49], v[64:65] op_sel_hi:[0, 1, 1]
	v_pk_mul_f32 v[64:65], v[70:71], v[98:99]
	v_pk_fma_f32 v[62:63], s[84:85], v[104:105], v[62:63]
	v_pk_fma_f32 v[98:99], v[22:23], s[50:51], v[64:65] op_sel_hi:[0, 1, 1]
	v_pk_fma_f32 v[62:63], s[86:87], v[98:99], v[62:63]
	s_nop 0
	v_add_f32_e32 v18, v62, v63
	v_fma_mix_f32 v18, v1, v19, v18 op_sel_hi:[0,1,0]
	v_fma_mixlo_f16 v18, v18, v23, 0 op_sel_hi:[0,1,0]
	ds_write_b16 v68, v18 offset:31136
	s_waitcnt lgkmcnt(0)
	s_load_dwordx16 s[36:51], s[54:55], 0xe00
	s_load_dwordx16 s[72:87], s[54:55], 0xe40
	v_cvt_f32_f16_sdwa v18, v27 dst_sel:DWORD dst_unused:UNUSED_PAD src0_sel:WORD_1
	v_pk_mul_f32 v[26:27], v[18:19], v[14:15] op_sel_hi:[0,1]
	v_exp_f32_e32 v26, v26
	v_exp_f32_e32 v27, v27
	v_pk_mul_f32 v[114:115], v[18:19], v[16:17] op_sel_hi:[0,1]
	v_exp_f32_e32 v114, v114
	v_exp_f32_e32 v115, v115
	v_fma_mix_f32 v22, v18, v19, 0 op_sel:[0,1,0] op_sel_hi:[0,1,0]
	v_pk_mul_f32 v[26:27], v[26:27], v[100:101]
	v_pk_fma_f32 v[26:27], v[22:23], s[56:57], v[26:27] op_sel_hi:[0, 1, 1]
	v_pk_fma_f32 v[30:31], s[88:89], v[26:27], 0 op_sel_hi:[1, 1, 0]
	v_pk_mul_f32 v[46:47], v[114:115], v[106:107]
	s_nop 0
	v_pk_fma_f32 v[100:101], v[22:23], s[58:59], v[46:47] op_sel_hi:[0, 1, 1]
	v_pk_mul_f32 v[32:33], v[18:19], v[10:11] op_sel_hi:[0,1]
	v_exp_f32_e32 v32, v32
	v_exp_f32_e32 v33, v33
	v_pk_mul_f32 v[46:47], v[18:19], v[12:13] op_sel_hi:[0,1]
	v_exp_f32_e32 v46, v46
	v_exp_f32_e32 v47, v47
	v_pk_mul_f32 v[32:33], v[32:33], v[108:109]
	v_pk_fma_f32 v[30:31], s[90:91], v[100:101], v[30:31]
	v_pk_fma_f32 v[106:107], v[22:23], s[60:61], v[32:33] op_sel_hi:[0, 1, 1]
	v_pk_mul_f32 v[32:33], v[46:47], v[110:111]
	v_pk_mul_f32 v[34:35], v[18:19], v[8:9] op_sel_hi:[0,1]
	v_pk_fma_f32 v[108:109], v[22:23], s[62:63], v[32:33] op_sel_hi:[0, 1, 1]
	v_pk_mul_f32 v[32:33], v[18:19], v[6:7] op_sel_hi:[0,1]
	v_exp_f32_e32 v32, v32
	v_exp_f32_e32 v33, v33
	v_exp_f32_e32 v34, v34
	v_exp_f32_e32 v35, v35
	v_pk_fma_f32 v[30:31], s[92:93], v[106:107], v[30:31]
	v_pk_mul_f32 v[32:33], v[32:33], v[112:113]
	v_pk_fma_f32 v[30:31], s[94:95], v[108:109], v[30:31]
	v_pk_fma_f32 v[110:111], v[22:23], s[64:65], v[32:33] op_sel_hi:[0, 1, 1]
	v_pk_mul_f32 v[32:33], v[34:35], v[102:103]
	v_pk_mul_f32 v[34:35], v[18:19], v[4:5] op_sel_hi:[0,1]
	v_pk_fma_f32 v[102:103], v[22:23], s[66:67], v[32:33] op_sel_hi:[0, 1, 1]
	v_pk_mul_f32 v[32:33], v[18:19], v[2:3] op_sel_hi:[0,1]
	v_exp_f32_e32 v32, v32
	v_exp_f32_e32 v33, v33
	v_exp_f32_e32 v34, v34
	v_exp_f32_e32 v35, v35
	v_pk_fma_f32 v[30:31], s[96:97], v[110:111], v[30:31]
	v_pk_mul_f32 v[32:33], v[32:33], v[104:105]
	v_pk_fma_f32 v[30:31], s[98:99], v[102:103], v[30:31]
	v_pk_fma_f32 v[104:105], v[22:23], s[68:69], v[32:33] op_sel_hi:[0, 1, 1]
	v_pk_mul_f32 v[32:33], v[34:35], v[98:99]
	v_pk_fma_f32 v[30:31], s[20:21], v[104:105], v[30:31]
	v_pk_fma_f32 v[98:99], v[22:23], s[70:71], v[32:33] op_sel_hi:[0, 1, 1]
	v_pk_fma_f32 v[30:31], s[22:23], v[98:99], v[30:31]
	s_nop 0
	v_add_f32_e32 v18, v30, v31
	v_fma_mix_f32 v18, v1, v19, v18 op_sel:[0,1,0] op_sel_hi:[0,1,0]
	v_fma_mixlo_f16 v18, v18, v23, 0 op_sel:[0,1,0] op_sel_hi:[0,1,0]
	ds_write_b16 v68, v18 offset:32176
	s_waitcnt lgkmcnt(0)
	s_load_dwordx16 s[56:71], s[54:55], 0xe80
	s_load_dwordx8 s[88:95], s[54:55], 0xec0
	s_load_dwordx4 s[96:99], s[54:55], 0xee0
	s_load_dwordx4 s[20:23], s[54:55], 0xef0
	v_cvt_f32_f16_e32 v18, v28
	v_pk_mul_f32 v[112:113], v[18:19], v[14:15] op_sel_hi:[0,1]
	v_exp_f32_e32 v112, v112
	v_exp_f32_e32 v113, v113
	v_pk_mul_f32 v[114:115], v[18:19], v[16:17] op_sel_hi:[0,1]
	v_exp_f32_e32 v114, v114
	v_exp_f32_e32 v115, v115
	v_fma_mix_f32 v22, v18, v20, 0 op_sel_hi:[0,1,0]
	v_pk_mul_f32 v[26:27], v[112:113], v[26:27]
	v_pk_fma_f32 v[26:27], v[22:23], s[36:37], v[26:27] op_sel_hi:[0, 1, 1]
	v_pk_fma_f32 v[62:63], s[72:73], v[26:27], 0 op_sel_hi:[1, 1, 0]
	v_pk_mul_f32 v[82:83], v[114:115], v[100:101]
	s_nop 0
	v_pk_fma_f32 v[100:101], v[22:23], s[38:39], v[82:83] op_sel_hi:[0, 1, 1]
	v_pk_mul_f32 v[64:65], v[18:19], v[10:11] op_sel_hi:[0,1]
	v_exp_f32_e32 v64, v64
	v_exp_f32_e32 v65, v65
	v_pk_mul_f32 v[82:83], v[18:19], v[12:13] op_sel_hi:[0,1]
	v_exp_f32_e32 v82, v82
	v_exp_f32_e32 v83, v83
	v_pk_mul_f32 v[64:65], v[64:65], v[106:107]
	v_pk_fma_f32 v[62:63], s[74:75], v[100:101], v[62:63]
	v_pk_fma_f32 v[106:107], v[22:23], s[40:41], v[64:65] op_sel_hi:[0, 1, 1]
	v_pk_mul_f32 v[64:65], v[82:83], v[108:109]
	v_pk_mul_f32 v[70:71], v[18:19], v[8:9] op_sel_hi:[0,1]
	v_pk_fma_f32 v[108:109], v[22:23], s[42:43], v[64:65] op_sel_hi:[0, 1, 1]
	v_pk_mul_f32 v[64:65], v[18:19], v[6:7] op_sel_hi:[0,1]
	v_exp_f32_e32 v64, v64
	v_exp_f32_e32 v65, v65
	v_exp_f32_e32 v70, v70
	v_exp_f32_e32 v71, v71
	v_pk_fma_f32 v[62:63], s[76:77], v[106:107], v[62:63]
	v_pk_mul_f32 v[64:65], v[64:65], v[110:111]
	v_pk_fma_f32 v[62:63], s[78:79], v[108:109], v[62:63]
	v_pk_fma_f32 v[110:111], v[22:23], s[44:45], v[64:65] op_sel_hi:[0, 1, 1]
	v_pk_mul_f32 v[64:65], v[70:71], v[102:103]
	v_pk_fma_f32 v[62:63], s[80:81], v[110:111], v[62:63]
	v_pk_fma_f32 v[102:103], v[22:23], s[46:47], v[64:65] op_sel_hi:[0, 1, 1]
	v_pk_mul_f32 v[64:65], v[18:19], v[2:3] op_sel_hi:[0,1]
	v_exp_f32_e32 v64, v64
	v_exp_f32_e32 v65, v65
	v_pk_mul_f32 v[18:19], v[18:19], v[4:5] op_sel_hi:[0,1]
	v_exp_f32_e32 v18, v18
	v_exp_f32_e32 v19, v19
	v_pk_mul_f32 v[64:65], v[64:65], v[104:105]
	v_pk_fma_f32 v[62:63], s[82:83], v[102:103], v[62:63]
	v_pk_fma_f32 v[104:105], v[22:23], s[48:49], v[64:65] op_sel_hi:[0, 1, 1]
	v_pk_mul_f32 v[18:19], v[18:19], v[98:99]
	v_pk_fma_f32 v[62:63], s[84:85], v[104:105], v[62:63]
	v_pk_fma_f32 v[18:19], v[22:23], s[50:51], v[18:19] op_sel_hi:[0, 1, 1]
	v_pk_fma_f32 v[22:23], s[86:87], v[18:19], v[62:63]
	s_nop 0
	v_add_f32_e32 v22, v22, v23
	v_fma_mix_f32 v22, v1, v20, v22 op_sel_hi:[0,1,0]
	v_fma_mixlo_f16 v22, v22, v24, 0 op_sel_hi:[0,1,0]
	ds_write_b16 v68, v22 offset:33216
	s_waitcnt lgkmcnt(0)
	s_load_dwordx16 s[36:51], s[54:55], 0xf00
	s_load_dwordx16 s[72:87], s[54:55], 0xf40
	v_cvt_f32_f16_sdwa v22, v28 dst_sel:DWORD dst_unused:UNUSED_PAD src0_sel:WORD_1
	v_pk_mul_f32 v[98:99], v[22:23], v[14:15] op_sel_hi:[0,1]
	v_exp_f32_e32 v98, v98
	v_exp_f32_e32 v99, v99
	v_pk_mul_f32 v[112:113], v[22:23], v[16:17] op_sel_hi:[0,1]
	v_exp_f32_e32 v112, v112
	v_exp_f32_e32 v113, v113
	v_fma_mix_f32 v28, v22, v20, 0 op_sel:[0,1,0] op_sel_hi:[0,1,0]
	v_pk_mul_f32 v[26:27], v[98:99], v[26:27]
	v_pk_fma_f32 v[26:27], v[28:29], s[56:57], v[26:27] op_sel_hi:[0, 1, 1]
	v_pk_fma_f32 v[30:31], s[88:89], v[26:27], 0 op_sel_hi:[1, 1, 0]
	v_pk_mul_f32 v[46:47], v[112:113], v[100:101]
	s_nop 0
	v_pk_fma_f32 v[98:99], v[28:29], s[58:59], v[46:47] op_sel_hi:[0, 1, 1]
	v_pk_mul_f32 v[32:33], v[22:23], v[10:11] op_sel_hi:[0,1]
	v_exp_f32_e32 v32, v32
	v_exp_f32_e32 v33, v33
	v_pk_mul_f32 v[46:47], v[22:23], v[12:13] op_sel_hi:[0,1]
	v_exp_f32_e32 v46, v46
	v_exp_f32_e32 v47, v47
	v_pk_mul_f32 v[32:33], v[32:33], v[106:107]
	v_pk_fma_f32 v[30:31], s[90:91], v[98:99], v[30:31]
	v_pk_fma_f32 v[100:101], v[28:29], s[60:61], v[32:33] op_sel_hi:[0, 1, 1]
	v_pk_mul_f32 v[32:33], v[46:47], v[108:109]
	v_pk_mul_f32 v[34:35], v[22:23], v[8:9] op_sel_hi:[0,1]
	v_pk_fma_f32 v[106:107], v[28:29], s[62:63], v[32:33] op_sel_hi:[0, 1, 1]
	v_pk_mul_f32 v[32:33], v[22:23], v[6:7] op_sel_hi:[0,1]
	v_exp_f32_e32 v32, v32
	v_exp_f32_e32 v33, v33
	v_exp_f32_e32 v34, v34
	v_exp_f32_e32 v35, v35
	v_pk_fma_f32 v[30:31], s[92:93], v[100:101], v[30:31]
	v_pk_mul_f32 v[32:33], v[32:33], v[110:111]
	v_pk_fma_f32 v[30:31], s[94:95], v[106:107], v[30:31]
	v_pk_fma_f32 v[108:109], v[28:29], s[64:65], v[32:33] op_sel_hi:[0, 1, 1]
	v_pk_mul_f32 v[32:33], v[34:35], v[102:103]
	v_pk_fma_f32 v[30:31], s[96:97], v[108:109], v[30:31]
	v_pk_fma_f32 v[102:103], v[28:29], s[66:67], v[32:33] op_sel_hi:[0, 1, 1]
	v_pk_mul_f32 v[32:33], v[22:23], v[2:3] op_sel_hi:[0,1]
	v_exp_f32_e32 v32, v32
	v_exp_f32_e32 v33, v33
	v_pk_mul_f32 v[22:23], v[22:23], v[4:5] op_sel_hi:[0,1]
	v_exp_f32_e32 v22, v22
	v_exp_f32_e32 v23, v23
	v_pk_mul_f32 v[32:33], v[32:33], v[104:105]
	v_pk_fma_f32 v[30:31], s[98:99], v[102:103], v[30:31]
	v_pk_fma_f32 v[104:105], v[28:29], s[68:69], v[32:33] op_sel_hi:[0, 1, 1]
	v_pk_mul_f32 v[18:19], v[22:23], v[18:19]
	v_pk_fma_f32 v[30:31], s[20:21], v[104:105], v[30:31]
	v_pk_fma_f32 v[18:19], v[28:29], s[70:71], v[18:19] op_sel_hi:[0, 1, 1]
	v_pk_fma_f32 v[22:23], s[22:23], v[18:19], v[30:31]
	s_nop 0
	v_add_f32_e32 v22, v22, v23
	v_fma_mix_f32 v20, v1, v20, v22 op_sel:[0,1,0] op_sel_hi:[0,1,0]
	v_fma_mixlo_f16 v20, v20, v24, 0 op_sel:[0,1,0] op_sel_hi:[0,1,0]
	ds_write_b16 v68, v20 offset:34256
	s_waitcnt lgkmcnt(0)
	s_load_dwordx16 s[56:71], s[54:55], 0xf80
	s_load_dwordx8 s[88:95], s[54:55], 0xfc0
	s_load_dwordx4 s[96:99], s[54:55], 0xfe0
	s_load_dwordx4 s[20:23], s[54:55], 0xff0
	v_cvt_f32_f16_e32 v20, v29
	v_pk_mul_f32 v[110:111], v[20:21], v[14:15] op_sel_hi:[0,1]
	v_exp_f32_e32 v110, v110
	v_exp_f32_e32 v111, v111
	v_pk_mul_f32 v[112:113], v[20:21], v[16:17] op_sel_hi:[0,1]
	v_exp_f32_e32 v112, v112
	v_exp_f32_e32 v113, v113
	v_fma_mix_f32 v22, v20, v21, 0 op_sel_hi:[0,1,0]
	v_pk_mul_f32 v[26:27], v[110:111], v[26:27]
	v_pk_fma_f32 v[26:27], v[22:23], s[36:37], v[26:27] op_sel_hi:[0, 1, 1]
	v_pk_fma_f32 v[62:63], s[72:73], v[26:27], 0 op_sel_hi:[1, 1, 0]
	v_pk_mul_f32 v[82:83], v[112:113], v[98:99]
	s_nop 0
	v_pk_fma_f32 v[64:65], v[22:23], s[38:39], v[82:83] op_sel_hi:[0, 1, 1]
	v_pk_mul_f32 v[82:83], v[20:21], v[10:11] op_sel_hi:[0,1]
	v_pk_fma_f32 v[62:63], s[74:75], v[64:65], v[62:63]
	v_exp_f32_e32 v82, v82
	v_exp_f32_e32 v83, v83
	v_pk_mul_f32 v[84:85], v[20:21], v[12:13] op_sel_hi:[0,1]
	v_exp_f32_e32 v84, v84
	v_exp_f32_e32 v85, v85
	v_pk_mul_f32 v[82:83], v[82:83], v[100:101]
	s_nop 0
	v_pk_fma_f32 v[70:71], v[22:23], s[40:41], v[82:83] op_sel_hi:[0, 1, 1]
	v_pk_mul_f32 v[82:83], v[84:85], v[106:107]
	v_pk_mul_f32 v[84:85], v[20:21], v[8:9] op_sel_hi:[0,1]
	v_pk_fma_f32 v[72:73], v[22:23], s[42:43], v[82:83] op_sel_hi:[0, 1, 1]
	v_pk_mul_f32 v[82:83], v[20:21], v[6:7] op_sel_hi:[0,1]
	v_exp_f32_e32 v82, v82
	v_exp_f32_e32 v83, v83
	v_exp_f32_e32 v84, v84
	v_exp_f32_e32 v85, v85
	v_pk_fma_f32 v[62:63], s[76:77], v[70:71], v[62:63]
	v_pk_mul_f32 v[82:83], v[82:83], v[108:109]
	v_pk_fma_f32 v[62:63], s[78:79], v[72:73], v[62:63]
	v_pk_fma_f32 v[74:75], v[22:23], s[44:45], v[82:83] op_sel_hi:[0, 1, 1]
	v_pk_mul_f32 v[82:83], v[84:85], v[102:103]
	v_pk_mul_f32 v[84:85], v[20:21], v[4:5] op_sel_hi:[0,1]
	v_pk_fma_f32 v[76:77], v[22:23], s[46:47], v[82:83] op_sel_hi:[0, 1, 1]
	v_pk_mul_f32 v[82:83], v[20:21], v[2:3] op_sel_hi:[0,1]
	v_exp_f32_e32 v82, v82
	v_exp_f32_e32 v83, v83
	v_exp_f32_e32 v84, v84
	v_exp_f32_e32 v85, v85
	v_pk_fma_f32 v[62:63], s[80:81], v[74:75], v[62:63]
	v_pk_mul_f32 v[82:83], v[82:83], v[104:105]
	v_pk_fma_f32 v[62:63], s[82:83], v[76:77], v[62:63]
	v_pk_fma_f32 v[78:79], v[22:23], s[48:49], v[82:83] op_sel_hi:[0, 1, 1]
	v_pk_mul_f32 v[18:19], v[84:85], v[18:19]
	v_pk_fma_f32 v[62:63], s[84:85], v[78:79], v[62:63]
	v_pk_fma_f32 v[18:19], v[22:23], s[50:51], v[18:19] op_sel_hi:[0, 1, 1]
	v_pk_fma_f32 v[22:23], s[86:87], v[18:19], v[62:63]
	s_nop 0
	v_add_f32_e32 v20, v22, v23
	v_fma_mix_f32 v20, v1, v21, v20 op_sel_hi:[0,1,0]
	v_fma_mixlo_f16 v20, v20, v25, 0 op_sel_hi:[0,1,0]
	ds_write_b16 v68, v20 offset:35296
	s_waitcnt lgkmcnt(0)
	v_cvt_f32_f16_sdwa v20, v29 dst_sel:DWORD dst_unused:UNUSED_PAD src0_sel:WORD_1
	v_pk_mul_f32 v[14:15], v[20:21], v[14:15] op_sel_hi:[0,1]
	v_exp_f32_e32 v14, v14
	v_exp_f32_e32 v15, v15
	v_pk_mul_f32 v[16:17], v[20:21], v[16:17] op_sel_hi:[0,1]
	v_exp_f32_e32 v16, v16
	v_exp_f32_e32 v17, v17
	v_pk_mul_f32 v[10:11], v[20:21], v[10:11] op_sel_hi:[0,1]
	v_exp_f32_e32 v10, v10
	v_exp_f32_e32 v11, v11
	v_pk_mul_f32 v[12:13], v[20:21], v[12:13] op_sel_hi:[0,1]
	v_exp_f32_e32 v12, v12
	v_exp_f32_e32 v13, v13
	v_pk_mul_f32 v[6:7], v[20:21], v[6:7] op_sel_hi:[0,1]
	v_fma_mix_f32 v22, v20, v21, 0 op_sel:[0,1,0] op_sel_hi:[0,1,0]
	v_pk_mul_f32 v[14:15], v[14:15], v[26:27]
	v_exp_f32_e32 v6, v6
	v_exp_f32_e32 v7, v7
	v_pk_mul_f32 v[8:9], v[20:21], v[8:9] op_sel_hi:[0,1]
	v_pk_fma_f32 v[14:15], v[22:23], s[56:57], v[14:15] op_sel_hi:[0, 1, 1]
	v_pk_mul_f32 v[16:17], v[16:17], v[64:65]
	v_exp_f32_e32 v8, v8
	v_exp_f32_e32 v9, v9
	v_pk_mul_f32 v[2:3], v[20:21], v[2:3] op_sel_hi:[0,1]
	v_pk_fma_f32 v[14:15], s[88:89], v[14:15], 0 op_sel_hi:[1, 1, 0]
	v_pk_fma_f32 v[16:17], v[22:23], s[58:59], v[16:17] op_sel_hi:[0, 1, 1]
	v_pk_mul_f32 v[10:11], v[10:11], v[70:71]
	v_exp_f32_e32 v2, v2
	v_exp_f32_e32 v3, v3
	v_pk_mul_f32 v[4:5], v[20:21], v[4:5] op_sel_hi:[0,1]
	v_pk_fma_f32 v[14:15], s[90:91], v[16:17], v[14:15]
	v_pk_fma_f32 v[10:11], v[22:23], s[60:61], v[10:11] op_sel_hi:[0, 1, 1]
	v_pk_mul_f32 v[12:13], v[12:13], v[72:73]
	v_exp_f32_e32 v4, v4
	v_exp_f32_e32 v5, v5
	v_pk_fma_f32 v[10:11], s[92:93], v[10:11], v[14:15]
	v_pk_fma_f32 v[12:13], v[22:23], s[62:63], v[12:13] op_sel_hi:[0, 1, 1]
	v_pk_mul_f32 v[6:7], v[6:7], v[74:75]
	v_pk_fma_f32 v[10:11], s[94:95], v[12:13], v[10:11]
	v_pk_fma_f32 v[6:7], v[22:23], s[64:65], v[6:7] op_sel_hi:[0, 1, 1]
	v_pk_mul_f32 v[8:9], v[8:9], v[76:77]
	v_pk_fma_f32 v[6:7], s[96:97], v[6:7], v[10:11]
	v_pk_fma_f32 v[8:9], v[22:23], s[66:67], v[8:9] op_sel_hi:[0, 1, 1]
	v_pk_mul_f32 v[2:3], v[2:3], v[78:79]
	v_pk_fma_f32 v[6:7], s[98:99], v[8:9], v[6:7]
	v_pk_fma_f32 v[2:3], v[22:23], s[68:69], v[2:3] op_sel_hi:[0, 1, 1]
	v_pk_mul_f32 v[4:5], v[4:5], v[18:19]
	v_pk_fma_f32 v[2:3], s[20:21], v[2:3], v[6:7]
	v_pk_fma_f32 v[4:5], v[22:23], s[70:71], v[4:5] op_sel_hi:[0, 1, 1]
	v_pk_fma_f32 v[2:3], s[22:23], v[4:5], v[2:3]
	s_nop 0
	v_add_f32_e32 v2, v2, v3
	v_fma_mix_f32 v1, v1, v21, v2 op_sel:[0,1,0] op_sel_hi:[0,1,0]
	v_fma_mixlo_f16 v1, v1, v25, 0 op_sel:[0,1,0] op_sel_hi:[0,1,0]
	ds_write_b16 v68, v1 offset:36336
	v_lshlrev_b32_e32 v1, 9, v0
	v_and_b32_e32 v2, 0x38000, v1
	v_mov_b32_e32 v3, v67
	v_and_b32_e32 v1, 63, v0
	s_bfe_u32 s14, s2, 0x40003
	v_lshl_add_u64 v[2:3], s[18:19], 0, v[2:3]
	v_lshlrev_b32_e32 v58, 4, v1
	v_mov_b32_e32 v59, v67
	s_lshl_b32 s13, s14, 6
	v_lshl_add_u64 v[20:21], v[2:3], 0, v[58:59]
	s_lshl_b32 s26, s14, 10
	s_add_i32 s12, s13, 64
	v_lshl_add_u64 v[2:3], v[20:21], 0, s[26:27]
	s_and_b32 s15, s12, 0x3c0
	v_add_co_u32_e32 v4, vcc, s52, v2
	s_lshl_b32 s26, s15, 4
	s_lshl_b32 s12, s12, 4
	v_addc_co_u32_e32 v5, vcc, 0, v3, vcc
	global_load_dwordx4 v[28:31], v[2:3], off
	global_load_dwordx4 v[32:35], v[4:5], off
	v_lshl_add_u64 v[2:3], v[20:21], 0, s[26:27]
	s_or_b32 s26, s12, 0x4000
	s_add_i32 s12, s13, 0x80
	s_and_b32 s15, s12, 0x3c0
	v_lshl_add_u64 v[4:5], v[20:21], 0, s[26:27]
	s_lshl_b32 s26, s15, 4
	s_lshl_b32 s12, s12, 4
	global_load_dwordx4 v[36:39], v[2:3], off
	global_load_dwordx4 v[40:43], v[4:5], off
	v_lshl_add_u64 v[2:3], v[20:21], 0, s[26:27]
	s_or_b32 s26, s12, 0x4000
	s_add_i32 s12, s13, 0xc0
	s_and_b32 s15, s12, 0x3c0
	v_lshl_add_u64 v[4:5], v[20:21], 0, s[26:27]
	s_lshl_b32 s26, s15, 4
	s_lshl_b32 s12, s12, 4
	global_load_dwordx4 v[44:47], v[2:3], off
	global_load_dwordx4 v[48:51], v[4:5], off
	v_lshl_add_u64 v[2:3], v[20:21], 0, s[26:27]
	s_or_b32 s26, s12, 0x4000
	s_add_i32 s12, s13, 0x100
	s_and_b32 s15, s12, 0x3c0
	v_lshl_add_u64 v[4:5], v[20:21], 0, s[26:27]
	s_lshl_b32 s26, s15, 4
	s_lshl_b32 s12, s12, 4
	global_load_dwordx4 v[52:55], v[2:3], off
	global_load_dwordx4 v[60:63], v[4:5], off
	v_lshl_add_u64 v[2:3], v[20:21], 0, s[26:27]
	s_or_b32 s26, s12, 0x4000
	s_add_i32 s12, s13, 0x140
	s_and_b32 s15, s12, 0x3c0
	v_lshl_add_u64 v[4:5], v[20:21], 0, s[26:27]
	s_lshl_b32 s26, s15, 4
	s_lshl_b32 s12, s12, 4
	global_load_dwordx4 v[68:71], v[2:3], off
	global_load_dwordx4 v[72:75], v[4:5], off
	v_lshl_add_u64 v[2:3], v[20:21], 0, s[26:27]
	s_or_b32 s26, s12, 0x4000
	s_add_i32 s12, s13, 0x180
	s_and_b32 s15, s12, 0x3c0
	v_lshl_add_u64 v[4:5], v[20:21], 0, s[26:27]
	s_lshl_b32 s26, s15, 4
	s_lshl_b32 s12, s12, 4
	global_load_dwordx4 v[76:79], v[2:3], off
	global_load_dwordx4 v[82:85], v[4:5], off
	v_lshl_add_u64 v[2:3], v[20:21], 0, s[26:27]
	s_or_b32 s26, s12, 0x4000
	s_add_i32 s12, s13, 0x1c0
	s_and_b32 s15, s12, 0x3c0
	v_lshl_add_u64 v[4:5], v[20:21], 0, s[26:27]
	s_lshl_b32 s26, s15, 4
	s_lshl_b32 s12, s12, 4
	v_lshl_add_u64 v[18:19], v[20:21], 0, s[26:27]
	s_or_b32 s26, s12, 0x4000
	s_xor_b32 s15, s13, 0x200
	v_lshl_add_u64 v[22:23], v[20:21], 0, s[26:27]
	s_lshl_b32 s26, s15, 4
	global_load_dwordx4 v[14:17], v[2:3], off
	global_load_dwordx4 v[10:13], v[4:5], off
	global_load_dwordx4 v[6:9], v[18:19], off
	s_nop 0
	global_load_dwordx4 v[2:5], v[22:23], off
	v_lshl_add_u64 v[18:19], v[20:21], 0, s[26:27]
	v_add_co_u32_e32 v22, vcc, s52, v18
	s_waitcnt lgkmcnt(0)
	s_barrier
	v_addc_co_u32_e32 v23, vcc, 0, v19, vcc
	global_load_dwordx4 v[86:89], v[18:19], off
	global_load_dwordx4 v[90:93], v[22:23], off
	v_lshrrev_b32_e32 v118, 6, v0
	v_lshlrev_b32_e32 v22, 7, v118
	v_mov_b32_e32 v23, v67
	v_and_b32_e32 v81, 15, v0
	v_lshl_add_u64 v[24:25], s[4:5], 0, v[22:23]
	v_and_b32_e32 v18, 48, v0
	v_mov_b32_e32 v19, v67
	s_movk_i32 s12, 0x410
	v_lshl_add_u64 v[56:57], v[24:25], 0, v[18:19]
	v_mad_u32_u24 v19, v81, s12, v18
	v_add_u32_e32 v23, s13, v19
	ds_read_b128 v[94:97], v23 offset:4096
	ds_read_b128 v[98:101], v23 offset:20736
	v_or_b32_e32 v26, s28, v81
	v_mov_b32_e32 v27, v67
	v_lshlrev_b64 v[24:25], 10, v[26:27]
	v_or_b32_e32 v26, 16, v26
	v_lshlrev_b64 v[26:27], 10, v[26:27]
	v_lshrrev_b32_e32 v23, 1, v0
	v_lshl_add_u64 v[24:25], v[56:57], 0, v[24:25]
	v_lshl_add_u64 v[26:27], v[56:57], 0, v[26:27]
	v_and_b32_e32 v80, 24, v23
	s_lshl_b32 s14, s14, 5
	s_setprio 1
	s_waitcnt vmcnt(17) lgkmcnt(1)
	v_mfma_f32_16x16x32_f16 v[102:105], v[28:31], v[94:97], 0
	s_waitcnt lgkmcnt(0)
	v_mfma_f32_16x16x32_f16 v[28:31], v[28:31], v[98:101], 0
	s_waitcnt vmcnt(16)
	v_mfma_f32_16x16x32_f16 v[94:97], v[32:35], v[94:97], 0
	v_mfma_f32_16x16x32_f16 v[32:35], v[32:35], v[98:101], 0
	s_setprio 0
	s_add_i32 s16, s13, 0x240
	s_and_b32 s17, s16, 0x3c0
	s_lshl_b32 s26, s17, 4
	s_lshl_b32 s16, s16, 4
	v_lshl_add_u64 v[56:57], v[20:21], 0, s[26:27]
	s_or_b32 s26, s16, 0x4000
	v_lshl_add_u64 v[64:65], v[20:21], 0, s[26:27]
	global_load_dwordx4 v[98:101], v[56:57], off
	global_load_dwordx4 v[106:109], v[64:65], off
	s_add_i32 s16, s14, 32
	s_and_b32 s16, s16, 0x1e0
	v_lshl_add_u32 v23, s16, 1, v19
	ds_read_b128 v[110:113], v23 offset:4096
	ds_read_b128 v[114:117], v23 offset:20736
	s_setprio 1
	s_waitcnt vmcnt(17) lgkmcnt(1)
	v_mfma_f32_16x16x32_f16 v[102:105], v[36:39], v[110:113], v[102:105]
	s_waitcnt lgkmcnt(0)
	v_mfma_f32_16x16x32_f16 v[28:31], v[36:39], v[114:117], v[28:31]
	s_waitcnt vmcnt(16)
	v_mfma_f32_16x16x32_f16 v[36:39], v[40:43], v[110:113], v[94:97]
	v_mfma_f32_16x16x32_f16 v[32:35], v[40:43], v[114:117], v[32:35]
	s_setprio 0
	s_add_i32 s16, s13, 0x280
	s_and_b32 s17, s16, 0x3c0
	s_lshl_b32 s26, s17, 4
	s_lshl_b32 s16, s16, 4
	v_lshl_add_u64 v[56:57], v[20:21], 0, s[26:27]
	s_or_b32 s26, s16, 0x4000
	v_lshl_add_u64 v[64:65], v[20:21], 0, s[26:27]
	global_load_dwordx4 v[40:43], v[56:57], off
	global_load_dwordx4 v[94:97], v[64:65], off
	s_add_i32 s16, s14, 64
	s_and_b32 s16, s16, 0x1e0
	v_lshl_add_u32 v23, s16, 1, v19
	ds_read_b128 v[110:113], v23 offset:4096
	ds_read_b128 v[114:117], v23 offset:20736
	s_setprio 1
	s_waitcnt vmcnt(17) lgkmcnt(1)
	v_mfma_f32_16x16x32_f16 v[102:105], v[44:47], v[110:113], v[102:105]
	s_waitcnt lgkmcnt(0)
	v_mfma_f32_16x16x32_f16 v[28:31], v[44:47], v[114:117], v[28:31]
	s_waitcnt vmcnt(16)
	v_mfma_f32_16x16x32_f16 v[36:39], v[48:51], v[110:113], v[36:39]
	v_mfma_f32_16x16x32_f16 v[32:35], v[48:51], v[114:117], v[32:35]
	s_setprio 0
	s_add_i32 s16, s13, 0x2c0
	s_and_b32 s17, s16, 0x3c0
	s_lshl_b32 s26, s17, 4
	s_lshl_b32 s16, s16, 4
	v_lshl_add_u64 v[56:57], v[20:21], 0, s[26:27]
	s_or_b32 s26, s16, 0x4000
	v_lshl_add_u64 v[64:65], v[20:21], 0, s[26:27]
	global_load_dwordx4 v[44:47], v[56:57], off
	global_load_dwordx4 v[48:51], v[64:65], off
	s_add_i32 s16, s14, 0x60
	s_and_b32 s16, s16, 0x1e0
	v_lshl_add_u32 v23, s16, 1, v19
	ds_read_b128 v[110:113], v23 offset:4096
	ds_read_b128 v[114:117], v23 offset:20736
	s_setprio 1
	s_waitcnt vmcnt(17) lgkmcnt(1)
	v_mfma_f32_16x16x32_f16 v[102:105], v[52:55], v[110:113], v[102:105]
	s_waitcnt lgkmcnt(0)
	v_mfma_f32_16x16x32_f16 v[28:31], v[52:55], v[114:117], v[28:31]
	s_waitcnt vmcnt(16)
	v_mfma_f32_16x16x32_f16 v[36:39], v[60:63], v[110:113], v[36:39]
	v_mfma_f32_16x16x32_f16 v[32:35], v[60:63], v[114:117], v[32:35]
	s_setprio 0
	s_add_i32 s16, s13, 0x300
	s_and_b32 s17, s16, 0x3c0
	s_lshl_b32 s26, s17, 4
	s_lshl_b32 s16, s16, 4
	v_lshl_add_u64 v[56:57], v[20:21], 0, s[26:27]
	s_or_b32 s26, s16, 0x4000
	v_lshl_add_u64 v[64:65], v[20:21], 0, s[26:27]
	global_load_dwordx4 v[52:55], v[56:57], off
	global_load_dwordx4 v[60:63], v[64:65], off
	s_add_i32 s16, s14, 0x80
	s_and_b32 s16, s16, 0x1e0
	v_lshl_add_u32 v23, s16, 1, v19
	ds_read_b128 v[110:113], v23 offset:4096
	ds_read_b128 v[114:117], v23 offset:20736
	s_setprio 1
	s_waitcnt vmcnt(17) lgkmcnt(1)
	v_mfma_f32_16x16x32_f16 v[102:105], v[68:71], v[110:113], v[102:105]
	s_waitcnt lgkmcnt(0)
	v_mfma_f32_16x16x32_f16 v[28:31], v[68:71], v[114:117], v[28:31]
	s_waitcnt vmcnt(16)
	v_mfma_f32_16x16x32_f16 v[36:39], v[72:75], v[110:113], v[36:39]
	v_mfma_f32_16x16x32_f16 v[32:35], v[72:75], v[114:117], v[32:35]
	s_setprio 0
	s_add_i32 s16, s13, 0x340
	s_and_b32 s17, s16, 0x3c0
	s_lshl_b32 s26, s17, 4
	s_lshl_b32 s16, s16, 4
	v_lshl_add_u64 v[56:57], v[20:21], 0, s[26:27]
	s_or_b32 s26, s16, 0x4000
	v_lshl_add_u64 v[64:65], v[20:21], 0, s[26:27]
	global_load_dwordx4 v[68:71], v[56:57], off
	global_load_dwordx4 v[72:75], v[64:65], off
	s_add_i32 s16, s14, 0xa0
	s_and_b32 s16, s16, 0x1e0
	v_lshl_add_u32 v23, s16, 1, v19
	ds_read_b128 v[110:113], v23 offset:4096
	ds_read_b128 v[114:117], v23 offset:20736
	s_setprio 1
	s_waitcnt vmcnt(17) lgkmcnt(1)
	v_mfma_f32_16x16x32_f16 v[102:105], v[76:79], v[110:113], v[102:105]
	s_waitcnt lgkmcnt(0)
	v_mfma_f32_16x16x32_f16 v[28:31], v[76:79], v[114:117], v[28:31]
	s_waitcnt vmcnt(16)
	v_mfma_f32_16x16x32_f16 v[36:39], v[82:85], v[110:113], v[36:39]
	v_mfma_f32_16x16x32_f16 v[32:35], v[82:85], v[114:117], v[32:35]
	s_setprio 0
	s_add_i32 s16, s13, 0x380
	s_and_b32 s17, s16, 0x3c0
	s_lshl_b32 s26, s17, 4
	s_lshl_b32 s16, s16, 4
	v_lshl_add_u64 v[56:57], v[20:21], 0, s[26:27]
	s_or_b32 s26, s16, 0x4000
	v_lshl_add_u64 v[64:65], v[20:21], 0, s[26:27]
	global_load_dwordx4 v[76:79], v[56:57], off
	global_load_dwordx4 v[82:85], v[64:65], off
	s_add_i32 s16, s14, 0xc0
	s_and_b32 s16, s16, 0x1e0
	v_lshl_add_u32 v23, s16, 1, v19
	ds_read_b128 v[110:113], v23 offset:4096
	ds_read_b128 v[114:117], v23 offset:20736
	s_setprio 1
	s_waitcnt vmcnt(17) lgkmcnt(1)
	v_mfma_f32_16x16x32_f16 v[102:105], v[14:17], v[110:113], v[102:105]
	s_waitcnt lgkmcnt(0)
	v_mfma_f32_16x16x32_f16 v[14:17], v[14:17], v[114:117], v[28:31]
	s_waitcnt vmcnt(16)
	v_mfma_f32_16x16x32_f16 v[28:31], v[10:13], v[110:113], v[36:39]
	v_mfma_f32_16x16x32_f16 v[10:13], v[10:13], v[114:117], v[32:35]
	s_setprio 0
	s_addk_i32 s13, 0x3c0
	s_and_b32 s16, s13, 0x3c0
	s_lshl_b32 s26, s16, 4
	s_lshl_b32 s13, s13, 4
	v_lshl_add_u64 v[56:57], v[20:21], 0, s[26:27]
	s_or_b32 s26, s13, 0x4000
	v_lshl_add_u64 v[20:21], v[20:21], 0, s[26:27]
	global_load_dwordx4 v[32:35], v[56:57], off
	global_load_dwordx4 v[36:39], v[20:21], off
	s_add_i32 s13, s14, 0xe0
	s_and_b32 s13, s13, 0x1e0
	v_lshl_add_u32 v20, s13, 1, v19
	ds_read_b128 v[110:113], v20 offset:4096
	ds_read_b128 v[114:117], v20 offset:20736
	s_setprio 1
	s_waitcnt vmcnt(17) lgkmcnt(1)
	v_mfma_f32_16x16x32_f16 v[102:105], v[6:9], v[110:113], v[102:105]
	s_waitcnt lgkmcnt(0)
	v_mfma_f32_16x16x32_f16 v[6:9], v[6:9], v[114:117], v[14:17]
	s_waitcnt vmcnt(16)
	v_mfma_f32_16x16x32_f16 v[14:17], v[2:5], v[110:113], v[28:31]
	v_mfma_f32_16x16x32_f16 v[2:5], v[2:5], v[114:117], v[10:13]
	s_setprio 0
	v_add_u32_e32 v20, s15, v19
	s_nop 0
	ds_read_b128 v[10:13], v20 offset:4096
	ds_read_b128 v[28:31], v20 offset:20736
	s_setprio 1
	s_waitcnt vmcnt(15) lgkmcnt(1)
	v_mfma_f32_16x16x32_f16 v[102:105], v[86:89], v[10:13], v[102:105]
	s_waitcnt lgkmcnt(0)
	v_mfma_f32_16x16x32_f16 v[6:9], v[86:89], v[28:31], v[6:9]
	s_waitcnt vmcnt(14)
	v_mfma_f32_16x16x32_f16 v[10:13], v[90:93], v[10:13], v[14:17]
	v_mfma_f32_16x16x32_f16 v[2:5], v[90:93], v[28:31], v[2:5]
	s_setprio 0
	s_add_i32 s13, s14, 0x120
	s_and_b32 s13, s13, 0x1e0
	v_lshl_add_u32 v20, s13, 1, v19
	ds_read_b128 v[14:17], v20 offset:4096
	ds_read_b128 v[28:31], v20 offset:20736
	s_setprio 1
	s_waitcnt vmcnt(13) lgkmcnt(1)
	v_mfma_f32_16x16x32_f16 v[86:89], v[98:101], v[14:17], v[102:105]
	s_waitcnt lgkmcnt(0)
	v_mfma_f32_16x16x32_f16 v[6:9], v[98:101], v[28:31], v[6:9]
	s_waitcnt vmcnt(12)
	v_mfma_f32_16x16x32_f16 v[10:13], v[106:109], v[14:17], v[10:13]
	v_mfma_f32_16x16x32_f16 v[2:5], v[106:109], v[28:31], v[2:5]
	s_setprio 0
	s_add_i32 s13, s14, 0x140
	s_and_b32 s13, s13, 0x1e0
	v_lshl_add_u32 v20, s13, 1, v19
	ds_read_b128 v[14:17], v20 offset:4096
	ds_read_b128 v[28:31], v20 offset:20736
	s_setprio 1
	s_waitcnt vmcnt(11) lgkmcnt(1)
	v_mfma_f32_16x16x32_f16 v[86:89], v[40:43], v[14:17], v[86:89]
	s_waitcnt lgkmcnt(0)
	v_mfma_f32_16x16x32_f16 v[6:9], v[40:43], v[28:31], v[6:9]
	s_waitcnt vmcnt(10)
	v_mfma_f32_16x16x32_f16 v[10:13], v[94:97], v[14:17], v[10:13]
	v_mfma_f32_16x16x32_f16 v[2:5], v[94:97], v[28:31], v[2:5]
	s_setprio 0
	s_add_i32 s13, s14, 0x160
	s_and_b32 s13, s13, 0x1e0
	v_lshl_add_u32 v20, s13, 1, v19
	ds_read_b128 v[14:17], v20 offset:4096
	ds_read_b128 v[28:31], v20 offset:20736
	s_setprio 1
	s_waitcnt vmcnt(9) lgkmcnt(1)
	v_mfma_f32_16x16x32_f16 v[40:43], v[44:47], v[14:17], v[86:89]
	s_waitcnt lgkmcnt(0)
	v_mfma_f32_16x16x32_f16 v[6:9], v[44:47], v[28:31], v[6:9]
	s_waitcnt vmcnt(8)
	v_mfma_f32_16x16x32_f16 v[10:13], v[48:51], v[14:17], v[10:13]
	v_mfma_f32_16x16x32_f16 v[2:5], v[48:51], v[28:31], v[2:5]
	s_setprio 0
	s_add_i32 s13, s14, 0x180
	s_and_b32 s13, s13, 0x1e0
	v_lshl_add_u32 v20, s13, 1, v19
	ds_read_b128 v[14:17], v20 offset:4096
	ds_read_b128 v[28:31], v20 offset:20736
	s_setprio 1
	s_waitcnt vmcnt(7) lgkmcnt(1)
	v_mfma_f32_16x16x32_f16 v[40:43], v[52:55], v[14:17], v[40:43]
	s_waitcnt lgkmcnt(0)
	v_mfma_f32_16x16x32_f16 v[6:9], v[52:55], v[28:31], v[6:9]
	s_waitcnt vmcnt(6)
	v_mfma_f32_16x16x32_f16 v[10:13], v[60:63], v[14:17], v[10:13]
	v_mfma_f32_16x16x32_f16 v[2:5], v[60:63], v[28:31], v[2:5]
	s_setprio 0
	s_add_i32 s13, s14, 0x1a0
	s_and_b32 s13, s13, 0x1e0
	v_lshl_add_u32 v20, s13, 1, v19
	ds_read_b128 v[14:17], v20 offset:4096
	ds_read_b128 v[28:31], v20 offset:20736
	s_setprio 1
	s_waitcnt vmcnt(5) lgkmcnt(1)
	v_mfma_f32_16x16x32_f16 v[40:43], v[68:71], v[14:17], v[40:43]
	s_waitcnt lgkmcnt(0)
	v_mfma_f32_16x16x32_f16 v[6:9], v[68:71], v[28:31], v[6:9]
	s_waitcnt vmcnt(4)
	v_mfma_f32_16x16x32_f16 v[10:13], v[72:75], v[14:17], v[10:13]
	v_mfma_f32_16x16x32_f16 v[2:5], v[72:75], v[28:31], v[2:5]
	s_setprio 0
	s_add_i32 s13, s14, 0x1c0
	s_and_b32 s13, s13, 0x1e0
	v_lshl_add_u32 v20, s13, 1, v19
	ds_read_b128 v[14:17], v20 offset:4096
	ds_read_b128 v[28:31], v20 offset:20736
	s_setprio 1
	s_waitcnt vmcnt(3) lgkmcnt(1)
	v_mfma_f32_16x16x32_f16 v[40:43], v[76:79], v[14:17], v[40:43]
	s_waitcnt lgkmcnt(0)
	v_mfma_f32_16x16x32_f16 v[6:9], v[76:79], v[28:31], v[6:9]
	s_waitcnt vmcnt(2)
	v_mfma_f32_16x16x32_f16 v[10:13], v[82:85], v[14:17], v[10:13]
	v_mfma_f32_16x16x32_f16 v[2:5], v[82:85], v[28:31], v[2:5]
	s_setprio 0
	s_addk_i32 s14, 0x1e0
	s_and_b32 s13, s14, 0x1e0
	v_lshl_add_u32 v20, s13, 1, v19
	ds_read_b128 v[14:17], v20 offset:4096
	ds_read_b128 v[28:31], v20 offset:20736
	s_setprio 1
	s_waitcnt vmcnt(1) lgkmcnt(1)
	v_mfma_f32_16x16x32_f16 v[40:43], v[32:35], v[14:17], v[40:43]
	s_waitcnt lgkmcnt(0)
	v_mfma_f32_16x16x32_f16 v[6:9], v[32:35], v[28:31], v[6:9]
	s_waitcnt vmcnt(0)
	v_mfma_f32_16x16x32_f16 v[10:13], v[36:39], v[14:17], v[10:13]
	v_mfma_f32_16x16x32_f16 v[2:5], v[36:39], v[28:31], v[2:5]
	s_setprio 0
	v_add_u32_e32 v19, v19, v22
	v_lshlrev_b32_e32 v20, 15, v118
	v_mov_b32_e32 v21, v67
	s_bfe_u32 s22, s2, 0x30003
	v_lshl_add_u64 v[20:21], s[10:11], 0, v[20:21]
	s_lshl_b32 s26, s22, 10
	v_lshl_add_u64 v[64:65], v[20:21], 0, v[58:59]
	v_lshl_add_u64 v[52:53], v[64:65], 0, s[26:27]
	v_add_co_u32_e32 v76, vcc, s29, v52
	s_lshl_b32 s53, s22, 6
	s_nop 0
	v_addc_co_u32_e32 v77, vcc, 0, v53, vcc
	s_mov_b32 s14, 0x14000
	v_mov_b32_e32 v22, 0x14000
	v_mul_u32_u24_e32 v23, 0x210, v81
	s_add_i32 s38, s53, 64
	v_lshlrev_b32_e32 v83, 2, v118
	s_movk_i32 s16, 0x1040
	s_movk_i32 s18, 0x840
	v_lshl_or_b32 v1, v1, 3, v22
	v_add3_u32 v84, v23, v18, s14
	s_and_b32 s14, s38, 0x1c0
	s_movk_i32 s20, 0x210
	s_mov_b32 s19, s27
	v_mad_u32_u24 v56, v118, s16, v58
	v_or_b32_e32 v22, 1, v83
	v_mad_u32_u24 v98, v118, s18, v1
	s_lshl_b32 s18, s14, 4
	v_mad_u32_u24 v99, v22, s12, v58
	v_mad_u32_u24 v85, v22, s20, v1
	v_lshl_add_u64 v[54:55], v[64:65], 0, s[18:19]
	s_add_i32 s12, s53, 0xc0
	s_and_b32 s2, s3, 0x7ffffff
	s_lshl_b32 s3, s22, 5
	s_and_b32 s39, s12, 0x1c0
	s_lshl_b32 s14, s39, 4
	s_add_i32 s39, s3, 32
	s_and_b32 s39, s39, 0xe0
	v_lshl_add_u32 v82, s39, 1, v84
	s_add_i32 s11, s53, 0x80
	s_lshl_b32 s16, s38, 4
	s_mov_b32 s21, s27
	s_and_b32 s30, s11, 0x1c0
	s_lshl_b32 s11, s11, 4
	s_or_b32 s20, s16, 0x2000
	s_mov_b32 s23, s27
	s_mov_b32 s31, s27
	s_mov_b32 s35, s27
	s_or_b32 s22, s16, 0x6000
	s_lshl_b32 s30, s30, 4
	s_or_b32 s34, s11, 0x2000
	v_lshl_add_u64 v[26:27], v[64:65], 0, s[20:21]
	v_lshl_add_u64 v[28:29], v[64:65], 0, s[22:23]
	v_lshl_add_u64 v[30:31], v[64:65], 0, s[30:31]
	v_lshl_add_u64 v[32:33], v[64:65], 0, s[34:35]
	s_mov_b64 s[40:41], 0x40000
	v_lshl_add_u64 v[60:61], v[64:65], 0, s[40:41]
	s_mov_b32 s37, s27
	s_or_b32 s36, s11, 0x6000
	v_lshl_add_u64 v[74:75], v[64:65], 0, s[36:37]
	s_mov_b32 s15, s27
	s_lshl_b32 s12, s12, 4
	v_lshl_add_u64 v[70:71], v[64:65], 0, s[14:15]
	s_mov_b32 s17, s27
	s_or_b32 s16, s12, 0x2000
	s_mov_b32 s13, s27
	s_or_b32 s12, s12, 0x6000
	v_lshl_add_u64 v[72:73], v[64:65], 0, s[16:17]
	v_lshl_add_u64 v[68:69], v[64:65], 0, s[12:13]
	v_add_u32_e32 v1, s53, v84
	s_xor_b32 s10, s26, 0x1000
	s_mov_b32 s11, s27
	s_mov_b32 s49, s27
	s_mov_b32 s51, s27
	s_mov_b32 s47, s27
	v_pk_add_f32 v[14:15], v[180:181], v[40:41]
	v_pk_add_f32 v[16:17], v[182:183], v[42:43]
	v_pk_add_f32 v[10:11], v[184:185], v[10:11]
	v_pk_add_f32 v[12:13], v[186:187], v[12:13]
	v_pk_add_f32 v[6:7], v[188:189], v[6:7]
	v_pk_add_f32 v[8:9], v[190:191], v[8:9]
	v_pk_add_f32 v[2:3], v[192:193], v[2:3]
	v_pk_add_f32 v[4:5], v[194:195], v[4:5]
	ds_write_b128 v19, v[14:17] offset:37376
	ds_write_b128 v19, v[10:13] offset:37440
	ds_write_b128 v19, v[6:9] offset:54016
	ds_write_b128 v19, v[2:5] offset:54080
	v_mov_b64_e32 v[34:35], v[204:205]
	v_mov_b64_e32 v[36:37], v[206:207]
	v_mov_b64_e32 v[38:39], v[208:209]
	v_mov_b64_e32 v[40:41], v[210:211]
	v_add_co_u32_e32 v2, vcc, s52, v52
	s_waitcnt lgkmcnt(0)
	s_nop 0
	v_addc_co_u32_e32 v3, vcc, 0, v53, vcc
	v_add_co_u32_e32 v4, vcc, s33, v52
	s_barrier
	s_nop 0
	v_addc_co_u32_e32 v5, vcc, 0, v53, vcc
	global_load_dwordx4 v[14:17], v[2:3], off
	global_load_dwordx4 v[18:21], v[4:5], off
	global_load_dwordx4 v[22:25], v[52:53], off
	global_load_dwordx4 v[10:13], v[54:55], off
	ds_read_b128 v[2:5], v56 offset:37376
	ds_read_b128 v[6:9], v99 offset:37376
	v_add_co_u32_e32 v78, vcc, s52, v54
	s_mov_b32 s43, s27
	s_waitcnt lgkmcnt(1)
	v_add_f32_e32 v42, v2, v3
	v_add_f32_e32 v42, v42, v4
	v_add_f32_e32 v42, v42, v5
	v_addc_co_u32_e32 v79, vcc, 0, v55, vcc
	s_nop 0
	v_add_f32_dpp v42, v42, v42 quad_perm:[1,0,3,2] row_mask:0xf bank_mask:0xf bound_ctrl:1
	s_mov_b32 s45, s27
	s_mov_b32 s41, s27
	v_add_f32_dpp v42, v42, v42 quad_perm:[2,3,0,1] row_mask:0xf bank_mask:0xf bound_ctrl:1
	v_lshl_add_u64 v[62:63], v[64:65], 0, s[10:11]
	v_lshl_add_u64 v[58:59], s[4:5], 0, v[58:59]
	v_add_f32_dpp v42, v42, v42 row_half_mirror row_mask:0xf bank_mask:0xf bound_ctrl:1
	v_lshl_add_u64 v[152:153], v[60:61], 0, s[26:27]
	v_lshl_add_u64 v[154:155], v[60:61], 0, s[18:19]
	v_add_f32_dpp v42, v42, v42 row_mirror row_mask:0xf bank_mask:0xf bound_ctrl:1
	v_lshl_add_u64 v[156:157], v[60:61], 0, s[20:21]
	v_readlane_b32 s8, v42, 16
	v_readlane_b32 s9, v42, 48
	v_readlane_b32 s6, v42, 0
	v_readlane_b32 s7, v42, 32
	v_mov_b32_e32 v42, s8
	v_mov_b32_e32 v43, s9
	v_pk_add_f32 v[42:43], s[6:7], v[42:43]
	s_mov_b32 s6, 0x3b800000
	v_add_f32_e32 v42, v42, v43
	v_mul_f32_e32 v42, 0x3b800000, v42
	v_pk_add_f32 v[86:87], v[2:3], v[42:43] op_sel_hi:[1,0] neg_lo:[0,1] neg_hi:[0,1]
	v_pk_add_f32 v[88:89], v[4:5], v[42:43] op_sel_hi:[1,0] neg_lo:[0,1] neg_hi:[0,1]
	v_pk_mul_f32 v[42:43], v[86:87], v[86:87]
	v_pk_mul_f32 v[44:45], v[88:89], v[88:89]
	v_add_f32_e32 v42, v42, v43
	v_add_f32_e32 v42, v44, v42
	s_waitcnt lgkmcnt(0)
	v_add_f32_e32 v44, v6, v7
	v_add_f32_e32 v42, v45, v42
	v_add_f32_e32 v44, v44, v8
	v_add_f32_e32 v44, v44, v9
	v_add_f32_dpp v42, v42, v42 quad_perm:[1,0,3,2] row_mask:0xf bank_mask:0xf bound_ctrl:1
	v_lshl_add_u64 v[158:159], v[60:61], 0, s[22:23]
	v_add_f32_dpp v44, v44, v44 quad_perm:[1,0,3,2] row_mask:0xf bank_mask:0xf bound_ctrl:1
	v_add_f32_dpp v42, v42, v42 quad_perm:[2,3,0,1] row_mask:0xf bank_mask:0xf bound_ctrl:1
	v_lshl_add_u64 v[160:161], v[60:61], 0, s[30:31]
	v_add_f32_dpp v44, v44, v44 quad_perm:[2,3,0,1] row_mask:0xf bank_mask:0xf bound_ctrl:1
	v_add_f32_dpp v42, v42, v42 row_half_mirror row_mask:0xf bank_mask:0xf bound_ctrl:1
	v_lshl_add_u64 v[162:163], v[60:61], 0, s[34:35]
	v_add_f32_dpp v44, v44, v44 row_half_mirror row_mask:0xf bank_mask:0xf bound_ctrl:1
	v_add_f32_dpp v42, v42, v42 row_mirror row_mask:0xf bank_mask:0xf bound_ctrl:1
	v_lshl_add_u64 v[164:165], v[60:61], 0, s[36:37]
	v_readlane_b32 s7, v42, 16
	v_readlane_b32 s39, v42, 48
	v_add_f32_dpp v44, v44, v44 row_mirror row_mask:0xf bank_mask:0xf bound_ctrl:1
	v_readlane_b32 s8, v42, 0
	v_readlane_b32 s9, v42, 32
	v_mov_b32_e32 v42, s7
	v_mov_b32_e32 v43, s39
	v_readlane_b32 s7, v44, 16
	v_readlane_b32 s39, v44, 48
	v_pk_add_f32 v[42:43], s[8:9], v[42:43]
	v_readlane_b32 s8, v44, 0
	v_readlane_b32 s9, v44, 32
	v_mov_b32_e32 v44, s7
	v_mov_b32_e32 v45, s39
	v_pk_add_f32 v[44:45], s[8:9], v[44:45]
	s_nop 0
	v_add_f32_e32 v44, v44, v45
	v_mul_f32_e32 v44, 0x3b800000, v44
	v_pk_add_f32 v[90:91], v[6:7], v[44:45] op_sel_hi:[1,0] neg_lo:[0,1] neg_hi:[0,1]
	v_pk_add_f32 v[92:93], v[8:9], v[44:45] op_sel_hi:[1,0] neg_lo:[0,1] neg_hi:[0,1]
	v_pk_mul_f32 v[46:47], v[90:91], v[90:91]
	v_pk_mul_f32 v[44:45], v[92:93], v[92:93]
	v_add_f32_e32 v46, v46, v47
	v_add_f32_e32 v44, v44, v46
	v_add_f32_e32 v44, v45, v44
	v_mov_b32_e32 v47, v42
	s_nop 0
	v_add_f32_dpp v44, v44, v44 quad_perm:[1,0,3,2] row_mask:0xf bank_mask:0xf bound_ctrl:1
	s_nop 1
	v_add_f32_dpp v44, v44, v44 quad_perm:[2,3,0,1] row_mask:0xf bank_mask:0xf bound_ctrl:1
	s_nop 1
	v_add_f32_dpp v44, v44, v44 row_half_mirror row_mask:0xf bank_mask:0xf bound_ctrl:1
	s_nop 1
	v_add_f32_dpp v44, v44, v44 row_mirror row_mask:0xf bank_mask:0xf bound_ctrl:1
	s_nop 0
	v_readlane_b32 s7, v44, 16
	v_readlane_b32 s39, v44, 48
	v_readlane_b32 s8, v44, 0
	v_readlane_b32 s9, v44, 32
	v_mov_b32_e32 v44, s7
	v_mov_b32_e32 v45, s39
	v_pk_add_f32 v[44:45], s[8:9], v[44:45]
	s_mov_b32 s8, 0x3727c5ac
	v_mov_b32_e32 v46, v44
	v_mov_b32_e32 v42, v45
	v_pk_add_f32 v[42:43], v[46:47], v[42:43]
	v_mov_b64_e32 v[94:95], s[8:9]
	v_pk_fma_f32 v[96:97], v[42:43], s[6:7], v[94:95] op_sel_hi:[1,0,0]
	s_mov_b32 s7, 0x800000
	v_mul_f32_e32 v42, 0x4b800000, v97
	v_cmp_gt_f32_e32 vcc, s7, v97
	s_nop 1
	v_cndmask_b32_e32 v42, v97, v42, vcc
	v_rsq_f32_e32 v97, v42
	global_load_dwordx4 v[54:57], v[26:27], off
	global_load_dwordx4 v[50:53], v[28:29], off
	global_load_dwordx4 v[46:49], v[30:31], off
	global_load_dwordx4 v[42:45], v[32:33], off
	v_mul_f32_e32 v26, 0x45800000, v97
	v_cndmask_b32_e32 v26, v97, v26, vcc
	v_pk_mul_f32 v[28:29], v[86:87], v[26:27] op_sel_hi:[1,0]
	v_cmp_gt_f32_e32 vcc, s7, v96
	s_waitcnt vmcnt(8)
	v_pk_fma_f32 v[28:29], v[34:35], v[28:29], v[38:39]
	v_pk_mul_f32 v[26:27], v[88:89], v[26:27] op_sel_hi:[1,0]
	v_cvt_pk_f16_f32 v28, v28, v29
	v_mul_f32_e32 v29, 0x4b800000, v96
	v_cndmask_b32_e32 v29, v96, v29, vcc
	v_rsq_f32_e32 v32, v29
	v_pk_fma_f32 v[26:27], v[36:37], v[26:27], v[40:41]
	s_nop 0
	v_cvt_pk_f16_f32 v29, v26, v27
	v_mul_f32_e32 v26, 0x45800000, v32
	v_cndmask_b32_e32 v26, v32, v26, vcc
	ds_write_b64 v98, v[28:29]
	v_pk_mul_f32 v[28:29], v[90:91], v[26:27] op_sel_hi:[1,0]
	v_pk_mul_f32 v[26:27], v[92:93], v[26:27] op_sel_hi:[1,0]
	v_pk_fma_f32 v[28:29], v[34:35], v[28:29], v[38:39]
	v_pk_fma_f32 v[26:27], v[36:37], v[26:27], v[40:41]
	v_cvt_pk_f16_f32 v28, v28, v29
	v_cvt_pk_f16_f32 v29, v26, v27
	ds_write_b64 v85, v[28:29]
	ds_read_b128 v[26:29], v99 offset:38416
	v_add_co_u32_e32 v102, vcc, s52, v30
	s_nop 1
	v_addc_co_u32_e32 v103, vcc, 0, v31, vcc
	ds_read_b128 v[30:33], v99 offset:39456
	s_waitcnt lgkmcnt(1)
	v_add_f32_e32 v86, v26, v27
	v_add_f32_e32 v86, v86, v28
	v_add_f32_e32 v86, v86, v29
	s_nop 1
	v_add_f32_dpp v86, v86, v86 quad_perm:[1,0,3,2] row_mask:0xf bank_mask:0xf bound_ctrl:1
	s_nop 1
	v_add_f32_dpp v86, v86, v86 quad_perm:[2,3,0,1] row_mask:0xf bank_mask:0xf bound_ctrl:1
	s_nop 1
	v_add_f32_dpp v86, v86, v86 row_half_mirror row_mask:0xf bank_mask:0xf bound_ctrl:1
	s_nop 1
	v_add_f32_dpp v86, v86, v86 row_mirror row_mask:0xf bank_mask:0xf bound_ctrl:1
	s_nop 0
	v_readlane_b32 s39, v86, 16
	v_readlane_b32 s40, v86, 48
	v_readlane_b32 s8, v86, 0
	v_readlane_b32 s9, v86, 32
	v_mov_b32_e32 v86, s39
	v_mov_b32_e32 v87, s40
	v_pk_add_f32 v[86:87], s[8:9], v[86:87]
	s_nop 0
	v_add_f32_e32 v86, v86, v87
	v_mul_f32_e32 v86, 0x3b800000, v86
	v_pk_add_f32 v[104:105], v[26:27], v[86:87] op_sel_hi:[1,0] neg_lo:[0,1] neg_hi:[0,1]
	v_pk_add_f32 v[106:107], v[28:29], v[86:87] op_sel_hi:[1,0] neg_lo:[0,1] neg_hi:[0,1]
	v_pk_mul_f32 v[88:89], v[104:105], v[104:105]
	v_pk_mul_f32 v[86:87], v[106:107], v[106:107]
	v_add_f32_e32 v88, v88, v89
	v_add_f32_e32 v86, v86, v88
	s_waitcnt lgkmcnt(0)
	v_add_f32_e32 v88, v30, v31
	v_add_f32_e32 v86, v87, v86
	v_add_f32_e32 v88, v88, v32
	v_add_f32_e32 v88, v88, v33
	v_add_f32_dpp v86, v86, v86 quad_perm:[1,0,3,2] row_mask:0xf bank_mask:0xf bound_ctrl:1
	s_nop 0
	v_add_f32_dpp v88, v88, v88 quad_perm:[1,0,3,2] row_mask:0xf bank_mask:0xf bound_ctrl:1
	v_add_f32_dpp v86, v86, v86 quad_perm:[2,3,0,1] row_mask:0xf bank_mask:0xf bound_ctrl:1
	s_nop 0
	v_add_f32_dpp v88, v88, v88 quad_perm:[2,3,0,1] row_mask:0xf bank_mask:0xf bound_ctrl:1
	v_add_f32_dpp v86, v86, v86 row_half_mirror row_mask:0xf bank_mask:0xf bound_ctrl:1
	s_nop 0
	v_add_f32_dpp v88, v88, v88 row_half_mirror row_mask:0xf bank_mask:0xf bound_ctrl:1
	v_add_f32_dpp v86, v86, v86 row_mirror row_mask:0xf bank_mask:0xf bound_ctrl:1
	s_nop 0
	v_readlane_b32 s39, v86, 16
	v_readlane_b32 s40, v86, 48
	v_add_f32_dpp v88, v88, v88 row_mirror row_mask:0xf bank_mask:0xf bound_ctrl:1
	v_readlane_b32 s8, v86, 0
	v_readlane_b32 s9, v86, 32
	v_mov_b32_e32 v86, s39
	v_mov_b32_e32 v87, s40
	v_readlane_b32 s39, v88, 16
	v_readlane_b32 s40, v88, 48
	v_pk_add_f32 v[86:87], s[8:9], v[86:87]
	v_readlane_b32 s8, v88, 0
	v_readlane_b32 s9, v88, 32
	v_mov_b32_e32 v88, s39
	v_mov_b32_e32 v89, s40
	v_pk_add_f32 v[88:89], s[8:9], v[88:89]
	s_nop 0
	v_add_f32_e32 v88, v88, v89
	v_mul_f32_e32 v88, 0x3b800000, v88
	v_pk_add_f32 v[108:109], v[30:31], v[88:89] op_sel_hi:[1,0] neg_lo:[0,1] neg_hi:[0,1]
	v_pk_add_f32 v[110:111], v[32:33], v[88:89] op_sel_hi:[1,0] neg_lo:[0,1] neg_hi:[0,1]
	v_pk_mul_f32 v[90:91], v[108:109], v[108:109]
	v_pk_mul_f32 v[88:89], v[110:111], v[110:111]
	v_add_f32_e32 v90, v90, v91
	v_add_f32_e32 v88, v88, v90
	v_add_f32_e32 v88, v89, v88
	v_mov_b32_e32 v91, v86
	s_nop 0
	v_add_f32_dpp v88, v88, v88 quad_perm:[1,0,3,2] row_mask:0xf bank_mask:0xf bound_ctrl:1
	s_nop 1
	v_add_f32_dpp v88, v88, v88 quad_perm:[2,3,0,1] row_mask:0xf bank_mask:0xf bound_ctrl:1
	s_nop 1
	v_add_f32_dpp v88, v88, v88 row_half_mirror row_mask:0xf bank_mask:0xf bound_ctrl:1
	s_nop 1
	v_add_f32_dpp v88, v88, v88 row_mirror row_mask:0xf bank_mask:0xf bound_ctrl:1
	s_nop 0
	v_readlane_b32 s39, v88, 16
	v_readlane_b32 s40, v88, 48
	v_readlane_b32 s8, v88, 0
	v_readlane_b32 s9, v88, 32
	v_mov_b32_e32 v88, s39
	v_mov_b32_e32 v89, s40
	v_pk_add_f32 v[88:89], s[8:9], v[88:89]
	s_mov_b32 s9, s27
	v_mov_b32_e32 v90, v88
	v_mov_b32_e32 v86, v89
	v_pk_add_f32 v[86:87], v[90:91], v[86:87]
	s_mov_b32 s39, s27
	v_pk_fma_f32 v[112:113], v[86:87], s[6:7], v[94:95] op_sel_hi:[1,0,0]
	s_add_i32 s6, s53, 0x140
	v_mul_f32_e32 v86, 0x4b800000, v113
	v_cmp_gt_f32_e32 vcc, s7, v113
	s_nop 1
	v_cndmask_b32_e32 v86, v113, v86, vcc
	v_rsq_f32_e32 v113, v86
	global_load_dwordx4 v[86:89], v[78:79], off
	global_load_dwordx4 v[90:93], v[102:103], off
	global_load_dwordx4 v[94:97], v[76:77], off
	global_load_dwordx4 v[98:101], v[74:75], off
	v_mul_f32_e32 v74, 0x45800000, v113
	v_cndmask_b32_e32 v74, v113, v74, vcc
	v_pk_mul_f32 v[76:77], v[104:105], v[74:75] op_sel_hi:[1,0]
	v_mul_f32_e32 v75, 0x4b800000, v112
	v_cmp_gt_f32_e32 vcc, s7, v112
	v_pk_fma_f32 v[76:77], v[34:35], v[76:77], v[38:39]
	s_and_b32 s7, s6, 0x1c0
	v_cndmask_b32_e32 v75, v112, v75, vcc
	v_rsq_f32_e32 v78, v75
	v_pk_mul_f32 v[74:75], v[106:107], v[74:75] op_sel_hi:[1,0]
	v_cvt_pk_f16_f32 v76, v76, v77
	v_pk_fma_f32 v[74:75], v[36:37], v[74:75], v[40:41]
	s_lshl_b32 s6, s6, 4
	v_cvt_pk_f16_f32 v77, v74, v75
	v_mul_f32_e32 v74, 0x45800000, v78
	v_cndmask_b32_e32 v74, v78, v74, vcc
	v_pk_mul_f32 v[78:79], v[108:109], v[74:75] op_sel_hi:[1,0]
	s_or_b32 s50, s6, 0x2000
	v_pk_fma_f32 v[34:35], v[34:35], v[78:79], v[38:39]
	v_pk_mul_f32 v[38:39], v[110:111], v[74:75] op_sel_hi:[1,0]
	v_add_co_u32_e32 v78, vcc, s52, v70
	v_pk_fma_f32 v[36:37], v[36:37], v[38:39], v[40:41]
	v_cvt_pk_f16_f32 v34, v34, v35
	v_cvt_pk_f16_f32 v35, v36, v37
	v_addc_co_u32_e32 v79, vcc, 0, v71, vcc
	ds_write2_b64 v85, v[76:77], v[34:35] offset0:66 offset1:132
	s_waitcnt lgkmcnt(0)
	s_barrier
	global_load_dwordx4 v[34:37], v[70:71], off
	global_load_dwordx4 v[38:41], v[72:73], off
	s_nop 0
	global_load_dwordx4 v[70:73], v[78:79], off
	global_load_dwordx4 v[74:77], v[68:69], off
	s_or_b32 s46, s6, 0x6000
	s_sub_i32 s6, s38, s3
	s_and_b32 s6, s6, 0xe0
	v_lshl_add_u32 v172, s6, 1, v84
	s_add_i32 s6, s53, 0x180
	s_lshl_b32 s48, s7, 4
	s_and_b32 s7, s6, 0x1c0
	s_lshl_b32 s6, s6, 4
	s_or_b32 s44, s6, 0x2000
	s_or_b32 s40, s6, 0x6000
	s_add_i32 s6, s3, 0x60
	s_and_b32 s6, s6, 0xe0
	v_lshl_add_u32 v173, s6, 1, v84
	s_add_i32 s6, s53, 0x1c0
	s_xor_b32 s53, s53, 0x100
	v_add_u32_e32 v174, s53, v84
	s_add_i32 s53, s3, 0xa0
	s_lshl_b32 s42, s7, 4
	s_and_b32 s7, s6, 0x1c0
	s_lshl_b32 s6, s6, 4
	s_and_b32 s53, s53, 0xe0
	s_lshl_b32 s8, s7, 4
	s_or_b32 s38, s6, 0x2000
	s_or_b32 s6, s6, 0x6000
	s_mov_b32 s7, s27
	v_lshl_add_u32 v175, s53, 1, v84
	s_add_i32 s53, s3, 0xc0
	s_addk_i32 s3, 0xe0
	v_lshl_add_u64 v[68:69], v[64:65], 0, s[48:49]
	v_lshl_add_u64 v[78:79], v[64:65], 0, s[50:51]
	v_lshl_add_u64 v[138:139], v[64:65], 0, s[46:47]
	v_lshl_add_u64 v[140:141], v[64:65], 0, s[42:43]
	v_lshl_add_u64 v[142:143], v[64:65], 0, s[44:45]
	v_lshl_add_u64 v[144:145], v[64:65], 0, s[40:41]
	v_lshl_add_u64 v[146:147], v[64:65], 0, s[8:9]
	v_lshl_add_u64 v[148:149], v[64:65], 0, s[38:39]
	v_lshl_add_u64 v[150:151], v[64:65], 0, s[6:7]
	s_and_b32 s53, s53, 0xe0
	s_and_b32 s3, s3, 0xe0
	v_add_u32_e32 v64, s28, v83
	v_mov_b32_e32 v65, v67
	v_lshl_add_u32 v176, s53, 1, v84
	v_lshl_add_u32 v177, s3, 1, v84
	v_lshlrev_b64 v[84:85], 10, v[64:65]
	ds_read_b128 v[102:105], v1
	ds_read_b128 v[106:109], v1 offset:8448
	v_lshl_add_u64 v[166:167], v[58:59], 0, v[84:85]
	v_or_b32_e32 v84, 1, v64
	v_mov_b32_e32 v85, v67
	v_lshlrev_b64 v[84:85], 10, v[84:85]
	v_lshl_add_u64 v[168:169], v[58:59], 0, v[84:85]
	v_or_b32_e32 v84, 2, v64
	v_mov_b32_e32 v85, v67
	v_or_b32_e32 v64, 3, v64
	v_lshlrev_b64 v[84:85], 10, v[84:85]
	v_lshlrev_b64 v[64:65], 10, v[64:65]
	v_lshl_add_u64 v[170:171], v[58:59], 0, v[84:85]
	v_lshl_add_u64 v[58:59], v[58:59], 0, v[64:65]
	s_setprio 1
	s_waitcnt vmcnt(13) lgkmcnt(1)
	v_mfma_f32_16x16x32_f16 v[110:113], v[102:105], v[22:25], 0
	s_waitcnt lgkmcnt(0)
	v_mfma_f32_16x16x32_f16 v[22:25], v[106:109], v[22:25], 0
	s_waitcnt vmcnt(5)
	v_mfma_f32_16x16x32_f16 v[114:117], v[102:105], v[94:97], 0
	v_mfma_f32_16x16x32_f16 v[94:97], v[106:109], v[94:97], 0
	v_mfma_f32_16x16x32_f16 v[118:121], v[102:105], v[14:17], 0
	v_mfma_f32_16x16x32_f16 v[14:17], v[106:109], v[14:17], 0
	v_mfma_f32_16x16x32_f16 v[102:105], v[102:105], v[18:21], 0
	v_mfma_f32_16x16x32_f16 v[18:21], v[106:109], v[18:21], 0
	s_setprio 0
	v_add_co_u32_e32 v64, vcc, s29, v62
	global_load_dwordx4 v[106:109], v[62:63], off
	s_nop 0
	v_addc_co_u32_e32 v65, vcc, 0, v63, vcc
	v_add_co_u32_e32 v84, vcc, s52, v62
	s_nop 1
	v_addc_co_u32_e32 v85, vcc, 0, v63, vcc
	v_add_co_u32_e32 v62, vcc, s33, v62
	global_load_dwordx4 v[122:125], v[64:65], off
	global_load_dwordx4 v[126:129], v[84:85], off
	v_addc_co_u32_e32 v63, vcc, 0, v63, vcc
	global_load_dwordx4 v[62:65], v[62:63], off
	ds_read_b128 v[130:133], v82
	ds_read_b128 v[134:137], v82 offset:8448
	s_setprio 1
	s_waitcnt lgkmcnt(1)
	v_mfma_f32_16x16x32_f16 v[110:113], v[130:133], v[10:13], v[110:113]
	s_waitcnt lgkmcnt(0)
	v_mfma_f32_16x16x32_f16 v[10:13], v[134:137], v[10:13], v[22:25]
	v_mfma_f32_16x16x32_f16 v[22:25], v[130:133], v[54:57], v[114:117]
	v_mfma_f32_16x16x32_f16 v[54:57], v[134:137], v[54:57], v[94:97]
	v_mfma_f32_16x16x32_f16 v[94:97], v[130:133], v[86:89], v[118:121]
	v_mfma_f32_16x16x32_f16 v[14:17], v[134:137], v[86:89], v[14:17]
	v_mfma_f32_16x16x32_f16 v[84:87], v[130:133], v[50:53], v[102:105]
	v_mfma_f32_16x16x32_f16 v[18:21], v[134:137], v[50:53], v[18:21]
	s_setprio 0
	global_load_dwordx4 v[50:53], v[68:69], off
	global_load_dwordx4 v[102:105], v[78:79], off
	v_add_co_u32_e32 v68, vcc, s52, v68
	s_nop 1
	v_addc_co_u32_e32 v69, vcc, 0, v69, vcc
	global_load_dwordx4 v[114:117], v[68:69], off
	global_load_dwordx4 v[118:121], v[138:139], off
	ds_read_b128 v[130:133], v172
	ds_read_b128 v[134:137], v172 offset:8448
	s_setprio 1
	s_waitcnt lgkmcnt(1)
	v_mfma_f32_16x16x32_f16 v[110:113], v[130:133], v[46:49], v[110:113]
	s_waitcnt lgkmcnt(0)
	v_mfma_f32_16x16x32_f16 v[10:13], v[134:137], v[46:49], v[10:13]
	v_mfma_f32_16x16x32_f16 v[22:25], v[130:133], v[42:45], v[22:25]
	v_mfma_f32_16x16x32_f16 v[42:45], v[134:137], v[42:45], v[54:57]
	v_mfma_f32_16x16x32_f16 v[46:49], v[130:133], v[90:93], v[94:97]
	v_mfma_f32_16x16x32_f16 v[14:17], v[134:137], v[90:93], v[14:17]
	s_waitcnt vmcnt(12)
	v_mfma_f32_16x16x32_f16 v[54:57], v[130:133], v[98:101], v[84:87]
	v_mfma_f32_16x16x32_f16 v[18:21], v[134:137], v[98:101], v[18:21]
	s_setprio 0
	v_add_co_u32_e32 v68, vcc, s52, v140
	global_load_dwordx4 v[84:87], v[140:141], off
	global_load_dwordx4 v[88:91], v[142:143], off
	v_addc_co_u32_e32 v69, vcc, 0, v141, vcc
	global_load_dwordx4 v[92:95], v[68:69], off
	global_load_dwordx4 v[96:99], v[144:145], off
	ds_read_b128 v[130:133], v173
	ds_read_b128 v[134:137], v173 offset:8448
	s_setprio 1
	s_waitcnt vmcnt(15) lgkmcnt(1)
	v_mfma_f32_16x16x32_f16 v[110:113], v[130:133], v[34:37], v[110:113]
	s_waitcnt lgkmcnt(0)
	v_mfma_f32_16x16x32_f16 v[10:13], v[134:137], v[34:37], v[10:13]
	s_waitcnt vmcnt(14)
	v_mfma_f32_16x16x32_f16 v[22:25], v[130:133], v[38:41], v[22:25]
	v_mfma_f32_16x16x32_f16 v[34:37], v[134:137], v[38:41], v[42:45]
	s_waitcnt vmcnt(13)
	v_mfma_f32_16x16x32_f16 v[38:41], v[130:133], v[70:73], v[46:49]
	v_mfma_f32_16x16x32_f16 v[14:17], v[134:137], v[70:73], v[14:17]
	s_waitcnt vmcnt(12)
	v_mfma_f32_16x16x32_f16 v[42:45], v[130:133], v[74:77], v[54:57]
	v_mfma_f32_16x16x32_f16 v[18:21], v[134:137], v[74:77], v[18:21]
	s_setprio 0
	v_add_co_u32_e32 v68, vcc, s52, v146
	global_load_dwordx4 v[46:49], v[146:147], off
	global_load_dwordx4 v[54:57], v[148:149], off
	v_addc_co_u32_e32 v69, vcc, 0, v147, vcc
	global_load_dwordx4 v[68:71], v[68:69], off
	s_nop 0
	global_load_dwordx4 v[72:75], v[150:151], off
	ds_read_b128 v[76:79], v174
	ds_read_b128 v[130:133], v174 offset:8448
	s_setprio 1
	s_waitcnt vmcnt(15) lgkmcnt(1)
	v_mfma_f32_16x16x32_f16 v[110:113], v[76:79], v[106:109], v[110:113]
	s_waitcnt lgkmcnt(0)
	v_mfma_f32_16x16x32_f16 v[10:13], v[130:133], v[106:109], v[10:13]
	s_waitcnt vmcnt(14)
	v_mfma_f32_16x16x32_f16 v[22:25], v[76:79], v[122:125], v[22:25]
	v_mfma_f32_16x16x32_f16 v[34:37], v[130:133], v[122:125], v[34:37]
	s_waitcnt vmcnt(13)
	v_mfma_f32_16x16x32_f16 v[38:41], v[76:79], v[126:129], v[38:41]
	v_mfma_f32_16x16x32_f16 v[14:17], v[130:133], v[126:129], v[14:17]
	s_waitcnt vmcnt(12)
	v_mfma_f32_16x16x32_f16 v[42:45], v[76:79], v[62:65], v[42:45]
	v_mfma_f32_16x16x32_f16 v[18:21], v[130:133], v[62:65], v[18:21]
	s_setprio 0
	ds_read_b128 v[62:65], v175
	ds_read_b128 v[76:79], v175 offset:8448
	s_setprio 1
	s_waitcnt vmcnt(11) lgkmcnt(1)
	v_mfma_f32_16x16x32_f16 v[106:109], v[62:65], v[50:53], v[110:113]
	s_waitcnt lgkmcnt(0)
	v_mfma_f32_16x16x32_f16 v[10:13], v[76:79], v[50:53], v[10:13]
	s_waitcnt vmcnt(10)
	v_mfma_f32_16x16x32_f16 v[22:25], v[62:65], v[102:105], v[22:25]
	v_mfma_f32_16x16x32_f16 v[34:37], v[76:79], v[102:105], v[34:37]
	s_waitcnt vmcnt(9)
	v_mfma_f32_16x16x32_f16 v[38:41], v[62:65], v[114:117], v[38:41]
	v_mfma_f32_16x16x32_f16 v[14:17], v[76:79], v[114:117], v[14:17]
	s_waitcnt vmcnt(8)
	v_mfma_f32_16x16x32_f16 v[42:45], v[62:65], v[118:121], v[42:45]
	v_mfma_f32_16x16x32_f16 v[18:21], v[76:79], v[118:121], v[18:21]
	s_setprio 0
	ds_read_b128 v[50:53], v176
	ds_read_b128 v[62:65], v176 offset:8448
	s_setprio 1
	s_waitcnt vmcnt(7) lgkmcnt(1)
	v_mfma_f32_16x16x32_f16 v[76:79], v[50:53], v[84:87], v[106:109]
	s_waitcnt lgkmcnt(0)
	v_mfma_f32_16x16x32_f16 v[10:13], v[62:65], v[84:87], v[10:13]
	s_waitcnt vmcnt(6)
	v_mfma_f32_16x16x32_f16 v[22:25], v[50:53], v[88:91], v[22:25]
	v_mfma_f32_16x16x32_f16 v[34:37], v[62:65], v[88:91], v[34:37]
	s_waitcnt vmcnt(5)
	v_mfma_f32_16x16x32_f16 v[38:41], v[50:53], v[92:95], v[38:41]
	v_mfma_f32_16x16x32_f16 v[14:17], v[62:65], v[92:95], v[14:17]
	s_waitcnt vmcnt(4)
	v_mfma_f32_16x16x32_f16 v[42:45], v[50:53], v[96:99], v[42:45]
	v_mfma_f32_16x16x32_f16 v[18:21], v[62:65], v[96:99], v[18:21]
	s_setprio 0
	ds_read_b128 v[50:53], v177
	ds_read_b128 v[62:65], v177 offset:8448
	s_setprio 1
	s_waitcnt vmcnt(3) lgkmcnt(1)
	v_mfma_f32_16x16x32_f16 v[76:79], v[50:53], v[46:49], v[76:79]
	s_waitcnt lgkmcnt(0)
	v_mfma_f32_16x16x32_f16 v[10:13], v[62:65], v[46:49], v[10:13]
	s_waitcnt vmcnt(2)
	v_mfma_f32_16x16x32_f16 v[22:25], v[50:53], v[54:57], v[22:25]
	v_mfma_f32_16x16x32_f16 v[34:37], v[62:65], v[54:57], v[34:37]
	s_waitcnt vmcnt(1)
	v_mfma_f32_16x16x32_f16 v[38:41], v[50:53], v[68:71], v[38:41]
	v_mfma_f32_16x16x32_f16 v[14:17], v[62:65], v[68:71], v[14:17]
	s_waitcnt vmcnt(0)
	v_mfma_f32_16x16x32_f16 v[42:45], v[50:53], v[72:75], v[42:45]
	v_mfma_f32_16x16x32_f16 v[18:21], v[62:65], v[72:75], v[18:21]
	s_setprio 0
	v_add_co_u32_e32 v108, vcc, s29, v152
	v_and_b32_e32 v67, 0x1c0, v0
	s_nop 0
	v_addc_co_u32_e32 v109, vcc, 0, v153, vcc
	v_add_co_u32_e32 v46, vcc, s52, v152
	s_movk_i32 s4, 0x50
	s_nop 0
	v_addc_co_u32_e32 v47, vcc, 0, v153, vcc
	v_add_co_u32_e32 v68, vcc, s33, v152
	v_or_b32_e32 v116, 16, v67
	s_nop 0
	v_addc_co_u32_e32 v69, vcc, 0, v153, vcc
	v_add_co_u32_e32 v110, vcc, s52, v154
	global_load_dwordx4 v[46:49], v[46:47], off
	s_nop 0
	global_load_dwordx4 v[50:53], v[68:69], off
	global_load_dwordx4 v[54:57], v[152:153], off
	global_load_dwordx4 v[62:65], v[154:155], off
	v_addc_co_u32_e32 v111, vcc, 0, v155, vcc
	v_add_co_u32_e32 v112, vcc, s52, v160
	global_load_dwordx4 v[68:71], v[156:157], off
	global_load_dwordx4 v[72:75], v[158:159], off
	global_load_dwordx4 v[84:87], v[160:161], off
	global_load_dwordx4 v[88:91], v[162:163], off
	v_addc_co_u32_e32 v113, vcc, 0, v161, vcc
	global_load_dwordx4 v[92:95], v[110:111], off
	global_load_dwordx4 v[96:99], v[112:113], off
	global_load_dwordx4 v[100:103], v[108:109], off
	global_load_dwordx4 v[104:107], v[164:165], off
	s_nop 0
	global_store_dwordx4 v[166:167], v[2:5], off sc0 sc1
	global_store_dwordx4 v[168:169], v[6:9], off sc0 sc1
	global_store_dwordx4 v[170:171], v[26:29], off sc0 sc1
	global_store_dwordx4 v[58:59], v[30:33], off sc0 sc1
	v_and_b32_e32 v4, 0x1cf, v0
	v_cvt_pk_f16_f32 v3, v78, v79
	v_cvt_pk_f16_f32 v2, v76, v77
	v_mad_u32_u24 v4, v4, s4, v80
	v_or_b32_e32 v5, v116, v81
	v_or_b32_e32 v117, 32, v67
	ds_write_b64 v4, v[2:3]
	v_cvt_pk_f16_f32 v3, v24, v25
	v_cvt_pk_f16_f32 v2, v22, v23
	v_mad_u32_u24 v5, v5, s4, v80
	v_or_b32_e32 v6, v117, v81
	v_or_b32_e32 v118, 48, v67
	ds_write_b64 v5, v[2:3]
	v_cvt_pk_f16_f32 v3, v40, v41
	v_cvt_pk_f16_f32 v2, v38, v39
	v_mad_u32_u24 v6, v6, s4, v80
	v_or_b32_e32 v7, v118, v81
	ds_write_b64 v6, v[2:3]
	v_cvt_pk_f16_f32 v3, v44, v45
	v_cvt_pk_f16_f32 v2, v42, v43
	v_mad_u32_u24 v7, v7, s4, v80
	ds_write_b64 v7, v[2:3]
	v_cvt_pk_f16_f32 v3, v12, v13
	v_cvt_pk_f16_f32 v2, v10, v11
	ds_write_b64 v4, v[2:3] offset:32
	v_cvt_pk_f16_f32 v3, v36, v37
	v_cvt_pk_f16_f32 v2, v34, v35
	ds_write_b64 v5, v[2:3] offset:32
	v_cvt_pk_f16_f32 v3, v16, v17
	v_cvt_pk_f16_f32 v2, v14, v15
	v_lshl_add_u64 v[10:11], v[60:61], 0, s[14:15]
	ds_write_b64 v6, v[2:3] offset:32
	v_cvt_pk_f16_f32 v2, v18, v19
	v_add_co_u32_e32 v18, vcc, s52, v10
	v_cvt_pk_f16_f32 v3, v20, v21
	v_lshl_add_u64 v[12:13], v[60:61], 0, s[16:17]
	v_addc_co_u32_e32 v19, vcc, 0, v11, vcc
	ds_write_b64 v7, v[2:3] offset:32
	s_waitcnt lgkmcnt(0)
	s_barrier
	global_load_dwordx4 v[2:5], v[10:11], off
	global_load_dwordx4 v[6:9], v[12:13], off
	v_lshl_add_u64 v[20:21], v[60:61], 0, s[12:13]
	global_load_dwordx4 v[10:13], v[18:19], off
	global_load_dwordx4 v[14:17], v[20:21], off
	ds_read_b128 v[18:21], v1
	ds_read_b128 v[22:25], v1 offset:8448
	s_mov_b32 s3, s27
	s_setprio 1
	s_waitcnt vmcnt(17) lgkmcnt(1)
	v_mfma_f32_16x16x32_f16 v[26:29], v[18:21], v[54:57], 0
	s_waitcnt lgkmcnt(0)
	v_mfma_f32_16x16x32_f16 v[30:33], v[22:25], v[54:57], 0
	s_waitcnt vmcnt(9)
	v_mfma_f32_16x16x32_f16 v[34:37], v[18:21], v[100:103], 0
	v_mfma_f32_16x16x32_f16 v[38:41], v[22:25], v[100:103], 0
	v_mfma_f32_16x16x32_f16 v[42:45], v[18:21], v[46:49], 0
	v_mfma_f32_16x16x32_f16 v[46:49], v[22:25], v[46:49], 0
	v_mfma_f32_16x16x32_f16 v[18:21], v[18:21], v[50:53], 0
	v_mfma_f32_16x16x32_f16 v[22:25], v[22:25], v[50:53], 0
	s_setprio 0
	v_lshl_add_u64 v[58:59], v[60:61], 0, s[10:11]
	v_add_co_u32_e32 v76, vcc, s29, v58
	s_nop 1
	v_addc_co_u32_e32 v77, vcc, 0, v59, vcc
	v_add_co_u32_e32 v108, vcc, s52, v58
	global_load_dwordx4 v[50:53], v[58:59], off
	global_load_dwordx4 v[54:57], v[76:77], off
	v_addc_co_u32_e32 v109, vcc, 0, v59, vcc
	v_add_co_u32_e32 v58, vcc, s33, v58
	s_nop 1
	v_addc_co_u32_e32 v59, vcc, 0, v59, vcc
	global_load_dwordx4 v[76:79], v[108:109], off
	global_load_dwordx4 v[100:103], v[58:59], off
	ds_read_b128 v[108:111], v82
	ds_read_b128 v[112:115], v82 offset:8448
	s_setprio 1
	s_waitcnt lgkmcnt(1)
	v_mfma_f32_16x16x32_f16 v[26:29], v[108:111], v[62:65], v[26:29]
	s_waitcnt lgkmcnt(0)
	v_mfma_f32_16x16x32_f16 v[30:33], v[112:115], v[62:65], v[30:33]
	v_mfma_f32_16x16x32_f16 v[34:37], v[108:111], v[68:71], v[34:37]
	v_mfma_f32_16x16x32_f16 v[38:41], v[112:115], v[68:71], v[38:41]
	v_mfma_f32_16x16x32_f16 v[42:45], v[108:111], v[92:95], v[42:45]
	v_mfma_f32_16x16x32_f16 v[46:49], v[112:115], v[92:95], v[46:49]
	v_mfma_f32_16x16x32_f16 v[18:21], v[108:111], v[72:75], v[18:21]
	v_mfma_f32_16x16x32_f16 v[22:25], v[112:115], v[72:75], v[22:25]
	s_setprio 0
	v_lshl_add_u64 v[58:59], v[60:61], 0, s[48:49]
	v_lshl_add_u64 v[72:73], v[60:61], 0, s[50:51]
	global_load_dwordx4 v[62:65], v[58:59], off
	global_load_dwordx4 v[68:71], v[72:73], off
	v_add_co_u32_e32 v58, vcc, s52, v58
	v_lshl_add_u64 v[82:83], v[60:61], 0, s[46:47]
	s_nop 0
	v_addc_co_u32_e32 v59, vcc, 0, v59, vcc
	global_load_dwordx4 v[72:75], v[58:59], off
	global_load_dwordx4 v[92:95], v[82:83], off
	ds_read_b128 v[108:111], v172
	ds_read_b128 v[112:115], v172 offset:8448
	s_setprio 1
	s_waitcnt lgkmcnt(1)
	v_mfma_f32_16x16x32_f16 v[26:29], v[108:111], v[84:87], v[26:29]
	s_waitcnt lgkmcnt(0)
	v_mfma_f32_16x16x32_f16 v[30:33], v[112:115], v[84:87], v[30:33]
	v_mfma_f32_16x16x32_f16 v[34:37], v[108:111], v[88:91], v[34:37]
	v_mfma_f32_16x16x32_f16 v[38:41], v[112:115], v[88:91], v[38:41]
	v_mfma_f32_16x16x32_f16 v[42:45], v[108:111], v[96:99], v[42:45]
	v_mfma_f32_16x16x32_f16 v[46:49], v[112:115], v[96:99], v[46:49]
	s_waitcnt vmcnt(16)
	v_mfma_f32_16x16x32_f16 v[18:21], v[108:111], v[104:107], v[18:21]
	v_mfma_f32_16x16x32_f16 v[22:25], v[112:115], v[104:107], v[22:25]
	s_setprio 0
	v_lshl_add_u64 v[58:59], v[60:61], 0, s[42:43]
	v_lshl_add_u64 v[90:91], v[60:61], 0, s[44:45]
	global_load_dwordx4 v[82:85], v[58:59], off
	global_load_dwordx4 v[86:89], v[90:91], off
	v_add_co_u32_e32 v58, vcc, s52, v58
	v_lshl_add_u64 v[90:91], v[60:61], 0, s[40:41]
	s_nop 0
	v_addc_co_u32_e32 v59, vcc, 0, v59, vcc
	global_load_dwordx4 v[96:99], v[58:59], off
	global_load_dwordx4 v[104:107], v[90:91], off
	ds_read_b128 v[108:111], v173
	ds_read_b128 v[112:115], v173 offset:8448
	s_setprio 1
	s_waitcnt vmcnt(15) lgkmcnt(1)
	v_mfma_f32_16x16x32_f16 v[26:29], v[108:111], v[2:5], v[26:29]
	s_waitcnt lgkmcnt(0)
	v_mfma_f32_16x16x32_f16 v[2:5], v[112:115], v[2:5], v[30:33]
	s_waitcnt vmcnt(14)
	v_mfma_f32_16x16x32_f16 v[30:33], v[108:111], v[6:9], v[34:37]
	v_mfma_f32_16x16x32_f16 v[6:9], v[112:115], v[6:9], v[38:41]
	s_waitcnt vmcnt(13)
	v_mfma_f32_16x16x32_f16 v[34:37], v[108:111], v[10:13], v[42:45]
	v_mfma_f32_16x16x32_f16 v[10:13], v[112:115], v[10:13], v[46:49]
	s_waitcnt vmcnt(12)
	v_mfma_f32_16x16x32_f16 v[18:21], v[108:111], v[14:17], v[18:21]
	v_mfma_f32_16x16x32_f16 v[14:17], v[112:115], v[14:17], v[22:25]
	s_setprio 0
	v_lshl_add_u64 v[42:43], v[60:61], 0, s[8:9]
	v_add_co_u32_e32 v58, vcc, s52, v42
	v_lshl_add_u64 v[44:45], v[60:61], 0, s[38:39]
	s_nop 0
	v_addc_co_u32_e32 v59, vcc, 0, v43, vcc
	global_load_dwordx4 v[22:25], v[42:43], off
	global_load_dwordx4 v[38:41], v[44:45], off
	v_lshl_add_u64 v[60:61], v[60:61], 0, s[6:7]
	global_load_dwordx4 v[42:45], v[58:59], off
	global_load_dwordx4 v[46:49], v[60:61], off
	ds_read_b128 v[58:61], v174
	ds_read_b128 v[108:111], v174 offset:8448
	s_setprio 1
	s_waitcnt vmcnt(15) lgkmcnt(1)
	v_mfma_f32_16x16x32_f16 v[26:29], v[58:61], v[50:53], v[26:29]
	s_waitcnt lgkmcnt(0)
	v_mfma_f32_16x16x32_f16 v[2:5], v[108:111], v[50:53], v[2:5]
	s_waitcnt vmcnt(14)
	v_mfma_f32_16x16x32_f16 v[30:33], v[58:61], v[54:57], v[30:33]
	v_mfma_f32_16x16x32_f16 v[6:9], v[108:111], v[54:57], v[6:9]
	s_waitcnt vmcnt(13)
	v_mfma_f32_16x16x32_f16 v[34:37], v[58:61], v[76:79], v[34:37]
	v_mfma_f32_16x16x32_f16 v[10:13], v[108:111], v[76:79], v[10:13]
	s_waitcnt vmcnt(12)
	v_mfma_f32_16x16x32_f16 v[18:21], v[58:61], v[100:103], v[18:21]
	v_mfma_f32_16x16x32_f16 v[14:17], v[108:111], v[100:103], v[14:17]
	s_setprio 0
	ds_read_b128 v[50:53], v175
	ds_read_b128 v[54:57], v175 offset:8448
	s_setprio 1
	s_waitcnt vmcnt(11) lgkmcnt(1)
	v_mfma_f32_16x16x32_f16 v[26:29], v[50:53], v[62:65], v[26:29]
	s_waitcnt lgkmcnt(0)
	v_mfma_f32_16x16x32_f16 v[2:5], v[54:57], v[62:65], v[2:5]
	s_waitcnt vmcnt(10)
	v_mfma_f32_16x16x32_f16 v[30:33], v[50:53], v[68:71], v[30:33]
	v_mfma_f32_16x16x32_f16 v[6:9], v[54:57], v[68:71], v[6:9]
	s_waitcnt vmcnt(9)
	v_mfma_f32_16x16x32_f16 v[34:37], v[50:53], v[72:75], v[34:37]
	v_mfma_f32_16x16x32_f16 v[10:13], v[54:57], v[72:75], v[10:13]
	s_waitcnt vmcnt(8)
	v_mfma_f32_16x16x32_f16 v[18:21], v[50:53], v[92:95], v[18:21]
	v_mfma_f32_16x16x32_f16 v[14:17], v[54:57], v[92:95], v[14:17]
	s_setprio 0
	ds_read_b128 v[50:53], v176
	ds_read_b128 v[54:57], v176 offset:8448
	s_setprio 1
	s_waitcnt vmcnt(7) lgkmcnt(1)
	v_mfma_f32_16x16x32_f16 v[26:29], v[50:53], v[82:85], v[26:29]
	s_waitcnt lgkmcnt(0)
	v_mfma_f32_16x16x32_f16 v[2:5], v[54:57], v[82:85], v[2:5]
	s_waitcnt vmcnt(6)
	v_mfma_f32_16x16x32_f16 v[30:33], v[50:53], v[86:89], v[30:33]
	v_mfma_f32_16x16x32_f16 v[6:9], v[54:57], v[86:89], v[6:9]
	s_waitcnt vmcnt(5)
	v_mfma_f32_16x16x32_f16 v[34:37], v[50:53], v[96:99], v[34:37]
	v_mfma_f32_16x16x32_f16 v[58:61], v[54:57], v[96:99], v[10:13]
	s_waitcnt vmcnt(4)
	v_mfma_f32_16x16x32_f16 v[18:21], v[50:53], v[104:107], v[18:21]
	v_mfma_f32_16x16x32_f16 v[50:53], v[54:57], v[104:107], v[14:17]
	s_setprio 0
	ds_read_b128 v[54:57], v177
	ds_read_b128 v[62:65], v177 offset:8448
	s_setprio 1
	s_waitcnt vmcnt(3) lgkmcnt(1)
	v_mfma_f32_16x16x32_f16 v[26:29], v[54:57], v[22:25], v[26:29]
	s_waitcnt lgkmcnt(0)
	v_mfma_f32_16x16x32_f16 v[14:17], v[62:65], v[22:25], v[2:5]
	s_waitcnt vmcnt(2)
	v_mfma_f32_16x16x32_f16 v[22:25], v[54:57], v[38:41], v[30:33]
	v_mfma_f32_16x16x32_f16 v[10:13], v[62:65], v[38:41], v[6:9]
	s_waitcnt vmcnt(1)
	v_mfma_f32_16x16x32_f16 v[30:33], v[54:57], v[42:45], v[34:37]
	v_mfma_f32_16x16x32_f16 v[6:9], v[62:65], v[42:45], v[58:61]
	s_waitcnt vmcnt(0)
	v_mfma_f32_16x16x32_f16 v[34:37], v[54:57], v[46:49], v[18:21]
	v_mfma_f32_16x16x32_f16 v[2:5], v[62:65], v[46:49], v[50:53]
	s_setprio 0
	s_nop 1
	v_mul_u32_u24_e32 v52, 0x50, v0
	ds_read_b128 v[18:21], v52
	s_lshl_b64 s[2:3], s[2:3], 15
	v_or_b32_e32 v0, s2, v66
	v_mov_b32_e32 v1, s3
	v_lshl_add_u64 v[50:51], s[24:25], 0, v[0:1]
	ds_read_b128 v[38:41], v52 offset:16
	ds_read_b128 v[42:45], v52 offset:32
	ds_read_b128 v[46:49], v52 offset:48
	s_waitcnt lgkmcnt(3)
	global_store_dwordx4 v[50:51], v[18:21], off sc0 sc1
	s_nop 1
	v_add_co_u32_e32 v18, vcc, s29, v50
	s_nop 1
	v_addc_co_u32_e32 v19, vcc, 0, v51, vcc
	s_waitcnt lgkmcnt(2)
	global_store_dwordx4 v[18:19], v[38:41], off sc0 sc1
	v_or_b32_e32 v18, 0x4000, v0
	v_mov_b32_e32 v19, s3
	v_lshl_add_u64 v[20:21], s[24:25], 0, v[18:19]
	s_waitcnt lgkmcnt(1)
	global_store_dwordx4 v[20:21], v[42:45], off sc0 sc1
	v_add_co_u32_e32 v20, vcc, s33, v50
	v_or_b32_e32 v39, 0x200, v81
	s_nop 0
	v_addc_co_u32_e32 v21, vcc, 0, v51, vcc
	s_waitcnt lgkmcnt(0)
	global_store_dwordx4 v[20:21], v[46:49], off sc0 sc1
	v_lshl_add_u64 v[0:1], s[0:1], 0, v[0:1]
	v_mov_b32_e32 v180, 0xbfb8aa3b
	v_mov_b32_e32 v181, 0xbfb8aa3b
	v_mov_b32_e32 v182, 1.0
	v_mov_b32_e32 v183, 1.0
	v_or_b32_e32 v184, v39, v67
	v_mad_u32_u24 v184, v184, s4, v80
	v_or_b32_e32 v185, v116, v39
	v_mad_u32_u24 v185, v185, s4, v80
	v_or_b32_e32 v186, v117, v39
	v_mad_u32_u24 v186, v186, s4, v80
	v_or_b32_e32 v187, v118, v39
	v_mad_u32_u24 v187, v187, s4, v80
	v_pk_mul_f32 v[188:189], v[26:27], v[180:181]
	v_pk_mul_f32 v[190:191], v[28:29], v[180:181]
	v_pk_mul_f32 v[196:197], v[22:23], v[180:181]
	v_pk_mul_f32 v[198:199], v[24:25], v[180:181]
	v_pk_mul_f32 v[204:205], v[30:31], v[180:181]
	v_pk_mul_f32 v[206:207], v[32:33], v[180:181]
	v_pk_mul_f32 v[212:213], v[34:35], v[180:181]
	v_pk_mul_f32 v[214:215], v[36:37], v[180:181]
	v_pk_mul_f32 v[220:221], v[14:15], v[180:181]
	v_pk_mul_f32 v[222:223], v[16:17], v[180:181]
	v_pk_mul_f32 v[228:229], v[10:11], v[180:181]
	v_pk_mul_f32 v[230:231], v[12:13], v[180:181]
	v_pk_mul_f32 v[236:237], v[6:7], v[180:181]
	v_pk_mul_f32 v[238:239], v[8:9], v[180:181]
	v_pk_mul_f32 v[244:245], v[2:3], v[180:181]
	v_pk_mul_f32 v[246:247], v[4:5], v[180:181]
	v_exp_f32_e32 v188, v188
	v_exp_f32_e32 v189, v189
	v_exp_f32_e32 v190, v190
	v_exp_f32_e32 v191, v191
	v_exp_f32_e32 v196, v196
	v_exp_f32_e32 v197, v197
	v_exp_f32_e32 v198, v198
	v_exp_f32_e32 v199, v199
	v_exp_f32_e32 v204, v204
	v_exp_f32_e32 v205, v205
	v_exp_f32_e32 v206, v206
	v_exp_f32_e32 v207, v207
	v_exp_f32_e32 v212, v212
	v_exp_f32_e32 v213, v213
	v_exp_f32_e32 v214, v214
	v_exp_f32_e32 v215, v215
	v_exp_f32_e32 v220, v220
	v_exp_f32_e32 v221, v221
	v_exp_f32_e32 v222, v222
	v_exp_f32_e32 v223, v223
	v_exp_f32_e32 v228, v228
	v_exp_f32_e32 v229, v229
	v_exp_f32_e32 v230, v230
	v_exp_f32_e32 v231, v231
	v_exp_f32_e32 v236, v236
	v_exp_f32_e32 v237, v237
	v_exp_f32_e32 v238, v238
	v_exp_f32_e32 v239, v239
	v_exp_f32_e32 v244, v244
	v_exp_f32_e32 v245, v245
	v_exp_f32_e32 v246, v246
	v_exp_f32_e32 v247, v247
	v_pk_add_f32 v[188:189], v[188:189], v[182:183]
	v_pk_add_f32 v[190:191], v[190:191], v[182:183]
	v_pk_add_f32 v[196:197], v[196:197], v[182:183]
	v_pk_add_f32 v[198:199], v[198:199], v[182:183]
	v_pk_add_f32 v[204:205], v[204:205], v[182:183]
	v_pk_add_f32 v[206:207], v[206:207], v[182:183]
	v_pk_add_f32 v[212:213], v[212:213], v[182:183]
	v_pk_add_f32 v[214:215], v[214:215], v[182:183]
	v_pk_add_f32 v[220:221], v[220:221], v[182:183]
	v_pk_add_f32 v[222:223], v[222:223], v[182:183]
	v_pk_add_f32 v[228:229], v[228:229], v[182:183]
	v_pk_add_f32 v[230:231], v[230:231], v[182:183]
	v_pk_add_f32 v[236:237], v[236:237], v[182:183]
	v_pk_add_f32 v[238:239], v[238:239], v[182:183]
	v_pk_add_f32 v[244:245], v[244:245], v[182:183]
	v_pk_add_f32 v[246:247], v[246:247], v[182:183]
	v_rcp_f32_e32 v188, v188
	v_rcp_f32_e32 v189, v189
	v_rcp_f32_e32 v190, v190
	v_rcp_f32_e32 v191, v191
	v_rcp_f32_e32 v196, v196
	v_rcp_f32_e32 v197, v197
	v_rcp_f32_e32 v198, v198
	v_rcp_f32_e32 v199, v199
	v_rcp_f32_e32 v204, v204
	v_rcp_f32_e32 v205, v205
	v_rcp_f32_e32 v206, v206
	v_rcp_f32_e32 v207, v207
	v_rcp_f32_e32 v212, v212
	v_rcp_f32_e32 v213, v213
	v_rcp_f32_e32 v214, v214
	v_rcp_f32_e32 v215, v215
	v_rcp_f32_e32 v220, v220
	v_rcp_f32_e32 v221, v221
	v_rcp_f32_e32 v222, v222
	v_rcp_f32_e32 v223, v223
	v_rcp_f32_e32 v228, v228
	v_rcp_f32_e32 v229, v229
	v_rcp_f32_e32 v230, v230
	v_rcp_f32_e32 v231, v231
	v_rcp_f32_e32 v236, v236
	v_rcp_f32_e32 v237, v237
	v_rcp_f32_e32 v238, v238
	v_rcp_f32_e32 v239, v239
	v_rcp_f32_e32 v244, v244
	v_rcp_f32_e32 v245, v245
	v_rcp_f32_e32 v246, v246
	v_rcp_f32_e32 v247, v247
	v_fma_mixlo_f16 v192, v26, v188, 0
	v_mul_f32_e32 v189, v27, v189
	v_mul_f32_e32 v190, v28, v190
	v_fma_mixlo_f16 v193, v29, v191, 0
	v_fma_mixlo_f16 v200, v22, v196, 0
	v_mul_f32_e32 v197, v23, v197
	v_mul_f32_e32 v198, v24, v198
	v_fma_mixlo_f16 v201, v25, v199, 0
	v_fma_mixlo_f16 v208, v30, v204, 0
	v_mul_f32_e32 v205, v31, v205
	v_mul_f32_e32 v206, v32, v206
	v_fma_mixlo_f16 v209, v33, v207, 0
	v_fma_mixlo_f16 v216, v34, v212, 0
	v_mul_f32_e32 v213, v35, v213
	v_mul_f32_e32 v214, v36, v214
	v_fma_mixlo_f16 v217, v37, v215, 0
	v_fma_mixlo_f16 v224, v14, v220, 0
	v_mul_f32_e32 v221, v15, v221
	v_mul_f32_e32 v222, v16, v222
	v_fma_mixlo_f16 v225, v17, v223, 0
	v_fma_mixlo_f16 v232, v10, v228, 0
	v_mul_f32_e32 v229, v11, v229
	v_mul_f32_e32 v230, v12, v230
	v_fma_mixlo_f16 v233, v13, v231, 0
	v_fma_mixlo_f16 v240, v6, v236, 0
	v_mul_f32_e32 v237, v7, v237
	v_mul_f32_e32 v238, v8, v238
	v_fma_mixlo_f16 v241, v9, v239, 0
	v_fma_mixlo_f16 v248, v2, v244, 0
	v_mul_f32_e32 v245, v3, v245
	v_mul_f32_e32 v246, v4, v246
	v_fma_mixlo_f16 v249, v5, v247, 0
	v_cvt_pk_f16_f32 v188, v189, v190
	v_cvt_pk_f16_f32 v196, v197, v198
	v_cvt_pk_f16_f32 v204, v205, v206
	v_cvt_pk_f16_f32 v212, v213, v214
	v_cvt_pk_f16_f32 v220, v221, v222
	v_cvt_pk_f16_f32 v228, v229, v230
	v_cvt_pk_f16_f32 v236, v237, v238
	v_cvt_pk_f16_f32 v244, v245, v246
	v_pack_b32_f16 v194, v192, v188
	v_alignbit_b32 v195, v193, v188, 16
	v_pack_b32_f16 v202, v200, v196
	v_alignbit_b32 v203, v201, v196, 16
	v_pack_b32_f16 v210, v208, v204
	v_alignbit_b32 v211, v209, v204, 16
	v_pack_b32_f16 v218, v216, v212
	v_alignbit_b32 v219, v217, v212, 16
	v_pack_b32_f16 v226, v224, v220
	v_alignbit_b32 v227, v225, v220, 16
	v_pack_b32_f16 v234, v232, v228
	v_alignbit_b32 v235, v233, v228, 16
	v_pack_b32_f16 v242, v240, v236
	v_alignbit_b32 v243, v241, v236, 16
	v_pack_b32_f16 v250, v248, v244
	v_alignbit_b32 v251, v249, v244, 16
	ds_write_b64 v184, v[194:195]
	ds_write_b64 v185, v[202:203]
	ds_write_b64 v186, v[210:211]
	ds_write_b64 v187, v[218:219]
	ds_write_b64 v184, v[226:227] offset:32
	ds_write_b64 v185, v[234:235] offset:32
	ds_write_b64 v186, v[242:243] offset:32
	ds_write_b64 v187, v[250:251] offset:32
	s_waitcnt lgkmcnt(0)
	s_barrier
	ds_read_b128 v[2:5], v52 offset:40960
	ds_read_b128 v[6:9], v52 offset:40976
	ds_read_b128 v[10:13], v52 offset:40992
	ds_read_b128 v[14:17], v52 offset:41008
	s_waitcnt lgkmcnt(3)
	global_store_dwordx4 v[0:1], v[2:5], off sc0 sc1
	s_nop 1
	v_add_co_u32_e32 v2, vcc, 0x2000, v0
	s_nop 1
	v_addc_co_u32_e32 v3, vcc, 0, v1, vcc
	v_add_co_u32_e32 v0, vcc, 0x6000, v0
	s_waitcnt lgkmcnt(2)
	global_store_dwordx4 v[2:3], v[6:9], off sc0 sc1
	v_lshl_add_u64 v[2:3], s[0:1], 0, v[18:19]
	v_addc_co_u32_e32 v1, vcc, 0, v1, vcc
	s_waitcnt lgkmcnt(1)
	global_store_dwordx4 v[2:3], v[10:13], off sc0 sc1
	s_waitcnt lgkmcnt(0)
	global_store_dwordx4 v[0:1], v[14:17], off sc0 sc1
	s_endpgm
	.p2align	8

	.amdhsa_kernel _Z4k_k2ILb0EEvPKDF16_S1_PKfS3_S3_S1_S1_PfS3_S3_S1_PDF16_PKiS4_S4_
		.amdhsa_group_segment_fixed_size 98816
		.amdhsa_private_segment_fixed_size 0
		.amdhsa_kernarg_size 120
		.amdhsa_user_sgpr_count 2
		.amdhsa_user_sgpr_dispatch_ptr 0
		.amdhsa_user_sgpr_queue_ptr 0
		.amdhsa_user_sgpr_kernarg_segment_ptr 1
		.amdhsa_user_sgpr_dispatch_id 0
		.amdhsa_user_sgpr_kernarg_preload_length 0
		.amdhsa_user_sgpr_kernarg_preload_offset 0
		.amdhsa_user_sgpr_private_segment_size 0
		.amdhsa_uses_dynamic_stack 0
		.amdhsa_enable_private_segment 0
		.amdhsa_system_sgpr_workgroup_id_x 1
		.amdhsa_system_sgpr_workgroup_id_y 0
		.amdhsa_system_sgpr_workgroup_id_z 0
		.amdhsa_system_sgpr_workgroup_info 0
		.amdhsa_system_vgpr_workitem_id 0
		.amdhsa_next_free_vgpr 252
		.amdhsa_next_free_sgpr 100
		.amdhsa_accum_offset 252
		.amdhsa_reserve_vcc 1
		.amdhsa_float_round_mode_32 0
		.amdhsa_float_round_mode_16_64 0
		.amdhsa_float_denorm_mode_32 3
		.amdhsa_float_denorm_mode_16_64 3
		.amdhsa_dx10_clamp 1
		.amdhsa_ieee_mode 1
		.amdhsa_fp16_overflow 0
		.amdhsa_tg_split 0
		.amdhsa_exception_fp_ieee_invalid_op 0
		.amdhsa_exception_fp_denorm_src 0
		.amdhsa_exception_fp_ieee_div_zero 0
		.amdhsa_exception_fp_ieee_overflow 0
		.amdhsa_exception_fp_ieee_underflow 0
		.amdhsa_exception_fp_ieee_inexact 0
		.amdhsa_exception_int_div_zero 0
	.end_amdhsa_kernel

amdhsa.kernels:
  - .agpr_count:     0
    .args:
      - .actual_access:  read_only
        .address_space:  global
        .offset:         0
        .size:           8
        .value_kind:     global_buffer
      - .actual_access:  write_only
        .address_space:  global
        .offset:         8
        .size:           8
        .value_kind:     global_buffer
      - .offset:         16
        .size:           4
        .value_kind:     by_value
      - .offset:         20
        .size:           4
        .value_kind:     by_value
      - .actual_access:  read_only
        .address_space:  global
        .offset:         24
        .size:           8
        .value_kind:     global_buffer
      - .actual_access:  write_only
        .address_space:  global
        .offset:         32
        .size:           8
        .value_kind:     global_buffer
      - .offset:         40
        .size:           4
        .value_kind:     by_value
      - .offset:         44
        .size:           4
        .value_kind:     by_value
      - .actual_access:  read_only
        .address_space:  global
        .offset:         48
        .size:           8
        .value_kind:     global_buffer
      - .actual_access:  write_only
        .address_space:  global
        .offset:         56
        .size:           8
        .value_kind:     global_buffer
      - .offset:         64
        .size:           4
        .value_kind:     by_value
      - .offset:         68
        .size:           4
        .value_kind:     by_value
      - .actual_access:  read_only
        .address_space:  global
        .offset:         72
        .size:           8
        .value_kind:     global_buffer
      - .actual_access:  write_only
        .address_space:  global
        .offset:         80
        .size:           8
        .value_kind:     global_buffer
      - .offset:         88
        .size:           4
        .value_kind:     by_value
      - .actual_access:  read_only
        .address_space:  global
        .offset:         96
        .size:           8
        .value_kind:     global_buffer
      - .actual_access:  write_only
        .address_space:  global
        .offset:         104
        .size:           8
        .value_kind:     global_buffer
      - .offset:         112
        .size:           4
        .value_kind:     by_value
      - .offset:         120
        .size:           4
        .value_kind:     hidden_block_count_x
      - .offset:         124
        .size:           4
        .value_kind:     hidden_block_count_y
      - .offset:         128
        .size:           4
        .value_kind:     hidden_block_count_z
      - .offset:         132
        .size:           2
        .value_kind:     hidden_group_size_x
      - .offset:         134
        .size:           2
        .value_kind:     hidden_group_size_y
      - .offset:         136
        .size:           2
        .value_kind:     hidden_group_size_z
      - .offset:         138
        .size:           2
        .value_kind:     hidden_remainder_x
      - .offset:         140
        .size:           2
        .value_kind:     hidden_remainder_y
      - .offset:         142
        .size:           2
        .value_kind:     hidden_remainder_z
      - .offset:         160
        .size:           8
        .value_kind:     hidden_global_offset_x
      - .offset:         168
        .size:           8
        .value_kind:     hidden_global_offset_y
      - .offset:         176
        .size:           8
        .value_kind:     hidden_global_offset_z
      - .offset:         184
        .size:           2
        .value_kind:     hidden_grid_dims
    .group_segment_fixed_size: 0
    .kernarg_segment_align: 8
    .kernarg_segment_size: 376
    .language:       OpenCL C
    .language_version:
      - 2
      - 0
    .max_flat_workgroup_size: 1024
    .name:           _Z5k_swzPKfPDF16_iiS0_S1_iiS0_S1_iiS0_PfiS0_S1_i
    .private_segment_fixed_size: 0
    .sgpr_count:     32
    .sgpr_spill_count: 0
    .symbol:         _Z5k_swzPKfPDF16_iiS0_S1_iiS0_S1_iiS0_PfiS0_S1_i.kd
    .uniform_work_group_size: 1
    .uses_dynamic_stack: false
    .vgpr_count:     14
    .vgpr_spill_count: 0
    .wavefront_size: 64
  - .agpr_count:     0
    .args:
      - .actual_access:  read_only
        .address_space:  global
        .offset:         0
        .size:           8
        .value_kind:     global_buffer
      - .actual_access:  read_only
        .address_space:  global
        .offset:         8
        .size:           8
        .value_kind:     global_buffer
      - .actual_access:  write_only
        .address_space:  global
        .offset:         16
        .size:           8
        .value_kind:     global_buffer
      - .actual_access:  read_only
        .address_space:  global
        .offset:         24
        .size:           8
        .value_kind:     global_buffer
      - .actual_access:  read_only
        .address_space:  global
        .offset:         32
        .size:           8
        .value_kind:     global_buffer
      - .actual_access:  read_only
        .address_space:  global
        .offset:         40
        .size:           8
        .value_kind:     global_buffer
      - .actual_access:  write_only
        .address_space:  global
        .offset:         48
        .size:           8
        .value_kind:     global_buffer
    .group_segment_fixed_size: 98816
    .kernarg_segment_align: 8
    .kernarg_segment_size: 56
    .language:       OpenCL C
    .language_version:
      - 2
      - 0
    .max_flat_workgroup_size: 512
    .name:           _Z10k_ka_firstPKfPKiPfS0_S0_PKDF16_PDF16_
    .private_segment_fixed_size: 0
    .sgpr_count:     59
    .sgpr_spill_count: 0
    .symbol:         _Z10k_ka_firstPKfPKiPfS0_S0_PKDF16_PDF16_.kd
    .uniform_work_group_size: 1
    .uses_dynamic_stack: false
    .vgpr_count:     174
    .vgpr_spill_count: 0
    .wavefront_size: 64
  - .agpr_count:     0
    .args:
      - .actual_access:  read_only
        .address_space:  global
        .offset:         0
        .size:           8
        .value_kind:     global_buffer
      - .actual_access:  read_only
        .address_space:  global
        .offset:         8
        .size:           8
        .value_kind:     global_buffer
      - .actual_access:  read_only
        .address_space:  global
        .offset:         16
        .size:           8
        .value_kind:     global_buffer
      - .actual_access:  read_only
        .address_space:  global
        .offset:         24
        .size:           8
        .value_kind:     global_buffer
      - .actual_access:  read_only
        .address_space:  global
        .offset:         32
        .size:           8
        .value_kind:     global_buffer
      - .actual_access:  read_only
        .address_space:  global
        .offset:         40
        .size:           8
        .value_kind:     global_buffer
      - .actual_access:  write_only
        .address_space:  global
        .offset:         48
        .size:           8
        .value_kind:     global_buffer
      - .actual_access:  write_only
        .address_space:  global
        .offset:         56
        .size:           8
        .value_kind:     global_buffer
      - .actual_access:  write_only
        .address_space:  global
        .offset:         64
        .size:           8
        .value_kind:     global_buffer
      - .actual_access:  read_only
        .address_space:  global
        .offset:         72
        .size:           8
        .value_kind:     global_buffer
      - .actual_access:  write_only
        .address_space:  global
        .offset:         80
        .size:           8
        .value_kind:     global_buffer
      - .actual_access:  write_only
        .address_space:  global
        .offset:         88
        .size:           8
        .value_kind:     global_buffer
    .group_segment_fixed_size: 47616
    .kernarg_segment_align: 8
    .kernarg_segment_size: 96
    .language:       OpenCL C
    .language_version:
      - 2
      - 0
    .max_flat_workgroup_size: 512
    .name:           _Z12k_conv_xprojPKDF16_PKfS2_S0_S0_S2_PDF16_S3_PfS2_S3_S4_
    .private_segment_fixed_size: 0
    .sgpr_count:     32
    .sgpr_spill_count: 0
    .symbol:         _Z12k_conv_xprojPKDF16_PKfS2_S0_S0_S2_PDF16_S3_PfS2_S3_S4_.kd
    .uniform_work_group_size: 1
    .uses_dynamic_stack: false
    .vgpr_count:     252
    .vgpr_spill_count: 0
    .wavefront_size: 64
  - .agpr_count:     0
    .args:
      - .actual_access:  read_only
        .address_space:  global
        .offset:         0
        .size:           8
        .value_kind:     global_buffer
      - .actual_access:  read_only
        .address_space:  global
        .offset:         8
        .size:           8
        .value_kind:     global_buffer
      - .actual_access:  read_only
        .address_space:  global
        .offset:         16
        .size:           8
        .value_kind:     global_buffer
      - .actual_access:  write_only
        .address_space:  global
        .offset:         24
        .size:           8
        .value_kind:     global_buffer
    .group_segment_fixed_size: 16384
    .kernarg_segment_align: 8
    .kernarg_segment_size: 32
    .language:       OpenCL C
    .language_version:
      - 2
      - 0
    .max_flat_workgroup_size: 512
    .name:           _Z11k_scan_combPKDF16_PKfS2_PDF16_
    .private_segment_fixed_size: 0
    .sgpr_count:     18
    .sgpr_spill_count: 0
    .symbol:         _Z11k_scan_combPKDF16_PKfS2_PDF16_.kd
    .uniform_work_group_size: 1
    .uses_dynamic_stack: false
    .vgpr_count:     120
    .vgpr_spill_count: 0
    .wavefront_size: 64
  - .agpr_count:     0
    .args:
      - .actual_access:  read_only
        .address_space:  global
        .offset:         0
        .size:           8
        .value_kind:     global_buffer
      - .actual_access:  read_only
        .address_space:  global
        .offset:         8
        .size:           8
        .value_kind:     global_buffer
      - .actual_access:  read_only
        .address_space:  global
        .offset:         16
        .size:           8
        .value_kind:     global_buffer
      - .actual_access:  read_only
        .address_space:  global
        .offset:         24
        .size:           8
        .value_kind:     global_buffer
      - .actual_access:  write_only
        .address_space:  global
        .offset:         32
        .size:           8
        .value_kind:     global_buffer
    .group_segment_fixed_size: 32
    .kernarg_segment_align: 8
    .kernarg_segment_size: 40
    .language:       OpenCL C
    .language_version:
      - 2
      - 0
    .max_flat_workgroup_size: 256
    .name:           _Z6k_headPKfS0_S0_S0_Pf
    .private_segment_fixed_size: 0
    .sgpr_count:     86
    .sgpr_spill_count: 0
    .symbol:         _Z6k_headPKfS0_S0_S0_Pf.kd
    .uniform_work_group_size: 1
    .uses_dynamic_stack: false
    .vgpr_count:     92
    .vgpr_spill_count: 0
    .wavefront_size: 64
  - .agpr_count:     0
    .args:
      - .actual_access:  read_only
        .address_space:  global
        .offset:         0
        .size:           8
        .value_kind:     global_buffer
      - .actual_access:  read_only
        .address_space:  global
        .offset:         8
        .size:           8
        .value_kind:     global_buffer
      - .actual_access:  read_only
        .address_space:  global
        .offset:         16
        .size:           8
        .value_kind:     global_buffer
      - .actual_access:  read_only
        .address_space:  global
        .offset:         24
        .size:           8
        .value_kind:     global_buffer
      - .actual_access:  read_only
        .address_space:  global
        .offset:         32
        .size:           8
        .value_kind:     global_buffer
      - .actual_access:  read_only
        .address_space:  global
        .offset:         40
        .size:           8
        .value_kind:     global_buffer
      - .actual_access:  read_only
        .address_space:  global
        .offset:         48
        .size:           8
        .value_kind:     global_buffer
      - .address_space:  global
        .offset:         56
        .size:           8
        .value_kind:     global_buffer
      - .actual_access:  read_only
        .address_space:  global
        .offset:         64
        .size:           8
        .value_kind:     global_buffer
      - .actual_access:  read_only
        .address_space:  global
        .offset:         72
        .size:           8
        .value_kind:     global_buffer
      - .actual_access:  read_only
        .address_space:  global
        .offset:         80
        .size:           8
        .value_kind:     global_buffer
      - .address_space:  global
        .offset:         88
        .size:           8
        .value_kind:     global_buffer
      - .actual_access:  read_only
        .address_space:  global
        .offset:         96
        .size:           8
        .value_kind:     global_buffer
      - .actual_access:  read_only
        .address_space:  global
        .offset:         104
        .size:           8
        .value_kind:     global_buffer
      - .actual_access:  read_only
        .address_space:  global
        .offset:         112
        .size:           8
        .value_kind:     global_buffer
    .group_segment_fixed_size: 98816
    .kernarg_segment_align: 8
    .kernarg_segment_size: 120
    .language:       OpenCL C
    .language_version:
      - 2
      - 0
    .max_flat_workgroup_size: 512
    .name:           _Z4k_k2ILb0EEvPKDF16_S1_PKfS3_S3_S1_S1_PfS3_S3_S1_PDF16_PKiS4_S4_
    .private_segment_fixed_size: 0
    .sgpr_count:     106
    .sgpr_spill_count: 0
    .symbol:         _Z4k_k2ILb0EEvPKDF16_S1_PKfS3_S3_S1_S1_PfS3_S3_S1_PDF16_PKiS4_S4_.kd
    .uniform_work_group_size: 1
    .uses_dynamic_stack: false
    .vgpr_count:     252
    .vgpr_spill_count: 0
    .wavefront_size: 64
  - .agpr_count:     0
    .args:
      - .actual_access:  read_only
        .address_space:  global
        .offset:         0
        .size:           8
        .value_kind:     global_buffer
      - .actual_access:  read_only
        .address_space:  global
        .offset:         8
        .size:           8
        .value_kind:     global_buffer
      - .actual_access:  read_only
        .address_space:  global
        .offset:         16
        .size:           8
        .value_kind:     global_buffer
      - .actual_access:  read_only
        .address_space:  global
        .offset:         24
        .size:           8
        .value_kind:     global_buffer
      - .actual_access:  read_only
        .address_space:  global
        .offset:         32
        .size:           8
        .value_kind:     global_buffer
      - .actual_access:  read_only
        .address_space:  global
        .offset:         40
        .size:           8
        .value_kind:     global_buffer
      - .actual_access:  read_only
        .address_space:  global
        .offset:         48
        .size:           8
        .value_kind:     global_buffer
      - .actual_access:  read_only
        .address_space:  global
        .offset:         56
        .size:           8
        .value_kind:     global_buffer
      - .actual_access:  read_only
        .address_space:  global
        .offset:         64
        .size:           8
        .value_kind:     global_buffer
      - .actual_access:  read_only
        .address_space:  global
        .offset:         72
        .size:           8
        .value_kind:     global_buffer
      - .actual_access:  read_only
        .address_space:  global
        .offset:         80
        .size:           8
        .value_kind:     global_buffer
      - .actual_access:  read_only
        .address_space:  global
        .offset:         88
        .size:           8
        .value_kind:     global_buffer
      - .actual_access:  read_only
        .address_space:  global
        .offset:         96
        .size:           8
        .value_kind:     global_buffer
      - .actual_access:  write_only
        .address_space:  global
        .offset:         104
        .size:           8
        .value_kind:     global_buffer
      - .actual_access:  write_only
        .address_space:  global
        .offset:         112
        .size:           8
        .value_kind:     global_buffer
    .group_segment_fixed_size: 98816
    .kernarg_segment_align: 8
    .kernarg_segment_size: 120
    .language:       OpenCL C
    .language_version:
      - 2
      - 0
    .max_flat_workgroup_size: 512
    .name:           _Z4k_k2ILb1EEvPKDF16_S1_PKfS3_S3_S1_S1_PfS3_S3_S1_PDF16_PKiS4_S4_
    .private_segment_fixed_size: 0
    .sgpr_count:     44
    .sgpr_spill_count: 0
    .symbol:         _Z4k_k2ILb1EEvPKDF16_S1_PKfS3_S3_S1_S1_PfS3_S3_S1_PDF16_PKiS4_S4_.kd
    .uniform_work_group_size: 1
    .uses_dynamic_stack: false
    .vgpr_count:     196
    .vgpr_spill_count: 0
    .wavefront_size: 64
